# speedup vs baseline: 1.0117x; 1.0021x over previous
.LE_loop16:
	s_sub_u32 s71, s33, 1
	s_add_u32 s61, s33, 1
	s_min_u32 s61, s61, s60
	s_and_b32 s64, s71, 1
	s_lshl_b32 s64, s64, 22
	s_add_u32 s64, s64, s50
	s_add_u32 s64, s64, 0x60000
	s_add_u32 s36, s6, s64
	s_addc_u32 s37, s7, 0
	s_lshl_b32 s64, s71, 3
	s_add_u32 s64, s64, s29
	s_lshl_b32 s64, s64, 5
	s_add_u32 s64, s64, s30
	s_lshl_b32 s64, s64, 2
	s_add_u32 s40, s8, s64
	s_addc_u32 s41, s9, 0
	s_lshl_b32 s64, s33, 11
	s_lshl_b32 s65, s29, 8
	s_add_u32 s64, s64, s65
	s_add_u32 s64, s64, 128
	s_lshl_b32 s64, s64, 3
	s_add_u32 s42, s12, s64
	s_addc_u32 s43, s13, 0
	s_nop 3
	global_load_dwordx2 v[228:229], v249, s[42:43] offset:0
	global_load_dwordx2 v[230:231], v249, s[42:43] offset:256
	s_waitcnt lgkmcnt(4)
	v_mfma_f32_32x32x16_f16 v[0:15], a[0:3], v[160:163], v[0:15]
	ds_read_b128 v[160:163], v192 offset:8192
	v_exp_f32_e32 v200, v96
	v_mfma_f32_32x32x16_f16 v[16:31], a[0:3], v[164:167], v[16:31]
	ds_read_b128 v[164:167], v192 offset:9216
	s_lshl_b32 s64, s71, 3
	s_add_u32 s64, s64, s29
	s_lshl_b32 s64, s64, 7
	s_add_u32 s38, s8, s64
	s_addc_u32 s39, s9, 0
	global_load_dword v251, v196, s[38:39] sc1
	v_exp_f32_e32 v201, v97
	v_add_f32_e32 v200, 1.0, v200
	v_mfma_f32_32x32x16_f16 v[0:15], a[4:7], v[168:171], v[0:15]
	ds_read_b128 v[168:171], v192 offset:10240
	v_exp_f32_e32 v202, v98
	v_add_f32_e32 v201, 1.0, v201
	v_mfma_f32_32x32x16_f16 v[16:31], a[4:7], v[172:175], v[16:31]
	ds_read_b128 v[172:175], v192 offset:11264
	global_load_lds_dwordx4 v192, s[44:45] offset:1024 sc1
	v_exp_f32_e32 v203, v99
	v_add_f32_e32 v202, 1.0, v202
	s_waitcnt lgkmcnt(4)
	v_mfma_f32_32x32x16_f16 v[0:15], a[8:11], v[176:179], v[0:15]
	ds_read_b128 v[176:179], v192 offset:12288
	v_exp_f32_e32 v204, v100
	v_add_f32_e32 v203, 1.0, v203
	v_mfma_f32_32x32x16_f16 v[16:31], a[8:11], v[180:183], v[16:31]
	ds_read_b128 v[180:183], v192 offset:13312
	v_exp_f32_e32 v205, v101
	v_add_f32_e32 v204, 1.0, v204
	v_mfma_f32_32x32x16_f16 v[0:15], a[12:15], v[184:187], v[0:15]
	ds_read_b128 v[184:187], v192 offset:14336
	v_exp_f32_e32 v206, v102
	v_add_f32_e32 v205, 1.0, v205
	v_mfma_f32_32x32x16_f16 v[16:31], a[12:15], v[188:191], v[16:31]
	ds_read_b128 v[188:191], v192 offset:15360
	global_load_lds_dwordx4 v192, s[44:45] offset:2048 sc1
	v_exp_f32_e32 v207, v103
	v_add_f32_e32 v206, 1.0, v206
	s_waitcnt lgkmcnt(4)
	v_mfma_f32_32x32x16_f16 v[0:15], a[16:19], v[160:163], v[0:15]
	ds_read_b128 v[160:163], v192 offset:16384
	v_exp_f32_e32 v208, v104
	v_add_f32_e32 v207, 1.0, v207
	v_mfma_f32_32x32x16_f16 v[16:31], a[16:19], v[164:167], v[16:31]
	ds_read_b128 v[164:167], v192 offset:17408
	v_exp_f32_e32 v209, v105
	v_add_f32_e32 v208, 1.0, v208
	v_mfma_f32_32x32x16_f16 v[0:15], a[20:23], v[168:171], v[0:15]
	ds_read_b128 v[168:171], v192 offset:18432
	v_exp_f32_e32 v210, v106
	v_add_f32_e32 v209, 1.0, v209
	v_mfma_f32_32x32x16_f16 v[16:31], a[20:23], v[172:175], v[16:31]
	ds_read_b128 v[172:175], v192 offset:19456
	global_load_lds_dwordx4 v192, s[44:45] offset:3072 sc1
	v_exp_f32_e32 v211, v107
	v_add_f32_e32 v210, 1.0, v210
	s_waitcnt lgkmcnt(4)
	v_mfma_f32_32x32x16_f16 v[0:15], a[24:27], v[176:179], v[0:15]
	ds_read_b128 v[176:179], v192 offset:20480
	v_exp_f32_e32 v212, v108
	v_add_f32_e32 v211, 1.0, v211
	v_mfma_f32_32x32x16_f16 v[16:31], a[24:27], v[180:183], v[16:31]
	ds_read_b128 v[180:183], v192 offset:21504
	v_exp_f32_e32 v213, v109
	v_add_f32_e32 v212, 1.0, v212
	v_mfma_f32_32x32x16_f16 v[0:15], a[28:31], v[184:187], v[0:15]
	ds_read_b128 v[184:187], v192 offset:22528
	v_exp_f32_e32 v214, v110
	v_add_f32_e32 v213, 1.0, v213
	v_mfma_f32_32x32x16_f16 v[16:31], a[28:31], v[188:191], v[16:31]
	ds_read_b128 v[188:191], v192 offset:23552
	s_add_u32 s44, s34, 0x11000
	s_addc_u32 s45, s35, 0
	s_mov_b32 m0, s57
	s_nop 0
	global_load_lds_dwordx4 v192, s[44:45] sc1
	v_exp_f32_e32 v215, v111
	v_add_f32_e32 v214, 1.0, v214
	s_waitcnt lgkmcnt(4)
	v_mfma_f32_32x32x16_f16 v[0:15], a[32:35], v[160:163], v[0:15]
	ds_read_b128 v[160:163], v192 offset:24576
	v_add_f32_e32 v215, 1.0, v215
	v_rcp_f32_e32 v200, v200
	v_mfma_f32_32x32x16_f16 v[16:31], a[32:35], v[164:167], v[16:31]
	ds_read_b128 v[164:167], v192 offset:25600
	v_rcp_f32_e32 v201, v201
	v_mfma_f32_32x32x16_f16 v[0:15], a[36:39], v[168:171], v[0:15]
	ds_read_b128 v[168:171], v192 offset:26624
	v_rcp_f32_e32 v202, v202
	v_mfma_f32_32x32x16_f16 v[16:31], a[36:39], v[172:175], v[16:31]
	ds_read_b128 v[172:175], v192 offset:27648
	global_load_lds_dwordx4 v192, s[44:45] offset:1024 sc1
	v_rcp_f32_e32 v203, v203
	s_waitcnt lgkmcnt(4)
	v_mfma_f32_32x32x16_f16 v[0:15], a[40:43], v[176:179], v[0:15]
	ds_read_b128 v[176:179], v192 offset:28672
	v_rcp_f32_e32 v204, v204
	v_mfma_f32_32x32x16_f16 v[16:31], a[40:43], v[180:183], v[16:31]
	ds_read_b128 v[180:183], v192 offset:29696
	v_rcp_f32_e32 v205, v205
	v_mul_f32_e32 v204, v204, v152
	v_mfma_f32_32x32x16_f16 v[0:15], a[44:47], v[184:187], v[0:15]
	ds_read_b128 v[184:187], v192 offset:30720
	v_rcp_f32_e32 v206, v206
	v_mul_f32_e32 v205, v205, v153
	v_mfma_f32_32x32x16_f16 v[16:31], a[44:47], v[188:191], v[16:31]
	ds_read_b128 v[188:191], v192 offset:31744
	global_load_lds_dwordx4 v192, s[44:45] offset:2048 sc1
	v_rcp_f32_e32 v207, v207
	v_mul_f32_e32 v206, v206, v154
	s_waitcnt vmcnt(10)
	s_barrier
	s_waitcnt lgkmcnt(4)
	v_mfma_f32_32x32x16_f16 v[0:15], a[48:51], v[160:163], v[0:15]
	ds_read_b128 v[160:163], v192 offset:32768
	v_rcp_f32_e32 v208, v208
	v_mul_f32_e32 v207, v207, v155
	v_mfma_f32_32x32x16_f16 v[16:31], a[48:51], v[164:167], v[16:31]
	ds_read_b128 v[164:167], v192 offset:33792
	v_rcp_f32_e32 v209, v209
	v_fmamk_f32 v208, v208, 0xc0b8aa3b, v198
	v_mfma_f32_32x32x16_f16 v[0:15], a[52:55], v[168:171], v[0:15]
	ds_read_b128 v[168:171], v192 offset:34816
	v_rcp_f32_e32 v210, v210
	v_fmamk_f32 v209, v209, 0xc0b8aa3b, v198
	v_fma_f32 v152, v200, v208, v204
	v_mfma_f32_32x32x16_f16 v[16:31], a[52:55], v[172:175], v[16:31]
	ds_read_b128 v[172:175], v192 offset:35840
	global_load_lds_dwordx4 v192, s[44:45] offset:3072 sc1
	v_rcp_f32_e32 v211, v211
	v_fmamk_f32 v210, v210, 0xc0b8aa3b, v198
	v_fma_f32 v153, v201, v209, v205
	s_waitcnt lgkmcnt(4)
	v_mfma_f32_32x32x16_f16 v[0:15], a[56:59], v[176:179], v[0:15]
	ds_read_b128 v[176:179], v192 offset:36864
	v_rcp_f32_e32 v212, v212
	v_fmamk_f32 v211, v211, 0xc0b8aa3b, v198
	v_fma_f32 v154, v202, v210, v206
	v_mfma_f32_32x32x16_f16 v[16:31], a[56:59], v[180:183], v[16:31]
	ds_read_b128 v[180:183], v192 offset:37888
	v_rcp_f32_e32 v213, v213
	v_fma_f32 v155, v203, v211, v207
	v_mfma_f32_32x32x16_f16 v[0:15], a[60:63], v[184:187], v[0:15]
	ds_read_b128 v[184:187], v192 offset:38912
	v_rcp_f32_e32 v214, v214
	v_mfma_f32_32x32x16_f16 v[16:31], a[60:63], v[188:191], v[16:31]
	ds_read_b128 v[188:191], v192 offset:39936
	s_add_u32 s44, s34, 0x18000
	s_addc_u32 s45, s35, 0
	s_mov_b32 m0, s58
	s_nop 0
	global_load_lds_dwordx4 v192, s[44:45] sc1
	v_rcp_f32_e32 v215, v215
	s_waitcnt lgkmcnt(4)
	v_mfma_f32_32x32x16_f16 v[0:15], a[64:67], v[160:163], v[0:15]
	ds_read_b128 v[160:163], v192 offset:40960
	v_exp_f32_e32 v200, v152
	v_mfma_f32_32x32x16_f16 v[16:31], a[64:67], v[164:167], v[16:31]
	ds_read_b128 v[164:167], v192 offset:41984
	v_exp_f32_e32 v201, v153
	v_add_f32_e32 v200, 1.0, v200
	v_mfma_f32_32x32x16_f16 v[0:15], a[68:71], v[168:171], v[0:15]
	ds_read_b128 v[168:171], v192 offset:43008
	v_exp_f32_e32 v202, v154
	v_add_f32_e32 v201, 1.0, v201
	v_mfma_f32_32x32x16_f16 v[16:31], a[68:71], v[172:175], v[16:31]
	ds_read_b128 v[172:175], v192 offset:44032
	global_load_lds_dwordx4 v192, s[44:45] offset:1024 sc1
	v_exp_f32_e32 v203, v155
	v_add_f32_e32 v202, 1.0, v202
	s_waitcnt lgkmcnt(4)
	v_mfma_f32_32x32x16_f16 v[0:15], a[72:75], v[176:179], v[0:15]
	ds_read_b128 v[176:179], v192 offset:45056
	v_add_f32_e32 v203, 1.0, v203
	v_rcp_f32_e32 v200, v200
	v_mfma_f32_32x32x16_f16 v[16:31], a[72:75], v[180:183], v[16:31]
	ds_read_b128 v[180:183], v192 offset:46080
	v_rcp_f32_e32 v201, v201
	v_fma_f32 v200, v200, 2.0, -1.0
	v_mfma_f32_32x32x16_f16 v[0:15], a[76:79], v[184:187], v[0:15]
	ds_read_b128 v[184:187], v192 offset:47104
	v_rcp_f32_e32 v202, v202
	v_fma_f32 v201, v201, 2.0, -1.0
	v_mul_f32_e32 v216, v212, v200
	v_mfma_f32_32x32x16_f16 v[16:31], a[76:79], v[188:191], v[16:31]
	ds_read_b128 v[188:191], v192 offset:48128
	global_load_lds_dwordx4 v192, s[44:45] offset:2048 sc1
	v_rcp_f32_e32 v203, v203
	v_fma_f32 v202, v202, 2.0, -1.0
	v_mul_f32_e32 v217, v213, v201
	s_waitcnt lgkmcnt(4)
	v_mfma_f32_32x32x16_f16 v[0:15], a[80:83], v[160:163], v[0:15]
	ds_read_b128 v[160:163], v192 offset:49152
	v_fma_f32 v203, v203, 2.0, -1.0
	v_mul_f32_e32 v218, v214, v202
	v_exp_f32_e32 v200, v112
	v_mfma_f32_32x32x16_f16 v[16:31], a[80:83], v[164:167], v[16:31]
	ds_read_b128 v[164:167], v192 offset:50176
	v_mul_f32_e32 v219, v215, v203
	v_cvt_pk_f16_f32 v220, v216, v217
	v_exp_f32_e32 v201, v113
	v_mfma_f32_32x32x16_f16 v[0:15], a[84:87], v[168:171], v[0:15]
	ds_read_b128 v[168:171], v192 offset:51200
	v_cvt_pk_f16_f32 v221, v218, v219
	v_exp_f32_e32 v202, v114
	v_add_f32_e32 v200, 1.0, v200
	v_mfma_f32_32x32x16_f16 v[16:31], a[84:87], v[172:175], v[16:31]
	ds_read_b128 v[172:175], v192 offset:52224
	global_load_lds_dwordx4 v192, s[44:45] offset:3072 sc1
	v_exp_f32_e32 v203, v115
	v_add_f32_e32 v201, 1.0, v201
	v_add_f32_e32 v202, 1.0, v202
	s_waitcnt lgkmcnt(4)
	v_mfma_f32_32x32x16_f16 v[0:15], a[88:91], v[176:179], v[0:15]
	ds_read_b128 v[176:179], v192 offset:53248
	v_exp_f32_e32 v204, v116
	v_add_f32_e32 v203, 1.0, v203
	v_mfma_f32_32x32x16_f16 v[16:31], a[88:91], v[180:183], v[16:31]
	ds_read_b128 v[180:183], v192 offset:54272
	v_exp_f32_e32 v205, v117
	v_add_f32_e32 v204, 1.0, v204
	v_mfma_f32_32x32x16_f16 v[0:15], a[92:95], v[184:187], v[0:15]
	ds_read_b128 v[184:187], v192 offset:55296
	v_exp_f32_e32 v206, v118
	v_add_f32_e32 v205, 1.0, v205
	v_mfma_f32_32x32x16_f16 v[16:31], a[92:95], v[188:191], v[16:31]
	ds_read_b128 v[188:191], v192 offset:56320
	s_add_u32 s44, s34, 0x19000
	s_addc_u32 s45, s35, 0
	s_mov_b32 m0, s59
	s_nop 0
	global_load_lds_dwordx4 v192, s[44:45] sc1
	v_exp_f32_e32 v207, v119
	v_add_f32_e32 v206, 1.0, v206
	s_waitcnt lgkmcnt(4)
	v_mfma_f32_32x32x16_f16 v[0:15], a[96:99], v[160:163], v[0:15]
	ds_read_b128 v[160:163], v192 offset:57344
	v_exp_f32_e32 v208, v120
	v_add_f32_e32 v207, 1.0, v207
	v_mfma_f32_32x32x16_f16 v[16:31], a[96:99], v[164:167], v[16:31]
	ds_read_b128 v[164:167], v192 offset:58368
	v_exp_f32_e32 v209, v121
	v_add_f32_e32 v208, 1.0, v208
	v_mfma_f32_32x32x16_f16 v[0:15], a[100:103], v[168:171], v[0:15]
	ds_read_b128 v[168:171], v192 offset:59392
	v_exp_f32_e32 v210, v122
	v_add_f32_e32 v209, 1.0, v209
	v_mfma_f32_32x32x16_f16 v[16:31], a[100:103], v[172:175], v[16:31]
	ds_read_b128 v[172:175], v192 offset:60416
	global_load_lds_dwordx4 v192, s[44:45] offset:1024 sc1
	v_exp_f32_e32 v211, v123
	v_add_f32_e32 v210, 1.0, v210
	s_waitcnt lgkmcnt(4)
	v_mfma_f32_32x32x16_f16 v[0:15], a[104:107], v[176:179], v[0:15]
	ds_read_b128 v[176:179], v192 offset:61440
	v_exp_f32_e32 v212, v124
	v_add_f32_e32 v211, 1.0, v211
	v_mfma_f32_32x32x16_f16 v[16:31], a[104:107], v[180:183], v[16:31]
	ds_read_b128 v[180:183], v192 offset:62464
	v_exp_f32_e32 v213, v125
	v_add_f32_e32 v212, 1.0, v212
	v_mfma_f32_32x32x16_f16 v[0:15], a[108:111], v[184:187], v[0:15]
	ds_read_b128 v[184:187], v192 offset:63488
	v_exp_f32_e32 v214, v126
	v_add_f32_e32 v213, 1.0, v213
	v_mfma_f32_32x32x16_f16 v[16:31], a[108:111], v[188:191], v[16:31]
	ds_read_b128 v[188:191], v192 offset:64512
	global_load_lds_dwordx4 v192, s[44:45] offset:2048 sc1
	v_exp_f32_e32 v215, v127
	v_add_f32_e32 v214, 1.0, v214
	s_waitcnt vmcnt(7)
	s_barrier
	s_waitcnt lgkmcnt(4)
	v_mfma_f32_32x32x16_f16 v[0:15], a[112:115], v[160:163], v[0:15]
	ds_read_b128 v[160:163], v193 offset:0
	v_add_f32_e32 v215, 1.0, v215
	v_rcp_f32_e32 v200, v200
	v_mfma_f32_32x32x16_f16 v[16:31], a[112:115], v[164:167], v[16:31]
	ds_read_b128 v[164:167], v193 offset:1024
	v_rcp_f32_e32 v201, v201
	v_mfma_f32_32x32x16_f16 v[0:15], a[116:119], v[168:171], v[0:15]
	ds_read_b128 v[168:171], v193 offset:2048
	v_rcp_f32_e32 v202, v202
	v_mfma_f32_32x32x16_f16 v[16:31], a[116:119], v[172:175], v[16:31]
	ds_read_b128 v[172:175], v193 offset:3072
	global_load_lds_dwordx4 v192, s[44:45] offset:3072 sc1
	v_rcp_f32_e32 v203, v203
	s_waitcnt lgkmcnt(4)
	v_mfma_f32_32x32x16_f16 v[0:15], a[120:123], v[176:179], v[0:15]
	ds_read_b128 v[176:179], v193 offset:4096
	v_rcp_f32_e32 v204, v204
	ds_read_b128 v[236:239], v248 offset:0
	ds_read_b64 v[240:241], v248 offset:32
	ds_read_b128 v[242:245], v248 offset:16
	ds_read_b64 v[246:247], v248 offset:40
	v_mfma_f32_32x32x16_f16 v[16:31], a[120:123], v[180:183], v[16:31]
	ds_read_b128 v[180:183], v193 offset:5120
	v_rcp_f32_e32 v205, v205
	v_mul_f32_e32 v204, v204, v156
	s_waitcnt lgkmcnt(3)
	v_fma_f32 v64, v229, v237, v240
	v_mfma_f32_32x32x16_f16 v[0:15], a[124:127], v[184:187], v[0:15]
	ds_read_b128 v[184:187], v193 offset:6144
	v_rcp_f32_e32 v206, v206
	v_mul_f32_e32 v205, v205, v157
	v_fma_f32 v65, v229, v239, v241
	v_fmac_f32_e32 v64, v228, v236
	v_mfma_f32_32x32x16_f16 v[16:31], a[124:127], v[188:191], v[16:31]
	ds_read_b128 v[188:191], v193 offset:7168
	v_cmp_gt_u32_e32 vcc, 2, v251
	s_cbranch_vccz .LE_tok20

.LE_join25:
	v_mfma_f32_32x32x16_f16 v[16:31], a[192:195], v[164:167], v[16:31]
	ds_read_b128 v[164:167], v193 offset:41984
	v_fmac_f32_e32 v78, v228, v242
	v_fmac_f32_e32 v79, v228, v244
	v_mfma_f32_32x32x16_f16 v[0:15], a[196:199], v[168:171], v[0:15]
	ds_read_b128 v[168:171], v193 offset:43008
	v_fma_f32 v94, v231, v243, v246
	v_fma_f32 v95, v231, v245, v247
	v_mfma_f32_32x32x16_f16 v[16:31], a[196:199], v[172:175], v[16:31]
	ds_read_b128 v[172:175], v193 offset:44032
	global_load_lds_dwordx4 v192, s[44:45] offset:1024 sc1
	v_fmac_f32_e32 v94, v230, v242
	v_fmac_f32_e32 v95, v230, v244
	s_waitcnt lgkmcnt(4)
	v_mfma_f32_32x32x16_f16 v[0:15], a[200:203], v[176:179], v[0:15]
	ds_read_b128 v[176:179], v193 offset:45056
	v_mfma_f32_32x32x16_f16 v[16:31], a[200:203], v[180:183], v[16:31]
	ds_read_b128 v[180:183], v193 offset:46080
	v_mfma_f32_32x32x16_f16 v[0:15], a[204:207], v[184:187], v[0:15]
	ds_read_b128 v[184:187], v193 offset:47104
	v_mfma_f32_32x32x16_f16 v[16:31], a[204:207], v[188:191], v[16:31]
	ds_read_b128 v[188:191], v193 offset:48128
	global_load_lds_dwordx4 v192, s[44:45] offset:2048 sc1
	s_waitcnt lgkmcnt(4)
	v_mfma_f32_32x32x16_f16 v[0:15], a[208:211], v[160:163], v[0:15]
	ds_read_b128 v[160:163], v193 offset:49152
	v_mfma_f32_32x32x16_f16 v[16:31], a[208:211], v[164:167], v[16:31]
	ds_read_b128 v[164:167], v193 offset:50176
	v_mfma_f32_32x32x16_f16 v[0:15], a[212:215], v[168:171], v[0:15]
	ds_read_b128 v[168:171], v193 offset:51200
	v_mfma_f32_32x32x16_f16 v[16:31], a[212:215], v[172:175], v[16:31]
	ds_read_b128 v[172:175], v193 offset:52224
	global_load_lds_dwordx4 v192, s[44:45] offset:3072 sc1
	s_waitcnt lgkmcnt(4)
	v_mfma_f32_32x32x16_f16 v[0:15], a[216:219], v[176:179], v[0:15]
	ds_read_b128 v[176:179], v193 offset:53248
	v_mfma_f32_32x32x16_f16 v[16:31], a[216:219], v[180:183], v[16:31]
	ds_read_b128 v[180:183], v193 offset:54272
	v_mfma_f32_32x32x16_f16 v[0:15], a[220:223], v[184:187], v[0:15]
	ds_read_b128 v[184:187], v193 offset:55296
	v_mfma_f32_32x32x16_f16 v[16:31], a[220:223], v[188:191], v[16:31]
	ds_read_b128 v[188:191], v193 offset:56320
	s_add_u32 s44, s34, 0x9000
	s_addc_u32 s45, s35, 0
	s_mov_b32 m0, s55
	s_nop 0
	global_load_lds_dwordx4 v192, s[44:45] sc1
	s_waitcnt lgkmcnt(4)
	v_mfma_f32_32x32x16_f16 v[0:15], a[224:227], v[160:163], v[0:15]
	ds_read_b128 v[160:163], v193 offset:57344
	v_mfma_f32_32x32x16_f16 v[16:31], a[224:227], v[164:167], v[16:31]
	ds_read_b128 v[164:167], v193 offset:58368
	v_mfma_f32_32x32x16_f16 v[0:15], a[228:231], v[168:171], v[0:15]
	ds_read_b128 v[168:171], v193 offset:59392
	v_mfma_f32_32x32x16_f16 v[16:31], a[228:231], v[172:175], v[16:31]
	ds_read_b128 v[172:175], v193 offset:60416
	global_load_lds_dwordx4 v192, s[44:45] offset:1024 sc1
	s_waitcnt lgkmcnt(4)
	v_mfma_f32_32x32x16_f16 v[0:15], a[232:235], v[176:179], v[0:15]
	ds_read_b128 v[176:179], v193 offset:61440
	v_mfma_f32_32x32x16_f16 v[16:31], a[232:235], v[180:183], v[16:31]
	ds_read_b128 v[180:183], v193 offset:62464
	v_mfma_f32_32x32x16_f16 v[0:15], a[236:239], v[184:187], v[0:15]
	ds_read_b128 v[184:187], v193 offset:63488
	v_mfma_f32_32x32x16_f16 v[16:31], a[236:239], v[188:191], v[16:31]
	ds_read_b128 v[188:191], v193 offset:64512
	global_load_lds_dwordx4 v192, s[44:45] offset:2048 sc1
	s_waitcnt vmcnt(8)
	s_barrier
	s_waitcnt lgkmcnt(4)
	v_mfma_f32_32x32x16_f16 v[0:15], a[240:243], v[160:163], v[0:15]
	ds_read_b128 v[160:163], v192 offset:0
	v_mfma_f32_32x32x16_f16 v[16:31], a[240:243], v[164:167], v[16:31]
	ds_read_b128 v[164:167], v192 offset:1024
	v_mfma_f32_32x32x16_f16 v[0:15], a[244:247], v[168:171], v[0:15]
	ds_read_b128 v[168:171], v192 offset:2048
	v_mfma_f32_32x32x16_f16 v[16:31], a[244:247], v[172:175], v[16:31]
	ds_read_b128 v[172:175], v192 offset:3072
	global_load_lds_dwordx4 v192, s[44:45] offset:3072 sc1
	s_waitcnt lgkmcnt(4)
	v_mfma_f32_32x32x16_f16 v[0:15], a[248:251], v[176:179], v[0:15]
	ds_read_b128 v[176:179], v192 offset:4096
	v_mfma_f32_32x32x16_f16 v[16:31], a[248:251], v[180:183], v[16:31]
	ds_read_b128 v[180:183], v192 offset:5120
	v_mfma_f32_32x32x16_f16 v[0:15], a[252:255], v[184:187], v[0:15]
	ds_read_b128 v[184:187], v192 offset:6144
	v_mfma_f32_32x32x16_f16 v[16:31], a[252:255], v[188:191], v[16:31]
	ds_read_b128 v[188:191], v192 offset:7168
	s_add_u32 s44, s34, 0x10000
	s_addc_u32 s45, s35, 0
	s_mov_b32 m0, s56
	s_nop 0
	global_load_lds_dwordx4 v192, s[44:45] sc1
	s_and_b32 s64, s33, 1
	s_lshl_b32 s64, s64, 22
	s_add_u32 s64, s64, s50
	s_add_u32 s36, s6, s64
	s_addc_u32 s37, s7, 0
	s_lshl_b32 s64, s33, 3
	s_add_u32 s64, s64, s29
	s_lshl_b32 s64, s64, 5
	s_add_u32 s64, s64, s30
	s_lshl_b32 s64, s64, 2
	s_add_u32 s40, s8, s64
	s_addc_u32 s41, s9, 0
	s_lshl_b32 s64, s33, 11
	s_lshl_b32 s65, s29, 8
	s_add_u32 s64, s64, s65
	s_add_u32 s64, s64, 192
	s_lshl_b32 s64, s64, 3
	s_add_u32 s42, s12, s64
	s_addc_u32 s43, s13, 0
	s_nop 3
	global_load_dwordx2 v[228:229], v249, s[42:43] offset:0
	global_load_dwordx2 v[230:231], v249, s[42:43] offset:256
	s_waitcnt lgkmcnt(4)
	v_mfma_f32_32x32x16_f16 v[32:47], a[0:3], v[160:163], v[32:47]
	ds_read_b128 v[160:163], v192 offset:8192
	v_exp_f32_e32 v200, v0
	v_mfma_f32_32x32x16_f16 v[48:63], a[0:3], v[164:167], v[48:63]
	ds_read_b128 v[164:167], v192 offset:9216
	s_lshl_b32 s64, s71, 3
	s_add_u32 s64, s64, s29
	s_lshl_b32 s64, s64, 7
	s_add_u32 s38, s8, s64
	s_addc_u32 s39, s9, 0
	global_load_dword v251, v196, s[38:39] sc1
	v_exp_f32_e32 v201, v1
	v_add_f32_e32 v200, 1.0, v200
	v_mfma_f32_32x32x16_f16 v[32:47], a[4:7], v[168:171], v[32:47]
	ds_read_b128 v[168:171], v192 offset:10240
	v_exp_f32_e32 v202, v2
	v_add_f32_e32 v201, 1.0, v201
	v_mfma_f32_32x32x16_f16 v[48:63], a[4:7], v[172:175], v[48:63]
	ds_read_b128 v[172:175], v192 offset:11264
	global_load_lds_dwordx4 v192, s[44:45] offset:1024 sc1
	v_exp_f32_e32 v203, v3
	v_add_f32_e32 v202, 1.0, v202
	s_waitcnt lgkmcnt(4)
	v_mfma_f32_32x32x16_f16 v[32:47], a[8:11], v[176:179], v[32:47]
	ds_read_b128 v[176:179], v192 offset:12288
	v_exp_f32_e32 v204, v4
	v_add_f32_e32 v203, 1.0, v203
	v_mfma_f32_32x32x16_f16 v[48:63], a[8:11], v[180:183], v[48:63]
	ds_read_b128 v[180:183], v192 offset:13312
	v_exp_f32_e32 v205, v5
	v_add_f32_e32 v204, 1.0, v204
	v_mfma_f32_32x32x16_f16 v[32:47], a[12:15], v[184:187], v[32:47]
	ds_read_b128 v[184:187], v192 offset:14336
	v_exp_f32_e32 v206, v6
	v_add_f32_e32 v205, 1.0, v205
	v_mfma_f32_32x32x16_f16 v[48:63], a[12:15], v[188:191], v[48:63]
	ds_read_b128 v[188:191], v192 offset:15360
	global_load_lds_dwordx4 v192, s[44:45] offset:2048 sc1
	v_exp_f32_e32 v207, v7
	v_add_f32_e32 v206, 1.0, v206
	s_waitcnt lgkmcnt(4)
	v_mfma_f32_32x32x16_f16 v[32:47], a[16:19], v[160:163], v[32:47]
	ds_read_b128 v[160:163], v192 offset:16384
	v_exp_f32_e32 v208, v8
	v_add_f32_e32 v207, 1.0, v207
	v_mfma_f32_32x32x16_f16 v[48:63], a[16:19], v[164:167], v[48:63]
	ds_read_b128 v[164:167], v192 offset:17408
	v_exp_f32_e32 v209, v9
	v_add_f32_e32 v208, 1.0, v208
	v_mfma_f32_32x32x16_f16 v[32:47], a[20:23], v[168:171], v[32:47]
	ds_read_b128 v[168:171], v192 offset:18432
	v_exp_f32_e32 v210, v10
	v_add_f32_e32 v209, 1.0, v209
	v_mfma_f32_32x32x16_f16 v[48:63], a[20:23], v[172:175], v[48:63]
	ds_read_b128 v[172:175], v192 offset:19456
	global_load_lds_dwordx4 v192, s[44:45] offset:3072 sc1
	v_exp_f32_e32 v211, v11
	v_add_f32_e32 v210, 1.0, v210
	s_waitcnt lgkmcnt(4)
	v_mfma_f32_32x32x16_f16 v[32:47], a[24:27], v[176:179], v[32:47]
	ds_read_b128 v[176:179], v192 offset:20480
	v_exp_f32_e32 v212, v12
	v_add_f32_e32 v211, 1.0, v211
	v_mfma_f32_32x32x16_f16 v[48:63], a[24:27], v[180:183], v[48:63]
	ds_read_b128 v[180:183], v192 offset:21504
	v_exp_f32_e32 v213, v13
	v_add_f32_e32 v212, 1.0, v212
	v_mfma_f32_32x32x16_f16 v[32:47], a[28:31], v[184:187], v[32:47]
	ds_read_b128 v[184:187], v192 offset:22528
	v_exp_f32_e32 v214, v14
	v_add_f32_e32 v213, 1.0, v213
	v_mfma_f32_32x32x16_f16 v[48:63], a[28:31], v[188:191], v[48:63]
	ds_read_b128 v[188:191], v192 offset:23552
	s_add_u32 s44, s34, 0x11000
	s_addc_u32 s45, s35, 0
	s_mov_b32 m0, s57
	s_nop 0
	global_load_lds_dwordx4 v192, s[44:45] sc1
	v_exp_f32_e32 v215, v15
	v_add_f32_e32 v214, 1.0, v214
	s_waitcnt lgkmcnt(4)
	v_mfma_f32_32x32x16_f16 v[32:47], a[32:35], v[160:163], v[32:47]
	ds_read_b128 v[160:163], v192 offset:24576
	v_add_f32_e32 v215, 1.0, v215
	v_rcp_f32_e32 v200, v200
	v_mfma_f32_32x32x16_f16 v[48:63], a[32:35], v[164:167], v[48:63]
	ds_read_b128 v[164:167], v192 offset:25600
	v_rcp_f32_e32 v201, v201
	v_mfma_f32_32x32x16_f16 v[32:47], a[36:39], v[168:171], v[32:47]
	ds_read_b128 v[168:171], v192 offset:26624
	v_rcp_f32_e32 v202, v202
	v_mfma_f32_32x32x16_f16 v[48:63], a[36:39], v[172:175], v[48:63]
	ds_read_b128 v[172:175], v192 offset:27648
	global_load_lds_dwordx4 v192, s[44:45] offset:1024 sc1
	v_rcp_f32_e32 v203, v203
	s_waitcnt lgkmcnt(4)
	v_mfma_f32_32x32x16_f16 v[32:47], a[40:43], v[176:179], v[32:47]
	ds_read_b128 v[176:179], v192 offset:28672
	v_rcp_f32_e32 v204, v204
	v_mfma_f32_32x32x16_f16 v[48:63], a[40:43], v[180:183], v[48:63]
	ds_read_b128 v[180:183], v192 offset:29696
	v_rcp_f32_e32 v205, v205
	v_mul_f32_e32 v204, v204, v128
	v_mfma_f32_32x32x16_f16 v[32:47], a[44:47], v[184:187], v[32:47]
	ds_read_b128 v[184:187], v192 offset:30720
	v_rcp_f32_e32 v206, v206
	v_mul_f32_e32 v205, v205, v129
	v_mfma_f32_32x32x16_f16 v[48:63], a[44:47], v[188:191], v[48:63]
	ds_read_b128 v[188:191], v192 offset:31744
	global_load_lds_dwordx4 v192, s[44:45] offset:2048 sc1
	v_rcp_f32_e32 v207, v207
	v_mul_f32_e32 v206, v206, v130
	s_waitcnt vmcnt(10)
	s_barrier
	s_waitcnt lgkmcnt(4)
	v_mfma_f32_32x32x16_f16 v[32:47], a[48:51], v[160:163], v[32:47]
	ds_read_b128 v[160:163], v192 offset:32768
	v_rcp_f32_e32 v208, v208
	v_mul_f32_e32 v207, v207, v131
	v_mfma_f32_32x32x16_f16 v[48:63], a[48:51], v[164:167], v[48:63]
	ds_read_b128 v[164:167], v192 offset:33792
	v_rcp_f32_e32 v209, v209
	v_fmamk_f32 v208, v208, 0xc0b8aa3b, v198
	v_mfma_f32_32x32x16_f16 v[32:47], a[52:55], v[168:171], v[32:47]
	ds_read_b128 v[168:171], v192 offset:34816
	v_rcp_f32_e32 v210, v210
	v_fmamk_f32 v209, v209, 0xc0b8aa3b, v198
	v_fma_f32 v128, v200, v208, v204
	v_mfma_f32_32x32x16_f16 v[48:63], a[52:55], v[172:175], v[48:63]
	ds_read_b128 v[172:175], v192 offset:35840
	global_load_lds_dwordx4 v192, s[44:45] offset:3072 sc1
	v_rcp_f32_e32 v211, v211
	v_fmamk_f32 v210, v210, 0xc0b8aa3b, v198
	v_fma_f32 v129, v201, v209, v205
	s_waitcnt lgkmcnt(4)
	v_mfma_f32_32x32x16_f16 v[32:47], a[56:59], v[176:179], v[32:47]
	ds_read_b128 v[176:179], v192 offset:36864
	v_rcp_f32_e32 v212, v212
	v_fmamk_f32 v211, v211, 0xc0b8aa3b, v198
	v_fma_f32 v130, v202, v210, v206
	v_mfma_f32_32x32x16_f16 v[48:63], a[56:59], v[180:183], v[48:63]
	ds_read_b128 v[180:183], v192 offset:37888
	v_rcp_f32_e32 v213, v213
	v_fma_f32 v131, v203, v211, v207
	v_mfma_f32_32x32x16_f16 v[32:47], a[60:63], v[184:187], v[32:47]
	ds_read_b128 v[184:187], v192 offset:38912
	v_rcp_f32_e32 v214, v214
	v_mfma_f32_32x32x16_f16 v[48:63], a[60:63], v[188:191], v[48:63]
	ds_read_b128 v[188:191], v192 offset:39936
	s_add_u32 s44, s34, 0x18000
	s_addc_u32 s45, s35, 0
	s_mov_b32 m0, s58
	s_nop 0
	global_load_lds_dwordx4 v192, s[44:45] sc1
	v_rcp_f32_e32 v215, v215
	s_waitcnt lgkmcnt(4)
	v_mfma_f32_32x32x16_f16 v[32:47], a[64:67], v[160:163], v[32:47]
	ds_read_b128 v[160:163], v192 offset:40960
	v_exp_f32_e32 v200, v128
	v_mfma_f32_32x32x16_f16 v[48:63], a[64:67], v[164:167], v[48:63]
	ds_read_b128 v[164:167], v192 offset:41984
	v_exp_f32_e32 v201, v129
	v_add_f32_e32 v200, 1.0, v200
	v_mfma_f32_32x32x16_f16 v[32:47], a[68:71], v[168:171], v[32:47]
	ds_read_b128 v[168:171], v192 offset:43008
	v_exp_f32_e32 v202, v130
	v_add_f32_e32 v201, 1.0, v201
	v_mfma_f32_32x32x16_f16 v[48:63], a[68:71], v[172:175], v[48:63]
	ds_read_b128 v[172:175], v192 offset:44032
	global_load_lds_dwordx4 v192, s[44:45] offset:1024 sc1
	v_exp_f32_e32 v203, v131
	v_add_f32_e32 v202, 1.0, v202
	s_waitcnt lgkmcnt(4)
	v_mfma_f32_32x32x16_f16 v[32:47], a[72:75], v[176:179], v[32:47]
	ds_read_b128 v[176:179], v192 offset:45056
	v_add_f32_e32 v203, 1.0, v203
	v_rcp_f32_e32 v200, v200
	v_mfma_f32_32x32x16_f16 v[48:63], a[72:75], v[180:183], v[48:63]
	ds_read_b128 v[180:183], v192 offset:46080
	v_rcp_f32_e32 v201, v201
	v_fma_f32 v200, v200, 2.0, -1.0
	v_mfma_f32_32x32x16_f16 v[32:47], a[76:79], v[184:187], v[32:47]
	ds_read_b128 v[184:187], v192 offset:47104
	v_rcp_f32_e32 v202, v202
	v_fma_f32 v201, v201, 2.0, -1.0
	v_mul_f32_e32 v216, v212, v200
	v_mfma_f32_32x32x16_f16 v[48:63], a[76:79], v[188:191], v[48:63]
	ds_read_b128 v[188:191], v192 offset:48128
	global_load_lds_dwordx4 v192, s[44:45] offset:2048 sc1
	v_rcp_f32_e32 v203, v203
	v_fma_f32 v202, v202, 2.0, -1.0
	v_mul_f32_e32 v217, v213, v201
	s_waitcnt lgkmcnt(4)
	v_mfma_f32_32x32x16_f16 v[32:47], a[80:83], v[160:163], v[32:47]
	ds_read_b128 v[160:163], v192 offset:49152
	v_fma_f32 v203, v203, 2.0, -1.0
	v_mul_f32_e32 v218, v214, v202
	v_exp_f32_e32 v200, v16
	v_mfma_f32_32x32x16_f16 v[48:63], a[80:83], v[164:167], v[48:63]
	ds_read_b128 v[164:167], v192 offset:50176
	v_mul_f32_e32 v219, v215, v203
	v_cvt_pk_f16_f32 v220, v216, v217
	v_exp_f32_e32 v201, v17
	v_mfma_f32_32x32x16_f16 v[32:47], a[84:87], v[168:171], v[32:47]
	ds_read_b128 v[168:171], v192 offset:51200
	v_cvt_pk_f16_f32 v221, v218, v219
	v_exp_f32_e32 v202, v18
	v_add_f32_e32 v200, 1.0, v200
	v_mfma_f32_32x32x16_f16 v[48:63], a[84:87], v[172:175], v[48:63]
	ds_read_b128 v[172:175], v192 offset:52224
	global_load_lds_dwordx4 v192, s[44:45] offset:3072 sc1
	s_cmp_lg_u32 s33, s60
	s_cbranch_scc1 .LE_nht26
	s_add_u32 s46, s62, 0x0
	s_addc_u32 s47, s63, 0
	global_store_dwordx4 v250, v[216:219], s[46:47]
	s_waitcnt vmcnt(0)
.LE_nht26:
	v_exp_f32_e32 v203, v19
	s_waitcnt lgkmcnt(4)
	v_mfma_f32_32x32x16_f16 v[32:47], a[88:91], v[176:179], v[32:47]
	ds_read_b128 v[176:179], v192 offset:53248
	v_exp_f32_e32 v204, v20
	v_add_f32_e32 v201, 1.0, v201
	v_add_f32_e32 v202, 1.0, v202
	v_mfma_f32_32x32x16_f16 v[48:63], a[88:91], v[180:183], v[48:63]
	ds_read_b128 v[180:183], v192 offset:54272
	v_exp_f32_e32 v205, v21
	v_add_f32_e32 v203, 1.0, v203
	v_add_f32_e32 v204, 1.0, v204
	v_mfma_f32_32x32x16_f16 v[32:47], a[92:95], v[184:187], v[32:47]
	ds_read_b128 v[184:187], v192 offset:55296
	v_exp_f32_e32 v206, v22
	v_add_f32_e32 v205, 1.0, v205
	v_mfma_f32_32x32x16_f16 v[48:63], a[92:95], v[188:191], v[48:63]
	ds_read_b128 v[188:191], v192 offset:56320
	s_add_u32 s44, s34, 0x19000
	s_addc_u32 s45, s35, 0
	s_mov_b32 m0, s59
	s_nop 0
	global_load_lds_dwordx4 v192, s[44:45] sc1
	v_exp_f32_e32 v207, v23
	v_add_f32_e32 v206, 1.0, v206
	s_waitcnt lgkmcnt(4)
	v_mfma_f32_32x32x16_f16 v[32:47], a[96:99], v[160:163], v[32:47]
	ds_read_b128 v[160:163], v192 offset:57344
	v_exp_f32_e32 v208, v24
	v_add_f32_e32 v207, 1.0, v207
	v_mfma_f32_32x32x16_f16 v[48:63], a[96:99], v[164:167], v[48:63]
	ds_read_b128 v[164:167], v192 offset:58368
	v_exp_f32_e32 v209, v25
	v_add_f32_e32 v208, 1.0, v208
	v_mfma_f32_32x32x16_f16 v[32:47], a[100:103], v[168:171], v[32:47]
	ds_read_b128 v[168:171], v192 offset:59392
	v_exp_f32_e32 v210, v26
	v_add_f32_e32 v209, 1.0, v209
	v_mfma_f32_32x32x16_f16 v[48:63], a[100:103], v[172:175], v[48:63]
	ds_read_b128 v[172:175], v192 offset:60416
	global_load_lds_dwordx4 v192, s[44:45] offset:1024 sc1
	v_exp_f32_e32 v211, v27
	v_add_f32_e32 v210, 1.0, v210
	s_waitcnt lgkmcnt(4)
	v_mfma_f32_32x32x16_f16 v[32:47], a[104:107], v[176:179], v[32:47]
	ds_read_b128 v[176:179], v192 offset:61440
	v_exp_f32_e32 v212, v28
	v_add_f32_e32 v211, 1.0, v211
	v_mfma_f32_32x32x16_f16 v[48:63], a[104:107], v[180:183], v[48:63]
	ds_read_b128 v[180:183], v192 offset:62464
	v_exp_f32_e32 v213, v29
	v_add_f32_e32 v212, 1.0, v212
	v_mfma_f32_32x32x16_f16 v[32:47], a[108:111], v[184:187], v[32:47]
	ds_read_b128 v[184:187], v192 offset:63488
	v_exp_f32_e32 v214, v30
	v_add_f32_e32 v213, 1.0, v213
	v_mfma_f32_32x32x16_f16 v[48:63], a[108:111], v[188:191], v[48:63]
	ds_read_b128 v[188:191], v192 offset:64512
	global_load_lds_dwordx4 v192, s[44:45] offset:2048 sc1
	v_exp_f32_e32 v215, v31
	v_add_f32_e32 v214, 1.0, v214
	s_waitcnt vmcnt(7)
	s_barrier
	s_waitcnt lgkmcnt(4)
	v_mfma_f32_32x32x16_f16 v[32:47], a[112:115], v[160:163], v[32:47]
	ds_read_b128 v[160:163], v193 offset:0
	v_add_f32_e32 v215, 1.0, v215
	v_rcp_f32_e32 v200, v200
	v_mfma_f32_32x32x16_f16 v[48:63], a[112:115], v[164:167], v[48:63]
	ds_read_b128 v[164:167], v193 offset:1024
	v_rcp_f32_e32 v201, v201
	v_mfma_f32_32x32x16_f16 v[32:47], a[116:119], v[168:171], v[32:47]
	ds_read_b128 v[168:171], v193 offset:2048
	v_rcp_f32_e32 v202, v202
	v_mfma_f32_32x32x16_f16 v[48:63], a[116:119], v[172:175], v[48:63]
	ds_read_b128 v[172:175], v193 offset:3072
	global_load_lds_dwordx4 v192, s[44:45] offset:3072 sc1
	v_rcp_f32_e32 v203, v203
	s_waitcnt lgkmcnt(4)
	v_mfma_f32_32x32x16_f16 v[32:47], a[120:123], v[176:179], v[32:47]
	ds_read_b128 v[176:179], v193 offset:4096
	v_rcp_f32_e32 v204, v204
	ds_read_b128 v[236:239], v248 offset:0
	ds_read_b64 v[240:241], v248 offset:32
	ds_read_b128 v[242:245], v248 offset:16
	ds_read_b64 v[246:247], v248 offset:40
	v_mfma_f32_32x32x16_f16 v[48:63], a[120:123], v[180:183], v[48:63]
	ds_read_b128 v[180:183], v193 offset:5120
	v_rcp_f32_e32 v205, v205
	v_mul_f32_e32 v204, v204, v132
	s_waitcnt lgkmcnt(3)
	v_fma_f32 v96, v229, v237, v240
	v_mfma_f32_32x32x16_f16 v[32:47], a[124:127], v[184:187], v[32:47]
	ds_read_b128 v[184:187], v193 offset:6144
	v_rcp_f32_e32 v206, v206
	v_mul_f32_e32 v205, v205, v133
	v_fma_f32 v97, v229, v239, v241
	v_fmac_f32_e32 v96, v228, v236
	v_mfma_f32_32x32x16_f16 v[48:63], a[124:127], v[188:191], v[48:63]
	ds_read_b128 v[188:191], v193 offset:7168
	v_cmp_gt_u32_e32 vcc, 3, v251
	s_cbranch_vccz .LE_tok27

.LE_join33:
	v_mfma_f32_32x32x16_f16 v[32:47], a[196:199], v[168:171], v[32:47]
	ds_read_b128 v[168:171], v193 offset:43008
	v_fma_f32 v126, v231, v243, v246
	v_fma_f32 v127, v231, v245, v247
	v_mfma_f32_32x32x16_f16 v[48:63], a[196:199], v[172:175], v[48:63]
	ds_read_b128 v[172:175], v193 offset:44032
	global_load_lds_dwordx4 v192, s[44:45] offset:1024 sc1
	v_fmac_f32_e32 v126, v230, v242
	v_fmac_f32_e32 v127, v230, v244
	s_waitcnt lgkmcnt(4)
	v_mfma_f32_32x32x16_f16 v[32:47], a[200:203], v[176:179], v[32:47]
	ds_read_b128 v[176:179], v193 offset:45056
	v_mfma_f32_32x32x16_f16 v[48:63], a[200:203], v[180:183], v[48:63]
	ds_read_b128 v[180:183], v193 offset:46080
	v_mfma_f32_32x32x16_f16 v[32:47], a[204:207], v[184:187], v[32:47]
	ds_read_b128 v[184:187], v193 offset:47104
	v_mfma_f32_32x32x16_f16 v[48:63], a[204:207], v[188:191], v[48:63]
	ds_read_b128 v[188:191], v193 offset:48128
	global_load_lds_dwordx4 v192, s[44:45] offset:2048 sc1
	s_waitcnt lgkmcnt(4)
	v_mfma_f32_32x32x16_f16 v[32:47], a[208:211], v[160:163], v[32:47]
	ds_read_b128 v[160:163], v193 offset:49152
	v_mfma_f32_32x32x16_f16 v[48:63], a[208:211], v[164:167], v[48:63]
	ds_read_b128 v[164:167], v193 offset:50176
	v_mfma_f32_32x32x16_f16 v[32:47], a[212:215], v[168:171], v[32:47]
	ds_read_b128 v[168:171], v193 offset:51200
	v_mfma_f32_32x32x16_f16 v[48:63], a[212:215], v[172:175], v[48:63]
	ds_read_b128 v[172:175], v193 offset:52224
	global_load_lds_dwordx4 v192, s[44:45] offset:3072 sc1
	s_waitcnt lgkmcnt(4)
	v_mfma_f32_32x32x16_f16 v[32:47], a[216:219], v[176:179], v[32:47]
	ds_read_b128 v[176:179], v193 offset:53248
	v_mfma_f32_32x32x16_f16 v[48:63], a[216:219], v[180:183], v[48:63]
	ds_read_b128 v[180:183], v193 offset:54272
	v_mfma_f32_32x32x16_f16 v[32:47], a[220:223], v[184:187], v[32:47]
	ds_read_b128 v[184:187], v193 offset:55296
	v_mfma_f32_32x32x16_f16 v[48:63], a[220:223], v[188:191], v[48:63]
	ds_read_b128 v[188:191], v193 offset:56320
	s_add_u32 s44, s34, 0x9000
	s_addc_u32 s45, s35, 0
	s_mov_b32 m0, s55
	s_nop 0
	global_load_lds_dwordx4 v192, s[44:45] sc1
	s_waitcnt lgkmcnt(4)
	v_mfma_f32_32x32x16_f16 v[32:47], a[224:227], v[160:163], v[32:47]
	ds_read_b128 v[160:163], v193 offset:57344
	v_mfma_f32_32x32x16_f16 v[48:63], a[224:227], v[164:167], v[48:63]
	ds_read_b128 v[164:167], v193 offset:58368
	v_mfma_f32_32x32x16_f16 v[32:47], a[228:231], v[168:171], v[32:47]
	ds_read_b128 v[168:171], v193 offset:59392
	v_mfma_f32_32x32x16_f16 v[48:63], a[228:231], v[172:175], v[48:63]
	ds_read_b128 v[172:175], v193 offset:60416
	global_load_lds_dwordx4 v192, s[44:45] offset:1024 sc1
	s_waitcnt lgkmcnt(4)
	v_mfma_f32_32x32x16_f16 v[32:47], a[232:235], v[176:179], v[32:47]
	ds_read_b128 v[176:179], v193 offset:61440
	v_mfma_f32_32x32x16_f16 v[48:63], a[232:235], v[180:183], v[48:63]
	ds_read_b128 v[180:183], v193 offset:62464
	v_mfma_f32_32x32x16_f16 v[32:47], a[236:239], v[184:187], v[32:47]
	ds_read_b128 v[184:187], v193 offset:63488
	v_mfma_f32_32x32x16_f16 v[48:63], a[236:239], v[188:191], v[48:63]
	ds_read_b128 v[188:191], v193 offset:64512
	global_load_lds_dwordx4 v192, s[44:45] offset:2048 sc1
	s_waitcnt vmcnt(8)
	s_barrier
	s_waitcnt lgkmcnt(4)
	v_mfma_f32_32x32x16_f16 v[32:47], a[240:243], v[160:163], v[32:47]
	ds_read_b128 v[160:163], v192 offset:0
	v_mfma_f32_32x32x16_f16 v[48:63], a[240:243], v[164:167], v[48:63]
	ds_read_b128 v[164:167], v192 offset:1024
	v_mfma_f32_32x32x16_f16 v[32:47], a[244:247], v[168:171], v[32:47]
	ds_read_b128 v[168:171], v192 offset:2048
	v_mfma_f32_32x32x16_f16 v[48:63], a[244:247], v[172:175], v[48:63]
	ds_read_b128 v[172:175], v192 offset:3072
	global_load_lds_dwordx4 v192, s[44:45] offset:3072 sc1
	s_waitcnt lgkmcnt(4)
	v_mfma_f32_32x32x16_f16 v[32:47], a[248:251], v[176:179], v[32:47]
	ds_read_b128 v[176:179], v192 offset:4096
	v_mfma_f32_32x32x16_f16 v[48:63], a[248:251], v[180:183], v[48:63]
	ds_read_b128 v[180:183], v192 offset:5120
	v_mfma_f32_32x32x16_f16 v[32:47], a[252:255], v[184:187], v[32:47]
	ds_read_b128 v[184:187], v192 offset:6144
	v_mfma_f32_32x32x16_f16 v[48:63], a[252:255], v[188:191], v[48:63]
	ds_read_b128 v[188:191], v192 offset:7168
	s_add_u32 s44, s34, 0x10000
	s_addc_u32 s45, s35, 0
	s_mov_b32 m0, s56
	s_nop 0
	global_load_lds_dwordx4 v192, s[44:45] sc1
	s_and_b32 s64, s33, 1
	s_lshl_b32 s64, s64, 22
	s_add_u32 s64, s64, s50
	s_add_u32 s64, s64, 0x20000
	s_add_u32 s36, s6, s64
	s_addc_u32 s37, s7, 0
	s_lshl_b32 s64, s33, 3
	s_add_u32 s64, s64, s29
	s_lshl_b32 s64, s64, 5
	s_add_u32 s64, s64, s30
	s_lshl_b32 s64, s64, 2
	s_add_u32 s40, s8, s64
	s_addc_u32 s41, s9, 0
	s_lshl_b32 s64, s61, 11
	s_lshl_b32 s65, s29, 8
	s_add_u32 s64, s64, s65
	s_lshl_b32 s64, s64, 3
	s_add_u32 s42, s12, s64
	s_addc_u32 s43, s13, 0
	s_nop 3
	global_load_dwordx2 v[228:229], v249, s[42:43] offset:0
	global_load_dwordx2 v[230:231], v249, s[42:43] offset:256
	s_waitcnt lgkmcnt(4)
	v_mfma_f32_32x32x16_f16 v[64:79], a[0:3], v[160:163], v[64:79]
	ds_read_b128 v[160:163], v192 offset:8192
	v_exp_f32_e32 v200, v32
	v_mfma_f32_32x32x16_f16 v[80:95], a[0:3], v[164:167], v[80:95]
	ds_read_b128 v[164:167], v192 offset:9216
	s_lshl_b32 s64, s71, 3
	s_add_u32 s64, s64, s29
	s_lshl_b32 s64, s64, 7
	s_add_u32 s38, s8, s64
	s_addc_u32 s39, s9, 0
	global_load_dword v251, v196, s[38:39] sc1
	v_exp_f32_e32 v201, v33
	v_add_f32_e32 v200, 1.0, v200
	v_mfma_f32_32x32x16_f16 v[64:79], a[4:7], v[168:171], v[64:79]
	ds_read_b128 v[168:171], v192 offset:10240
	v_exp_f32_e32 v202, v34
	v_add_f32_e32 v201, 1.0, v201
	v_mfma_f32_32x32x16_f16 v[80:95], a[4:7], v[172:175], v[80:95]
	ds_read_b128 v[172:175], v192 offset:11264
	global_load_lds_dwordx4 v192, s[44:45] offset:1024 sc1
	v_exp_f32_e32 v203, v35
	v_add_f32_e32 v202, 1.0, v202
	s_waitcnt lgkmcnt(4)
	v_mfma_f32_32x32x16_f16 v[64:79], a[8:11], v[176:179], v[64:79]
	ds_read_b128 v[176:179], v192 offset:12288
	v_exp_f32_e32 v204, v36
	v_add_f32_e32 v203, 1.0, v203
	v_mfma_f32_32x32x16_f16 v[80:95], a[8:11], v[180:183], v[80:95]
	ds_read_b128 v[180:183], v192 offset:13312
	v_exp_f32_e32 v205, v37
	v_add_f32_e32 v204, 1.0, v204
	v_mfma_f32_32x32x16_f16 v[64:79], a[12:15], v[184:187], v[64:79]
	ds_read_b128 v[184:187], v192 offset:14336
	v_exp_f32_e32 v206, v38
	v_add_f32_e32 v205, 1.0, v205
	v_mfma_f32_32x32x16_f16 v[80:95], a[12:15], v[188:191], v[80:95]
	ds_read_b128 v[188:191], v192 offset:15360
	global_load_lds_dwordx4 v192, s[44:45] offset:2048 sc1
	v_exp_f32_e32 v207, v39
	v_add_f32_e32 v206, 1.0, v206
	s_waitcnt lgkmcnt(4)
	v_mfma_f32_32x32x16_f16 v[64:79], a[16:19], v[160:163], v[64:79]
	ds_read_b128 v[160:163], v192 offset:16384
	v_exp_f32_e32 v208, v40
	v_add_f32_e32 v207, 1.0, v207
	v_mfma_f32_32x32x16_f16 v[80:95], a[16:19], v[164:167], v[80:95]
	ds_read_b128 v[164:167], v192 offset:17408
	v_exp_f32_e32 v209, v41
	v_add_f32_e32 v208, 1.0, v208
	v_mfma_f32_32x32x16_f16 v[64:79], a[20:23], v[168:171], v[64:79]
	ds_read_b128 v[168:171], v192 offset:18432
	v_exp_f32_e32 v210, v42
	v_add_f32_e32 v209, 1.0, v209
	v_mfma_f32_32x32x16_f16 v[80:95], a[20:23], v[172:175], v[80:95]
	ds_read_b128 v[172:175], v192 offset:19456
	global_load_lds_dwordx4 v192, s[44:45] offset:3072 sc1
	v_exp_f32_e32 v211, v43
	v_add_f32_e32 v210, 1.0, v210
	s_waitcnt lgkmcnt(4)
	v_mfma_f32_32x32x16_f16 v[64:79], a[24:27], v[176:179], v[64:79]
	ds_read_b128 v[176:179], v192 offset:20480
	v_exp_f32_e32 v212, v44
	v_add_f32_e32 v211, 1.0, v211
	v_mfma_f32_32x32x16_f16 v[80:95], a[24:27], v[180:183], v[80:95]
	ds_read_b128 v[180:183], v192 offset:21504
	v_exp_f32_e32 v213, v45
	v_add_f32_e32 v212, 1.0, v212
	v_mfma_f32_32x32x16_f16 v[64:79], a[28:31], v[184:187], v[64:79]
	ds_read_b128 v[184:187], v192 offset:22528
	v_exp_f32_e32 v214, v46
	v_add_f32_e32 v213, 1.0, v213
	v_mfma_f32_32x32x16_f16 v[80:95], a[28:31], v[188:191], v[80:95]
	ds_read_b128 v[188:191], v192 offset:23552
	s_add_u32 s44, s34, 0x11000
	s_addc_u32 s45, s35, 0
	s_mov_b32 m0, s57
	s_nop 0
	global_load_lds_dwordx4 v192, s[44:45] sc1
	v_exp_f32_e32 v215, v47
	v_add_f32_e32 v214, 1.0, v214
	s_waitcnt lgkmcnt(4)
	v_mfma_f32_32x32x16_f16 v[64:79], a[32:35], v[160:163], v[64:79]
	ds_read_b128 v[160:163], v192 offset:24576
	v_add_f32_e32 v215, 1.0, v215
	v_rcp_f32_e32 v200, v200
	v_mfma_f32_32x32x16_f16 v[80:95], a[32:35], v[164:167], v[80:95]
	ds_read_b128 v[164:167], v192 offset:25600
	v_rcp_f32_e32 v201, v201
	v_mfma_f32_32x32x16_f16 v[64:79], a[36:39], v[168:171], v[64:79]
	ds_read_b128 v[168:171], v192 offset:26624
	v_rcp_f32_e32 v202, v202
	v_mfma_f32_32x32x16_f16 v[80:95], a[36:39], v[172:175], v[80:95]
	ds_read_b128 v[172:175], v192 offset:27648
	global_load_lds_dwordx4 v192, s[44:45] offset:1024 sc1
	v_rcp_f32_e32 v203, v203
	s_waitcnt lgkmcnt(4)
	v_mfma_f32_32x32x16_f16 v[64:79], a[40:43], v[176:179], v[64:79]
	ds_read_b128 v[176:179], v192 offset:28672
	v_rcp_f32_e32 v204, v204
	v_mfma_f32_32x32x16_f16 v[80:95], a[40:43], v[180:183], v[80:95]
	ds_read_b128 v[180:183], v192 offset:29696
	v_rcp_f32_e32 v205, v205
	v_mul_f32_e32 v204, v204, v136
	v_mfma_f32_32x32x16_f16 v[64:79], a[44:47], v[184:187], v[64:79]
	ds_read_b128 v[184:187], v192 offset:30720
	v_rcp_f32_e32 v206, v206
	v_mul_f32_e32 v205, v205, v137
	v_mfma_f32_32x32x16_f16 v[80:95], a[44:47], v[188:191], v[80:95]
	ds_read_b128 v[188:191], v192 offset:31744
	global_load_lds_dwordx4 v192, s[44:45] offset:2048 sc1
	v_rcp_f32_e32 v207, v207
	v_mul_f32_e32 v206, v206, v138
	s_waitcnt vmcnt(10)
	s_barrier
	s_waitcnt lgkmcnt(4)
	v_mfma_f32_32x32x16_f16 v[64:79], a[48:51], v[160:163], v[64:79]
	ds_read_b128 v[160:163], v192 offset:32768
	v_rcp_f32_e32 v208, v208
	v_mul_f32_e32 v207, v207, v139
	v_mfma_f32_32x32x16_f16 v[80:95], a[48:51], v[164:167], v[80:95]
	ds_read_b128 v[164:167], v192 offset:33792
	v_rcp_f32_e32 v209, v209
	v_fmamk_f32 v208, v208, 0xc0b8aa3b, v198
	v_mfma_f32_32x32x16_f16 v[64:79], a[52:55], v[168:171], v[64:79]
	ds_read_b128 v[168:171], v192 offset:34816
	v_rcp_f32_e32 v210, v210
	v_fmamk_f32 v209, v209, 0xc0b8aa3b, v198
	v_fma_f32 v136, v200, v208, v204
	v_mfma_f32_32x32x16_f16 v[80:95], a[52:55], v[172:175], v[80:95]
	ds_read_b128 v[172:175], v192 offset:35840
	global_load_lds_dwordx4 v192, s[44:45] offset:3072 sc1
	v_rcp_f32_e32 v211, v211
	v_fmamk_f32 v210, v210, 0xc0b8aa3b, v198
	v_fma_f32 v137, v201, v209, v205
	s_waitcnt lgkmcnt(4)
	v_mfma_f32_32x32x16_f16 v[64:79], a[56:59], v[176:179], v[64:79]
	ds_read_b128 v[176:179], v192 offset:36864
	v_rcp_f32_e32 v212, v212
	v_fmamk_f32 v211, v211, 0xc0b8aa3b, v198
	v_fma_f32 v138, v202, v210, v206
	v_mfma_f32_32x32x16_f16 v[80:95], a[56:59], v[180:183], v[80:95]
	ds_read_b128 v[180:183], v192 offset:37888
	v_rcp_f32_e32 v213, v213
	v_fma_f32 v139, v203, v211, v207
	v_mfma_f32_32x32x16_f16 v[64:79], a[60:63], v[184:187], v[64:79]
	ds_read_b128 v[184:187], v192 offset:38912
	v_rcp_f32_e32 v214, v214
	v_mfma_f32_32x32x16_f16 v[80:95], a[60:63], v[188:191], v[80:95]
	ds_read_b128 v[188:191], v192 offset:39936
	s_add_u32 s44, s34, 0x18000
	s_addc_u32 s45, s35, 0
	s_mov_b32 m0, s58
	s_nop 0
	global_load_lds_dwordx4 v192, s[44:45] sc1
	v_rcp_f32_e32 v215, v215
	s_waitcnt lgkmcnt(4)
	v_mfma_f32_32x32x16_f16 v[64:79], a[64:67], v[160:163], v[64:79]
	ds_read_b128 v[160:163], v192 offset:40960
	v_exp_f32_e32 v200, v136
	v_mfma_f32_32x32x16_f16 v[80:95], a[64:67], v[164:167], v[80:95]
	ds_read_b128 v[164:167], v192 offset:41984
	v_exp_f32_e32 v201, v137
	v_add_f32_e32 v200, 1.0, v200
	v_mfma_f32_32x32x16_f16 v[64:79], a[68:71], v[168:171], v[64:79]
	ds_read_b128 v[168:171], v192 offset:43008
	v_exp_f32_e32 v202, v138
	v_add_f32_e32 v201, 1.0, v201
	v_mfma_f32_32x32x16_f16 v[80:95], a[68:71], v[172:175], v[80:95]
	ds_read_b128 v[172:175], v192 offset:44032
	global_load_lds_dwordx4 v192, s[44:45] offset:1024 sc1
	v_exp_f32_e32 v203, v139
	v_add_f32_e32 v202, 1.0, v202
	s_waitcnt lgkmcnt(4)
	v_mfma_f32_32x32x16_f16 v[64:79], a[72:75], v[176:179], v[64:79]
	ds_read_b128 v[176:179], v192 offset:45056
	v_add_f32_e32 v203, 1.0, v203
	v_rcp_f32_e32 v200, v200
	v_mfma_f32_32x32x16_f16 v[80:95], a[72:75], v[180:183], v[80:95]
	ds_read_b128 v[180:183], v192 offset:46080
	v_rcp_f32_e32 v201, v201
	v_fma_f32 v200, v200, 2.0, -1.0
	v_mfma_f32_32x32x16_f16 v[64:79], a[76:79], v[184:187], v[64:79]
	ds_read_b128 v[184:187], v192 offset:47104
	v_rcp_f32_e32 v202, v202
	v_fma_f32 v201, v201, 2.0, -1.0
	v_mul_f32_e32 v216, v212, v200
	v_mfma_f32_32x32x16_f16 v[80:95], a[76:79], v[188:191], v[80:95]
	ds_read_b128 v[188:191], v192 offset:48128
	global_load_lds_dwordx4 v192, s[44:45] offset:2048 sc1
	v_rcp_f32_e32 v203, v203
	v_fma_f32 v202, v202, 2.0, -1.0
	v_mul_f32_e32 v217, v213, v201
	s_waitcnt lgkmcnt(4)
	v_mfma_f32_32x32x16_f16 v[64:79], a[80:83], v[160:163], v[64:79]
	ds_read_b128 v[160:163], v192 offset:49152
	v_fma_f32 v203, v203, 2.0, -1.0
	v_mul_f32_e32 v218, v214, v202
	v_exp_f32_e32 v200, v48
	v_mfma_f32_32x32x16_f16 v[80:95], a[80:83], v[164:167], v[80:95]
	ds_read_b128 v[164:167], v192 offset:50176
	v_mul_f32_e32 v219, v215, v203
	v_cvt_pk_f16_f32 v220, v216, v217
	v_exp_f32_e32 v201, v49
	v_mfma_f32_32x32x16_f16 v[64:79], a[84:87], v[168:171], v[64:79]
	ds_read_b128 v[168:171], v192 offset:51200
	v_cvt_pk_f16_f32 v221, v218, v219
	v_exp_f32_e32 v202, v50
	v_add_f32_e32 v200, 1.0, v200
	v_mfma_f32_32x32x16_f16 v[80:95], a[84:87], v[172:175], v[80:95]
	ds_read_b128 v[172:175], v192 offset:52224
	global_load_lds_dwordx4 v192, s[44:45] offset:3072 sc1
	s_cmp_lg_u32 s33, s60
	s_cbranch_scc1 .LE_nht34
	s_add_u32 s46, s62, 0x40000
	s_addc_u32 s47, s63, 0
	global_store_dwordx4 v250, v[216:219], s[46:47]
	s_waitcnt vmcnt(0)
.LE_nht34:
	v_exp_f32_e32 v203, v51
	s_waitcnt lgkmcnt(4)
	v_mfma_f32_32x32x16_f16 v[64:79], a[88:91], v[176:179], v[64:79]
	ds_read_b128 v[176:179], v192 offset:53248
	v_exp_f32_e32 v204, v52
	v_add_f32_e32 v201, 1.0, v201
	v_add_f32_e32 v202, 1.0, v202
	v_mfma_f32_32x32x16_f16 v[80:95], a[88:91], v[180:183], v[80:95]
	ds_read_b128 v[180:183], v192 offset:54272
	v_exp_f32_e32 v205, v53
	v_add_f32_e32 v203, 1.0, v203
	v_add_f32_e32 v204, 1.0, v204
	v_mfma_f32_32x32x16_f16 v[64:79], a[92:95], v[184:187], v[64:79]
	ds_read_b128 v[184:187], v192 offset:55296
	v_exp_f32_e32 v206, v54
	v_add_f32_e32 v205, 1.0, v205
	v_mfma_f32_32x32x16_f16 v[80:95], a[92:95], v[188:191], v[80:95]
	ds_read_b128 v[188:191], v192 offset:56320
	s_add_u32 s44, s34, 0x19000
	s_addc_u32 s45, s35, 0
	s_mov_b32 m0, s59
	s_nop 0
	global_load_lds_dwordx4 v192, s[44:45] sc1
	v_exp_f32_e32 v207, v55
	v_add_f32_e32 v206, 1.0, v206
	s_waitcnt lgkmcnt(4)
	v_mfma_f32_32x32x16_f16 v[64:79], a[96:99], v[160:163], v[64:79]
	ds_read_b128 v[160:163], v192 offset:57344
	v_exp_f32_e32 v208, v56
	v_add_f32_e32 v207, 1.0, v207
	v_mfma_f32_32x32x16_f16 v[80:95], a[96:99], v[164:167], v[80:95]
	ds_read_b128 v[164:167], v192 offset:58368
	v_exp_f32_e32 v209, v57
	v_add_f32_e32 v208, 1.0, v208
	v_mfma_f32_32x32x16_f16 v[64:79], a[100:103], v[168:171], v[64:79]
	ds_read_b128 v[168:171], v192 offset:59392
	v_exp_f32_e32 v210, v58
	v_add_f32_e32 v209, 1.0, v209
	v_mfma_f32_32x32x16_f16 v[80:95], a[100:103], v[172:175], v[80:95]
	ds_read_b128 v[172:175], v192 offset:60416
	global_load_lds_dwordx4 v192, s[44:45] offset:1024 sc1
	v_exp_f32_e32 v211, v59
	v_add_f32_e32 v210, 1.0, v210
	s_waitcnt lgkmcnt(4)
	v_mfma_f32_32x32x16_f16 v[64:79], a[104:107], v[176:179], v[64:79]
	ds_read_b128 v[176:179], v192 offset:61440
	v_exp_f32_e32 v212, v60
	v_add_f32_e32 v211, 1.0, v211
	v_mfma_f32_32x32x16_f16 v[80:95], a[104:107], v[180:183], v[80:95]
	ds_read_b128 v[180:183], v192 offset:62464
	v_exp_f32_e32 v213, v61
	v_add_f32_e32 v212, 1.0, v212
	v_mfma_f32_32x32x16_f16 v[64:79], a[108:111], v[184:187], v[64:79]
	ds_read_b128 v[184:187], v192 offset:63488
	v_exp_f32_e32 v214, v62
	v_add_f32_e32 v213, 1.0, v213
	v_mfma_f32_32x32x16_f16 v[80:95], a[108:111], v[188:191], v[80:95]
	ds_read_b128 v[188:191], v192 offset:64512
	global_load_lds_dwordx4 v192, s[44:45] offset:2048 sc1
	v_exp_f32_e32 v215, v63
	v_add_f32_e32 v214, 1.0, v214
	s_waitcnt vmcnt(7)
	s_barrier
	s_waitcnt lgkmcnt(4)
	v_mfma_f32_32x32x16_f16 v[64:79], a[112:115], v[160:163], v[64:79]
	ds_read_b128 v[160:163], v193 offset:0
	v_add_f32_e32 v215, 1.0, v215
	v_rcp_f32_e32 v200, v200
	v_mfma_f32_32x32x16_f16 v[80:95], a[112:115], v[164:167], v[80:95]
	ds_read_b128 v[164:167], v193 offset:1024
	v_rcp_f32_e32 v201, v201
	v_mfma_f32_32x32x16_f16 v[64:79], a[116:119], v[168:171], v[64:79]
	ds_read_b128 v[168:171], v193 offset:2048
	v_rcp_f32_e32 v202, v202
	v_mfma_f32_32x32x16_f16 v[80:95], a[116:119], v[172:175], v[80:95]
	ds_read_b128 v[172:175], v193 offset:3072
	global_load_lds_dwordx4 v192, s[44:45] offset:3072 sc1
	v_rcp_f32_e32 v203, v203
	s_waitcnt lgkmcnt(4)
	v_mfma_f32_32x32x16_f16 v[64:79], a[120:123], v[176:179], v[64:79]
	ds_read_b128 v[176:179], v193 offset:4096
	v_rcp_f32_e32 v204, v204
	ds_read_b128 v[236:239], v248 offset:0
	ds_read_b64 v[240:241], v248 offset:32
	ds_read_b128 v[242:245], v248 offset:16
	ds_read_b64 v[246:247], v248 offset:40
	v_mfma_f32_32x32x16_f16 v[80:95], a[120:123], v[180:183], v[80:95]
	ds_read_b128 v[180:183], v193 offset:5120
	v_rcp_f32_e32 v205, v205
	v_mul_f32_e32 v204, v204, v140
	s_waitcnt lgkmcnt(3)
	v_fma_f32 v0, v229, v237, v240
	v_mfma_f32_32x32x16_f16 v[64:79], a[124:127], v[184:187], v[64:79]
	ds_read_b128 v[184:187], v193 offset:6144
	v_rcp_f32_e32 v206, v206
	v_mul_f32_e32 v205, v205, v141
	v_fma_f32 v1, v229, v239, v241
	v_fmac_f32_e32 v0, v228, v236
	v_mfma_f32_32x32x16_f16 v[80:95], a[124:127], v[188:191], v[80:95]
	ds_read_b128 v[188:191], v193 offset:7168
	v_cmp_gt_u32_e32 vcc, 4, v251
	s_cbranch_vccz .LE_tok35

.LE_join41:
	v_mfma_f32_32x32x16_f16 v[64:79], a[196:199], v[168:171], v[64:79]
	ds_read_b128 v[168:171], v193 offset:43008
	v_fma_f32 v30, v231, v243, v246
	v_fma_f32 v31, v231, v245, v247
	v_mfma_f32_32x32x16_f16 v[80:95], a[196:199], v[172:175], v[80:95]
	ds_read_b128 v[172:175], v193 offset:44032
	global_load_lds_dwordx4 v192, s[44:45] offset:1024 sc1
	v_fmac_f32_e32 v30, v230, v242
	v_fmac_f32_e32 v31, v230, v244
	s_waitcnt lgkmcnt(4)
	v_mfma_f32_32x32x16_f16 v[64:79], a[200:203], v[176:179], v[64:79]
	ds_read_b128 v[176:179], v193 offset:45056
	v_mfma_f32_32x32x16_f16 v[80:95], a[200:203], v[180:183], v[80:95]
	ds_read_b128 v[180:183], v193 offset:46080
	v_mfma_f32_32x32x16_f16 v[64:79], a[204:207], v[184:187], v[64:79]
	ds_read_b128 v[184:187], v193 offset:47104
	v_mfma_f32_32x32x16_f16 v[80:95], a[204:207], v[188:191], v[80:95]
	ds_read_b128 v[188:191], v193 offset:48128
	global_load_lds_dwordx4 v192, s[44:45] offset:2048 sc1
	s_waitcnt lgkmcnt(4)
	v_mfma_f32_32x32x16_f16 v[64:79], a[208:211], v[160:163], v[64:79]
	ds_read_b128 v[160:163], v193 offset:49152
	v_mfma_f32_32x32x16_f16 v[80:95], a[208:211], v[164:167], v[80:95]
	ds_read_b128 v[164:167], v193 offset:50176
	v_mfma_f32_32x32x16_f16 v[64:79], a[212:215], v[168:171], v[64:79]
	ds_read_b128 v[168:171], v193 offset:51200
	v_mfma_f32_32x32x16_f16 v[80:95], a[212:215], v[172:175], v[80:95]
	ds_read_b128 v[172:175], v193 offset:52224
	global_load_lds_dwordx4 v192, s[44:45] offset:3072 sc1
	s_waitcnt lgkmcnt(4)
	v_mfma_f32_32x32x16_f16 v[64:79], a[216:219], v[176:179], v[64:79]
	ds_read_b128 v[176:179], v193 offset:53248
	v_mfma_f32_32x32x16_f16 v[80:95], a[216:219], v[180:183], v[80:95]
	ds_read_b128 v[180:183], v193 offset:54272
	v_mfma_f32_32x32x16_f16 v[64:79], a[220:223], v[184:187], v[64:79]
	ds_read_b128 v[184:187], v193 offset:55296
	v_mfma_f32_32x32x16_f16 v[80:95], a[220:223], v[188:191], v[80:95]
	ds_read_b128 v[188:191], v193 offset:56320
	s_add_u32 s44, s34, 0x9000
	s_addc_u32 s45, s35, 0
	s_mov_b32 m0, s55
	s_nop 0
	global_load_lds_dwordx4 v192, s[44:45] sc1
	s_waitcnt lgkmcnt(4)
	v_mfma_f32_32x32x16_f16 v[64:79], a[224:227], v[160:163], v[64:79]
	ds_read_b128 v[160:163], v193 offset:57344
	v_mfma_f32_32x32x16_f16 v[80:95], a[224:227], v[164:167], v[80:95]
	ds_read_b128 v[164:167], v193 offset:58368
	v_mfma_f32_32x32x16_f16 v[64:79], a[228:231], v[168:171], v[64:79]
	ds_read_b128 v[168:171], v193 offset:59392
	v_mfma_f32_32x32x16_f16 v[80:95], a[228:231], v[172:175], v[80:95]
	ds_read_b128 v[172:175], v193 offset:60416
	global_load_lds_dwordx4 v192, s[44:45] offset:1024 sc1
	s_waitcnt lgkmcnt(4)
	v_mfma_f32_32x32x16_f16 v[64:79], a[232:235], v[176:179], v[64:79]
	ds_read_b128 v[176:179], v193 offset:61440
	v_mfma_f32_32x32x16_f16 v[80:95], a[232:235], v[180:183], v[80:95]
	ds_read_b128 v[180:183], v193 offset:62464
	v_mfma_f32_32x32x16_f16 v[64:79], a[236:239], v[184:187], v[64:79]
	ds_read_b128 v[184:187], v193 offset:63488
	v_mfma_f32_32x32x16_f16 v[80:95], a[236:239], v[188:191], v[80:95]
	ds_read_b128 v[188:191], v193 offset:64512
	global_load_lds_dwordx4 v192, s[44:45] offset:2048 sc1
	s_waitcnt vmcnt(8)
	s_barrier
	s_waitcnt lgkmcnt(4)
	v_mfma_f32_32x32x16_f16 v[64:79], a[240:243], v[160:163], v[64:79]
	ds_read_b128 v[160:163], v192 offset:0
	v_mfma_f32_32x32x16_f16 v[80:95], a[240:243], v[164:167], v[80:95]
	ds_read_b128 v[164:167], v192 offset:1024
	v_mfma_f32_32x32x16_f16 v[64:79], a[244:247], v[168:171], v[64:79]
	ds_read_b128 v[168:171], v192 offset:2048
	v_mfma_f32_32x32x16_f16 v[80:95], a[244:247], v[172:175], v[80:95]
	ds_read_b128 v[172:175], v192 offset:3072
	global_load_lds_dwordx4 v192, s[44:45] offset:3072 sc1
	s_waitcnt lgkmcnt(4)
	v_mfma_f32_32x32x16_f16 v[64:79], a[248:251], v[176:179], v[64:79]
	ds_read_b128 v[176:179], v192 offset:4096
	v_mfma_f32_32x32x16_f16 v[80:95], a[248:251], v[180:183], v[80:95]
	ds_read_b128 v[180:183], v192 offset:5120
	v_mfma_f32_32x32x16_f16 v[64:79], a[252:255], v[184:187], v[64:79]
	ds_read_b128 v[184:187], v192 offset:6144
	v_mfma_f32_32x32x16_f16 v[80:95], a[252:255], v[188:191], v[80:95]
	ds_read_b128 v[188:191], v192 offset:7168
	s_add_u32 s44, s34, 0x10000
	s_addc_u32 s45, s35, 0
	s_mov_b32 m0, s56
	s_nop 0
	global_load_lds_dwordx4 v192, s[44:45] sc1
	s_and_b32 s64, s33, 1
	s_lshl_b32 s64, s64, 22
	s_add_u32 s64, s64, s50
	s_add_u32 s64, s64, 0x40000
	s_add_u32 s36, s6, s64
	s_addc_u32 s37, s7, 0
	s_lshl_b32 s64, s33, 3
	s_add_u32 s64, s64, s29
	s_lshl_b32 s64, s64, 5
	s_add_u32 s64, s64, s30
	s_lshl_b32 s64, s64, 2
	s_add_u32 s40, s8, s64
	s_addc_u32 s41, s9, 0
	s_lshl_b32 s64, s61, 11
	s_lshl_b32 s65, s29, 8
	s_add_u32 s64, s64, s65
	s_add_u32 s64, s64, 64
	s_lshl_b32 s64, s64, 3
	s_add_u32 s42, s12, s64
	s_addc_u32 s43, s13, 0
	s_nop 3
	global_load_dwordx2 v[228:229], v249, s[42:43] offset:0
	global_load_dwordx2 v[230:231], v249, s[42:43] offset:256
	s_waitcnt lgkmcnt(4)
	v_mfma_f32_32x32x16_f16 v[96:111], a[0:3], v[160:163], v[96:111]
	ds_read_b128 v[160:163], v192 offset:8192
	v_exp_f32_e32 v200, v64
	v_mfma_f32_32x32x16_f16 v[112:127], a[0:3], v[164:167], v[112:127]
	ds_read_b128 v[164:167], v192 offset:9216
	s_lshl_b32 s64, s33, 3
	s_add_u32 s64, s64, s29
	s_lshl_b32 s64, s64, 7
	s_add_u32 s38, s8, s64
	s_addc_u32 s39, s9, 0
	global_load_dword v251, v196, s[38:39] sc1
	v_exp_f32_e32 v201, v65
	v_add_f32_e32 v200, 1.0, v200
	v_mfma_f32_32x32x16_f16 v[96:111], a[4:7], v[168:171], v[96:111]
	ds_read_b128 v[168:171], v192 offset:10240
	v_exp_f32_e32 v202, v66
	v_add_f32_e32 v201, 1.0, v201
	v_mfma_f32_32x32x16_f16 v[112:127], a[4:7], v[172:175], v[112:127]
	ds_read_b128 v[172:175], v192 offset:11264
	global_load_lds_dwordx4 v192, s[44:45] offset:1024 sc1
	v_exp_f32_e32 v203, v67
	v_add_f32_e32 v202, 1.0, v202
	s_waitcnt lgkmcnt(4)
	v_mfma_f32_32x32x16_f16 v[96:111], a[8:11], v[176:179], v[96:111]
	ds_read_b128 v[176:179], v192 offset:12288
	v_exp_f32_e32 v204, v68
	v_add_f32_e32 v203, 1.0, v203
	v_mfma_f32_32x32x16_f16 v[112:127], a[8:11], v[180:183], v[112:127]
	ds_read_b128 v[180:183], v192 offset:13312
	v_exp_f32_e32 v205, v69
	v_add_f32_e32 v204, 1.0, v204
	v_mfma_f32_32x32x16_f16 v[96:111], a[12:15], v[184:187], v[96:111]
	ds_read_b128 v[184:187], v192 offset:14336
	v_exp_f32_e32 v206, v70
	v_add_f32_e32 v205, 1.0, v205
	v_mfma_f32_32x32x16_f16 v[112:127], a[12:15], v[188:191], v[112:127]
	ds_read_b128 v[188:191], v192 offset:15360
	global_load_lds_dwordx4 v192, s[44:45] offset:2048 sc1
	v_exp_f32_e32 v207, v71
	v_add_f32_e32 v206, 1.0, v206
	s_waitcnt lgkmcnt(4)
	v_mfma_f32_32x32x16_f16 v[96:111], a[16:19], v[160:163], v[96:111]
	ds_read_b128 v[160:163], v192 offset:16384
	v_exp_f32_e32 v208, v72
	v_add_f32_e32 v207, 1.0, v207
	v_mfma_f32_32x32x16_f16 v[112:127], a[16:19], v[164:167], v[112:127]
	ds_read_b128 v[164:167], v192 offset:17408
	v_exp_f32_e32 v209, v73
	v_add_f32_e32 v208, 1.0, v208
	v_mfma_f32_32x32x16_f16 v[96:111], a[20:23], v[168:171], v[96:111]
	ds_read_b128 v[168:171], v192 offset:18432
	v_exp_f32_e32 v210, v74
	v_add_f32_e32 v209, 1.0, v209
	v_mfma_f32_32x32x16_f16 v[112:127], a[20:23], v[172:175], v[112:127]
	ds_read_b128 v[172:175], v192 offset:19456
	global_load_lds_dwordx4 v192, s[44:45] offset:3072 sc1
	v_exp_f32_e32 v211, v75
	v_add_f32_e32 v210, 1.0, v210
	s_waitcnt lgkmcnt(4)
	v_mfma_f32_32x32x16_f16 v[96:111], a[24:27], v[176:179], v[96:111]
	ds_read_b128 v[176:179], v192 offset:20480
	v_exp_f32_e32 v212, v76
	v_add_f32_e32 v211, 1.0, v211
	v_mfma_f32_32x32x16_f16 v[112:127], a[24:27], v[180:183], v[112:127]
	ds_read_b128 v[180:183], v192 offset:21504
	v_exp_f32_e32 v213, v77
	v_add_f32_e32 v212, 1.0, v212
	v_mfma_f32_32x32x16_f16 v[96:111], a[28:31], v[184:187], v[96:111]
	ds_read_b128 v[184:187], v192 offset:22528
	v_exp_f32_e32 v214, v78
	v_add_f32_e32 v213, 1.0, v213
	v_mfma_f32_32x32x16_f16 v[112:127], a[28:31], v[188:191], v[112:127]
	ds_read_b128 v[188:191], v192 offset:23552
	s_add_u32 s44, s34, 0x11000
	s_addc_u32 s45, s35, 0
	s_mov_b32 m0, s57
	s_nop 0
	global_load_lds_dwordx4 v192, s[44:45] sc1
	v_exp_f32_e32 v215, v79
	v_add_f32_e32 v214, 1.0, v214
	s_waitcnt lgkmcnt(4)
	v_mfma_f32_32x32x16_f16 v[96:111], a[32:35], v[160:163], v[96:111]
	ds_read_b128 v[160:163], v192 offset:24576
	v_add_f32_e32 v215, 1.0, v215
	v_rcp_f32_e32 v200, v200
	v_mfma_f32_32x32x16_f16 v[112:127], a[32:35], v[164:167], v[112:127]
	ds_read_b128 v[164:167], v192 offset:25600
	v_rcp_f32_e32 v201, v201
	v_mfma_f32_32x32x16_f16 v[96:111], a[36:39], v[168:171], v[96:111]
	ds_read_b128 v[168:171], v192 offset:26624
	v_rcp_f32_e32 v202, v202
	v_mfma_f32_32x32x16_f16 v[112:127], a[36:39], v[172:175], v[112:127]
	ds_read_b128 v[172:175], v192 offset:27648
	global_load_lds_dwordx4 v192, s[44:45] offset:1024 sc1
	v_rcp_f32_e32 v203, v203
	s_waitcnt lgkmcnt(4)
	v_mfma_f32_32x32x16_f16 v[96:111], a[40:43], v[176:179], v[96:111]
	ds_read_b128 v[176:179], v192 offset:28672
	v_rcp_f32_e32 v204, v204
	v_mfma_f32_32x32x16_f16 v[112:127], a[40:43], v[180:183], v[112:127]
	ds_read_b128 v[180:183], v192 offset:29696
	v_rcp_f32_e32 v205, v205
	v_mul_f32_e32 v204, v204, v144
	v_mfma_f32_32x32x16_f16 v[96:111], a[44:47], v[184:187], v[96:111]
	ds_read_b128 v[184:187], v192 offset:30720
	v_rcp_f32_e32 v206, v206
	v_mul_f32_e32 v205, v205, v145
	v_mfma_f32_32x32x16_f16 v[112:127], a[44:47], v[188:191], v[112:127]
	ds_read_b128 v[188:191], v192 offset:31744
	global_load_lds_dwordx4 v192, s[44:45] offset:2048 sc1
	v_rcp_f32_e32 v207, v207
	v_mul_f32_e32 v206, v206, v146
	s_waitcnt vmcnt(10)
	s_barrier
	s_waitcnt lgkmcnt(4)
	v_mfma_f32_32x32x16_f16 v[96:111], a[48:51], v[160:163], v[96:111]
	ds_read_b128 v[160:163], v192 offset:32768
	v_rcp_f32_e32 v208, v208
	v_mul_f32_e32 v207, v207, v147
	v_mfma_f32_32x32x16_f16 v[112:127], a[48:51], v[164:167], v[112:127]
	ds_read_b128 v[164:167], v192 offset:33792
	v_rcp_f32_e32 v209, v209
	v_fmamk_f32 v208, v208, 0xc0b8aa3b, v198
	v_mfma_f32_32x32x16_f16 v[96:111], a[52:55], v[168:171], v[96:111]
	ds_read_b128 v[168:171], v192 offset:34816
	v_rcp_f32_e32 v210, v210
	v_fmamk_f32 v209, v209, 0xc0b8aa3b, v198
	v_fma_f32 v144, v200, v208, v204
	v_mfma_f32_32x32x16_f16 v[112:127], a[52:55], v[172:175], v[112:127]
	ds_read_b128 v[172:175], v192 offset:35840
	global_load_lds_dwordx4 v192, s[44:45] offset:3072 sc1
	v_rcp_f32_e32 v211, v211
	v_fmamk_f32 v210, v210, 0xc0b8aa3b, v198
	v_fma_f32 v145, v201, v209, v205
	s_waitcnt lgkmcnt(4)
	v_mfma_f32_32x32x16_f16 v[96:111], a[56:59], v[176:179], v[96:111]
	ds_read_b128 v[176:179], v192 offset:36864
	v_rcp_f32_e32 v212, v212
	v_fmamk_f32 v211, v211, 0xc0b8aa3b, v198
	v_fma_f32 v146, v202, v210, v206
	v_mfma_f32_32x32x16_f16 v[112:127], a[56:59], v[180:183], v[112:127]
	ds_read_b128 v[180:183], v192 offset:37888
	v_rcp_f32_e32 v213, v213
	v_fma_f32 v147, v203, v211, v207
	v_mfma_f32_32x32x16_f16 v[96:111], a[60:63], v[184:187], v[96:111]
	ds_read_b128 v[184:187], v192 offset:38912
	v_rcp_f32_e32 v214, v214
	v_mfma_f32_32x32x16_f16 v[112:127], a[60:63], v[188:191], v[112:127]
	ds_read_b128 v[188:191], v192 offset:39936
	s_add_u32 s44, s34, 0x18000
	s_addc_u32 s45, s35, 0
	s_mov_b32 m0, s58
	s_nop 0
	global_load_lds_dwordx4 v192, s[44:45] sc1
	v_rcp_f32_e32 v215, v215
	s_waitcnt lgkmcnt(4)
	v_mfma_f32_32x32x16_f16 v[96:111], a[64:67], v[160:163], v[96:111]
	ds_read_b128 v[160:163], v192 offset:40960
	v_exp_f32_e32 v200, v144
	v_mfma_f32_32x32x16_f16 v[112:127], a[64:67], v[164:167], v[112:127]
	ds_read_b128 v[164:167], v192 offset:41984
	v_exp_f32_e32 v201, v145
	v_add_f32_e32 v200, 1.0, v200
	v_mfma_f32_32x32x16_f16 v[96:111], a[68:71], v[168:171], v[96:111]
	ds_read_b128 v[168:171], v192 offset:43008
	v_exp_f32_e32 v202, v146
	v_add_f32_e32 v201, 1.0, v201
	v_mfma_f32_32x32x16_f16 v[112:127], a[68:71], v[172:175], v[112:127]
	ds_read_b128 v[172:175], v192 offset:44032
	global_load_lds_dwordx4 v192, s[44:45] offset:1024 sc1
	v_exp_f32_e32 v203, v147
	v_add_f32_e32 v202, 1.0, v202
	s_waitcnt lgkmcnt(4)
	v_mfma_f32_32x32x16_f16 v[96:111], a[72:75], v[176:179], v[96:111]
	ds_read_b128 v[176:179], v192 offset:45056
	v_add_f32_e32 v203, 1.0, v203
	v_rcp_f32_e32 v200, v200
	v_mfma_f32_32x32x16_f16 v[112:127], a[72:75], v[180:183], v[112:127]
	ds_read_b128 v[180:183], v192 offset:46080
	v_rcp_f32_e32 v201, v201
	v_fma_f32 v200, v200, 2.0, -1.0
	v_mfma_f32_32x32x16_f16 v[96:111], a[76:79], v[184:187], v[96:111]
	ds_read_b128 v[184:187], v192 offset:47104
	v_rcp_f32_e32 v202, v202
	v_fma_f32 v201, v201, 2.0, -1.0
	v_mul_f32_e32 v216, v212, v200
	v_mfma_f32_32x32x16_f16 v[112:127], a[76:79], v[188:191], v[112:127]
	ds_read_b128 v[188:191], v192 offset:48128
	global_load_lds_dwordx4 v192, s[44:45] offset:2048 sc1
	v_rcp_f32_e32 v203, v203
	v_fma_f32 v202, v202, 2.0, -1.0
	v_mul_f32_e32 v217, v213, v201
	s_waitcnt lgkmcnt(4)
	v_mfma_f32_32x32x16_f16 v[96:111], a[80:83], v[160:163], v[96:111]
	ds_read_b128 v[160:163], v192 offset:49152
	v_fma_f32 v203, v203, 2.0, -1.0
	v_mul_f32_e32 v218, v214, v202
	v_exp_f32_e32 v200, v80
	v_mfma_f32_32x32x16_f16 v[112:127], a[80:83], v[164:167], v[112:127]
	ds_read_b128 v[164:167], v192 offset:50176
	v_mul_f32_e32 v219, v215, v203
	v_cvt_pk_f16_f32 v220, v216, v217
	v_exp_f32_e32 v201, v81
	v_mfma_f32_32x32x16_f16 v[96:111], a[84:87], v[168:171], v[96:111]
	ds_read_b128 v[168:171], v192 offset:51200
	v_cvt_pk_f16_f32 v221, v218, v219
	v_exp_f32_e32 v202, v82
	v_add_f32_e32 v200, 1.0, v200
	v_mfma_f32_32x32x16_f16 v[112:127], a[84:87], v[172:175], v[112:127]
	ds_read_b128 v[172:175], v192 offset:52224
	global_load_lds_dwordx4 v192, s[44:45] offset:3072 sc1
	s_cmp_lg_u32 s33, s60
	s_cbranch_scc1 .LE_nht42
	s_add_u32 s46, s62, 0x80000
	s_addc_u32 s47, s63, 0
	global_store_dwordx4 v250, v[216:219], s[46:47]
	s_waitcnt vmcnt(0)
.LE_nht42:
	v_exp_f32_e32 v203, v83
	s_waitcnt lgkmcnt(4)
	v_mfma_f32_32x32x16_f16 v[96:111], a[88:91], v[176:179], v[96:111]
	ds_read_b128 v[176:179], v192 offset:53248
	v_exp_f32_e32 v204, v84
	v_add_f32_e32 v201, 1.0, v201
	v_add_f32_e32 v202, 1.0, v202
	v_mfma_f32_32x32x16_f16 v[112:127], a[88:91], v[180:183], v[112:127]
	ds_read_b128 v[180:183], v192 offset:54272
	v_exp_f32_e32 v205, v85
	v_add_f32_e32 v203, 1.0, v203
	v_add_f32_e32 v204, 1.0, v204
	v_mfma_f32_32x32x16_f16 v[96:111], a[92:95], v[184:187], v[96:111]
	ds_read_b128 v[184:187], v192 offset:55296
	v_exp_f32_e32 v206, v86
	v_add_f32_e32 v205, 1.0, v205
	v_mfma_f32_32x32x16_f16 v[112:127], a[92:95], v[188:191], v[112:127]
	ds_read_b128 v[188:191], v192 offset:56320
	s_add_u32 s44, s34, 0x19000
	s_addc_u32 s45, s35, 0
	s_mov_b32 m0, s59
	s_nop 0
	global_load_lds_dwordx4 v192, s[44:45] sc1
	v_exp_f32_e32 v207, v87
	v_add_f32_e32 v206, 1.0, v206
	s_waitcnt lgkmcnt(4)
	v_mfma_f32_32x32x16_f16 v[96:111], a[96:99], v[160:163], v[96:111]
	ds_read_b128 v[160:163], v192 offset:57344
	v_exp_f32_e32 v208, v88
	v_add_f32_e32 v207, 1.0, v207
	v_mfma_f32_32x32x16_f16 v[112:127], a[96:99], v[164:167], v[112:127]
	ds_read_b128 v[164:167], v192 offset:58368
	v_exp_f32_e32 v209, v89
	v_add_f32_e32 v208, 1.0, v208
	v_mfma_f32_32x32x16_f16 v[96:111], a[100:103], v[168:171], v[96:111]
	ds_read_b128 v[168:171], v192 offset:59392
	v_exp_f32_e32 v210, v90
	v_add_f32_e32 v209, 1.0, v209
	v_mfma_f32_32x32x16_f16 v[112:127], a[100:103], v[172:175], v[112:127]
	ds_read_b128 v[172:175], v192 offset:60416
	global_load_lds_dwordx4 v192, s[44:45] offset:1024 sc1
	v_exp_f32_e32 v211, v91
	v_add_f32_e32 v210, 1.0, v210
	s_waitcnt lgkmcnt(4)
	v_mfma_f32_32x32x16_f16 v[96:111], a[104:107], v[176:179], v[96:111]
	ds_read_b128 v[176:179], v192 offset:61440
	v_exp_f32_e32 v212, v92
	v_add_f32_e32 v211, 1.0, v211
	v_mfma_f32_32x32x16_f16 v[112:127], a[104:107], v[180:183], v[112:127]
	ds_read_b128 v[180:183], v192 offset:62464
	v_exp_f32_e32 v213, v93
	v_add_f32_e32 v212, 1.0, v212
	v_mfma_f32_32x32x16_f16 v[96:111], a[108:111], v[184:187], v[96:111]
	ds_read_b128 v[184:187], v192 offset:63488
	v_exp_f32_e32 v214, v94
	v_add_f32_e32 v213, 1.0, v213
	v_mfma_f32_32x32x16_f16 v[112:127], a[108:111], v[188:191], v[112:127]
	ds_read_b128 v[188:191], v192 offset:64512
	global_load_lds_dwordx4 v192, s[44:45] offset:2048 sc1
	v_exp_f32_e32 v215, v95
	v_add_f32_e32 v214, 1.0, v214
	s_waitcnt vmcnt(7)
	s_barrier
	s_waitcnt lgkmcnt(4)
	v_mfma_f32_32x32x16_f16 v[96:111], a[112:115], v[160:163], v[96:111]
	ds_read_b128 v[160:163], v193 offset:0
	v_add_f32_e32 v215, 1.0, v215
	v_rcp_f32_e32 v200, v200
	v_mfma_f32_32x32x16_f16 v[112:127], a[112:115], v[164:167], v[112:127]
	ds_read_b128 v[164:167], v193 offset:1024
	v_rcp_f32_e32 v201, v201
	v_mfma_f32_32x32x16_f16 v[96:111], a[116:119], v[168:171], v[96:111]
	ds_read_b128 v[168:171], v193 offset:2048
	v_rcp_f32_e32 v202, v202
	v_mfma_f32_32x32x16_f16 v[112:127], a[116:119], v[172:175], v[112:127]
	ds_read_b128 v[172:175], v193 offset:3072
	global_load_lds_dwordx4 v192, s[44:45] offset:3072 sc1
	v_rcp_f32_e32 v203, v203
	s_waitcnt lgkmcnt(4)
	v_mfma_f32_32x32x16_f16 v[96:111], a[120:123], v[176:179], v[96:111]
	ds_read_b128 v[176:179], v193 offset:4096
	v_rcp_f32_e32 v204, v204
	ds_read_b128 v[236:239], v248 offset:0
	ds_read_b64 v[240:241], v248 offset:32
	ds_read_b128 v[242:245], v248 offset:16
	ds_read_b64 v[246:247], v248 offset:40
	v_mfma_f32_32x32x16_f16 v[112:127], a[120:123], v[180:183], v[112:127]
	ds_read_b128 v[180:183], v193 offset:5120
	v_rcp_f32_e32 v205, v205
	v_mul_f32_e32 v204, v204, v148
	s_waitcnt lgkmcnt(3)
	v_fma_f32 v32, v229, v237, v240
	v_mfma_f32_32x32x16_f16 v[96:111], a[124:127], v[184:187], v[96:111]
	ds_read_b128 v[184:187], v193 offset:6144
	v_rcp_f32_e32 v206, v206
	v_mul_f32_e32 v205, v205, v149
	v_fma_f32 v33, v229, v239, v241
	v_fmac_f32_e32 v32, v228, v236
	v_mfma_f32_32x32x16_f16 v[112:127], a[124:127], v[188:191], v[112:127]
	ds_read_b128 v[188:191], v193 offset:7168
	v_cmp_gt_u32_e32 vcc, 1, v251
	s_cbranch_vccz .LE_tok43

.LD_loop16:
	s_sub_u32 s71, s33, 1
	s_add_u32 s61, s33, 1
	s_min_u32 s61, s61, s60
	s_and_b32 s64, s71, 1
	s_lshl_b32 s64, s64, 22
	s_add_u32 s64, s64, s50
	s_add_u32 s64, s64, 0x60000
	s_add_u32 s36, s6, s64
	s_addc_u32 s37, s7, 0
	s_lshl_b32 s64, s71, 3
	s_add_u32 s64, s64, s29
	s_lshl_b32 s64, s64, 5
	s_add_u32 s64, s64, s30
	s_lshl_b32 s64, s64, 2
	s_add_u32 s40, s8, s64
	s_addc_u32 s41, s9, 0
	s_lshl_b32 s64, s71, 19
	s_add_u32 s64, s64, 0x600
	s_add_u32 s72, s62, s64
	s_addc_u32 s73, s63, 0
	s_nop 3
	s_waitcnt lgkmcnt(4)
	v_mfma_f32_32x32x16_f16 v[0:15], a[0:3], v[160:163], v[0:15]
	ds_read_b128 v[160:163], v192 offset:8192
	v_exp_f32_e32 v200, v96
	v_mfma_f32_32x32x16_f16 v[16:31], a[0:3], v[164:167], v[16:31]
	ds_read_b128 v[164:167], v192 offset:9216
	s_lshl_b32 s64, s71, 3
	s_add_u32 s64, s64, s29
	s_lshl_b32 s64, s64, 7
	s_add_u32 s38, s8, s64
	s_addc_u32 s39, s9, 0
	global_load_dword v251, v196, s[38:39] sc1
	v_exp_f32_e32 v201, v97
	v_add_f32_e32 v200, 1.0, v200
	v_mfma_f32_32x32x16_f16 v[0:15], a[4:7], v[168:171], v[0:15]
	ds_read_b128 v[168:171], v192 offset:10240
	v_exp_f32_e32 v202, v98
	v_add_f32_e32 v201, 1.0, v201
	v_mfma_f32_32x32x16_f16 v[16:31], a[4:7], v[172:175], v[16:31]
	ds_read_b128 v[172:175], v192 offset:11264
	global_load_lds_dwordx4 v192, s[44:45] offset:1024 sc1
	v_exp_f32_e32 v203, v99
	v_add_f32_e32 v202, 1.0, v202
	s_waitcnt lgkmcnt(4)
	v_mfma_f32_32x32x16_f16 v[0:15], a[8:11], v[176:179], v[0:15]
	ds_read_b128 v[176:179], v192 offset:12288
	v_exp_f32_e32 v204, v100
	v_add_f32_e32 v203, 1.0, v203
	v_mfma_f32_32x32x16_f16 v[16:31], a[8:11], v[180:183], v[16:31]
	ds_read_b128 v[180:183], v192 offset:13312
	v_exp_f32_e32 v205, v101
	v_add_f32_e32 v204, 1.0, v204
	v_mfma_f32_32x32x16_f16 v[0:15], a[12:15], v[184:187], v[0:15]
	ds_read_b128 v[184:187], v192 offset:14336
	v_exp_f32_e32 v206, v102
	v_add_f32_e32 v205, 1.0, v205
	v_mfma_f32_32x32x16_f16 v[16:31], a[12:15], v[188:191], v[16:31]
	ds_read_b128 v[188:191], v192 offset:15360
	global_load_lds_dwordx4 v192, s[44:45] offset:2048 sc1
	v_exp_f32_e32 v207, v103
	v_add_f32_e32 v206, 1.0, v206
	s_waitcnt lgkmcnt(4)
	v_mfma_f32_32x32x16_f16 v[0:15], a[16:19], v[160:163], v[0:15]
	ds_read_b128 v[160:163], v192 offset:16384
	v_exp_f32_e32 v208, v104
	v_add_f32_e32 v207, 1.0, v207
	v_mfma_f32_32x32x16_f16 v[16:31], a[16:19], v[164:167], v[16:31]
	ds_read_b128 v[164:167], v192 offset:17408
	v_exp_f32_e32 v209, v105
	v_add_f32_e32 v208, 1.0, v208
	v_mfma_f32_32x32x16_f16 v[0:15], a[20:23], v[168:171], v[0:15]
	ds_read_b128 v[168:171], v192 offset:18432
	v_exp_f32_e32 v210, v106
	v_add_f32_e32 v209, 1.0, v209
	v_mfma_f32_32x32x16_f16 v[16:31], a[20:23], v[172:175], v[16:31]
	ds_read_b128 v[172:175], v192 offset:19456
	global_load_lds_dwordx4 v192, s[44:45] offset:3072 sc1
	v_exp_f32_e32 v211, v107
	v_add_f32_e32 v210, 1.0, v210
	s_waitcnt lgkmcnt(4)
	v_mfma_f32_32x32x16_f16 v[0:15], a[24:27], v[176:179], v[0:15]
	ds_read_b128 v[176:179], v192 offset:20480
	v_exp_f32_e32 v212, v108
	v_add_f32_e32 v211, 1.0, v211
	v_mfma_f32_32x32x16_f16 v[16:31], a[24:27], v[180:183], v[16:31]
	ds_read_b128 v[180:183], v192 offset:21504
	v_exp_f32_e32 v213, v109
	v_add_f32_e32 v212, 1.0, v212
	v_mfma_f32_32x32x16_f16 v[0:15], a[28:31], v[184:187], v[0:15]
	ds_read_b128 v[184:187], v192 offset:22528
	v_exp_f32_e32 v214, v110
	v_add_f32_e32 v213, 1.0, v213
	v_mfma_f32_32x32x16_f16 v[16:31], a[28:31], v[188:191], v[16:31]
	ds_read_b128 v[188:191], v192 offset:23552
	s_add_u32 s44, s34, 0x11000
	s_addc_u32 s45, s35, 0
	s_mov_b32 m0, s57
	s_nop 0
	global_load_lds_dwordx4 v192, s[44:45] sc1
	v_exp_f32_e32 v215, v111
	v_add_f32_e32 v214, 1.0, v214
	s_waitcnt lgkmcnt(4)
	v_mfma_f32_32x32x16_f16 v[0:15], a[32:35], v[160:163], v[0:15]
	ds_read_b128 v[160:163], v192 offset:24576
	v_add_f32_e32 v215, 1.0, v215
	v_rcp_f32_e32 v200, v200
	v_mfma_f32_32x32x16_f16 v[16:31], a[32:35], v[164:167], v[16:31]
	ds_read_b128 v[164:167], v192 offset:25600
	v_rcp_f32_e32 v201, v201
	v_mfma_f32_32x32x16_f16 v[0:15], a[36:39], v[168:171], v[0:15]
	ds_read_b128 v[168:171], v192 offset:26624
	v_rcp_f32_e32 v202, v202
	v_mfma_f32_32x32x16_f16 v[16:31], a[36:39], v[172:175], v[16:31]
	ds_read_b128 v[172:175], v192 offset:27648
	global_load_lds_dwordx4 v192, s[44:45] offset:1024 sc1
	v_rcp_f32_e32 v203, v203
	s_waitcnt lgkmcnt(4)
	v_mfma_f32_32x32x16_f16 v[0:15], a[40:43], v[176:179], v[0:15]
	ds_read_b128 v[176:179], v192 offset:28672
	v_rcp_f32_e32 v204, v204
	v_mfma_f32_32x32x16_f16 v[16:31], a[40:43], v[180:183], v[16:31]
	ds_read_b128 v[180:183], v192 offset:29696
	v_rcp_f32_e32 v205, v205
	v_mul_f32_e32 v204, v204, v152
	v_mfma_f32_32x32x16_f16 v[0:15], a[44:47], v[184:187], v[0:15]
	ds_read_b128 v[184:187], v192 offset:30720
	v_rcp_f32_e32 v206, v206
	v_mul_f32_e32 v205, v205, v153
	v_mfma_f32_32x32x16_f16 v[16:31], a[44:47], v[188:191], v[16:31]
	ds_read_b128 v[188:191], v192 offset:31744
	global_load_lds_dwordx4 v192, s[44:45] offset:2048 sc1
	v_rcp_f32_e32 v207, v207
	v_mul_f32_e32 v206, v206, v154
	s_waitcnt vmcnt(8)
	s_barrier
	s_waitcnt lgkmcnt(4)
	v_mfma_f32_32x32x16_f16 v[0:15], a[48:51], v[160:163], v[0:15]
	ds_read_b128 v[160:163], v192 offset:32768
	v_rcp_f32_e32 v208, v208
	v_mul_f32_e32 v207, v207, v155
	v_mfma_f32_32x32x16_f16 v[16:31], a[48:51], v[164:167], v[16:31]
	ds_read_b128 v[164:167], v192 offset:33792
	v_rcp_f32_e32 v209, v209
	v_fmamk_f32 v208, v208, 0xc0b8aa3b, v198
	v_mfma_f32_32x32x16_f16 v[0:15], a[52:55], v[168:171], v[0:15]
	ds_read_b128 v[168:171], v192 offset:34816
	v_rcp_f32_e32 v210, v210
	v_fmamk_f32 v209, v209, 0xc0b8aa3b, v198
	v_fma_f32 v152, v200, v208, v204
	v_mfma_f32_32x32x16_f16 v[16:31], a[52:55], v[172:175], v[16:31]
	ds_read_b128 v[172:175], v192 offset:35840
	global_load_lds_dwordx4 v192, s[44:45] offset:3072 sc1
	v_rcp_f32_e32 v211, v211
	v_fmamk_f32 v210, v210, 0xc0b8aa3b, v198
	v_fma_f32 v153, v201, v209, v205
	s_waitcnt lgkmcnt(4)
	v_mfma_f32_32x32x16_f16 v[0:15], a[56:59], v[176:179], v[0:15]
	ds_read_b128 v[176:179], v192 offset:36864
	v_rcp_f32_e32 v212, v212
	v_fmamk_f32 v211, v211, 0xc0b8aa3b, v198
	v_fma_f32 v154, v202, v210, v206
	v_mfma_f32_32x32x16_f16 v[16:31], a[56:59], v[180:183], v[16:31]
	ds_read_b128 v[180:183], v192 offset:37888
	v_rcp_f32_e32 v213, v213
	v_fma_f32 v155, v203, v211, v207
	v_mfma_f32_32x32x16_f16 v[0:15], a[60:63], v[184:187], v[0:15]
	ds_read_b128 v[184:187], v192 offset:38912
	v_rcp_f32_e32 v214, v214
	v_mfma_f32_32x32x16_f16 v[16:31], a[60:63], v[188:191], v[16:31]
	ds_read_b128 v[188:191], v192 offset:39936
	s_add_u32 s44, s34, 0x18000
	s_addc_u32 s45, s35, 0
	s_mov_b32 m0, s58
	s_nop 0
	global_load_lds_dwordx4 v192, s[44:45] sc1
	v_rcp_f32_e32 v215, v215
	s_waitcnt lgkmcnt(4)
	v_mfma_f32_32x32x16_f16 v[0:15], a[64:67], v[160:163], v[0:15]
	ds_read_b128 v[160:163], v192 offset:40960
	v_exp_f32_e32 v200, v152
	v_mfma_f32_32x32x16_f16 v[16:31], a[64:67], v[164:167], v[16:31]
	ds_read_b128 v[164:167], v192 offset:41984
	v_exp_f32_e32 v201, v153
	v_add_f32_e32 v200, 1.0, v200
	v_mfma_f32_32x32x16_f16 v[0:15], a[68:71], v[168:171], v[0:15]
	ds_read_b128 v[168:171], v192 offset:43008
	v_exp_f32_e32 v202, v154
	v_add_f32_e32 v201, 1.0, v201
	v_mfma_f32_32x32x16_f16 v[16:31], a[68:71], v[172:175], v[16:31]
	ds_read_b128 v[172:175], v192 offset:44032
	global_load_lds_dwordx4 v192, s[44:45] offset:1024 sc1
	v_exp_f32_e32 v203, v155
	v_add_f32_e32 v202, 1.0, v202
	s_waitcnt lgkmcnt(4)
	v_mfma_f32_32x32x16_f16 v[0:15], a[72:75], v[176:179], v[0:15]
	ds_read_b128 v[176:179], v192 offset:45056
	v_add_f32_e32 v203, 1.0, v203
	v_rcp_f32_e32 v200, v200
	v_mfma_f32_32x32x16_f16 v[16:31], a[72:75], v[180:183], v[16:31]
	ds_read_b128 v[180:183], v192 offset:46080
	v_rcp_f32_e32 v201, v201
	v_fma_f32 v200, v200, 2.0, -1.0
	v_mfma_f32_32x32x16_f16 v[0:15], a[76:79], v[184:187], v[0:15]
	ds_read_b128 v[184:187], v192 offset:47104
	v_rcp_f32_e32 v202, v202
	v_fma_f32 v201, v201, 2.0, -1.0
	v_mul_f32_e32 v216, v212, v200
	v_mfma_f32_32x32x16_f16 v[16:31], a[76:79], v[188:191], v[16:31]
	ds_read_b128 v[188:191], v192 offset:48128
	global_load_lds_dwordx4 v192, s[44:45] offset:2048 sc1
	v_rcp_f32_e32 v203, v203
	v_fma_f32 v202, v202, 2.0, -1.0
	v_mul_f32_e32 v217, v213, v201
	s_waitcnt lgkmcnt(4)
	v_mfma_f32_32x32x16_f16 v[0:15], a[80:83], v[160:163], v[0:15]
	ds_read_b128 v[160:163], v192 offset:49152
	v_fma_f32 v203, v203, 2.0, -1.0
	v_mul_f32_e32 v218, v214, v202
	v_exp_f32_e32 v200, v112
	v_mfma_f32_32x32x16_f16 v[16:31], a[80:83], v[164:167], v[16:31]
	ds_read_b128 v[164:167], v192 offset:50176
	v_mul_f32_e32 v219, v215, v203
	v_mul_f32_e32 v236, v216, v228
	v_exp_f32_e32 v201, v113
	v_mfma_f32_32x32x16_f16 v[0:15], a[84:87], v[168:171], v[0:15]
	ds_read_b128 v[168:171], v192 offset:51200
	v_mul_f32_e32 v237, v216, v232
	v_fmac_f32_e32 v236, v217, v229
	v_exp_f32_e32 v202, v114
	v_mfma_f32_32x32x16_f16 v[16:31], a[84:87], v[172:175], v[16:31]
	ds_read_b128 v[172:175], v192 offset:52224
	global_load_lds_dwordx4 v192, s[44:45] offset:3072 sc1
	v_fmac_f32_e32 v237, v217, v233
	v_fmac_f32_e32 v236, v218, v230
	v_exp_f32_e32 v203, v115
	s_waitcnt lgkmcnt(4)
	v_mfma_f32_32x32x16_f16 v[0:15], a[88:91], v[176:179], v[0:15]
	ds_read_b128 v[176:179], v192 offset:53248
	v_fmac_f32_e32 v237, v218, v234
	v_fmac_f32_e32 v236, v219, v231
	v_exp_f32_e32 v204, v116
	v_mfma_f32_32x32x16_f16 v[16:31], a[88:91], v[180:183], v[16:31]
	ds_read_b128 v[180:183], v192 offset:54272
	v_fmac_f32_e32 v237, v219, v235
	v_mov_b32_e32 v238, v236
	v_exp_f32_e32 v205, v117
	v_mfma_f32_32x32x16_f16 v[0:15], a[92:95], v[184:187], v[0:15]
	ds_read_b128 v[184:187], v192 offset:55296
	v_mov_b32_e32 v239, v236
	v_mov_b32_e32 v240, v237
	v_exp_f32_e32 v206, v118
	v_mfma_f32_32x32x16_f16 v[16:31], a[92:95], v[188:191], v[16:31]
	ds_read_b128 v[188:191], v192 offset:56320
	s_add_u32 s44, s34, 0x19000
	s_addc_u32 s45, s35, 0
	s_mov_b32 m0, s59
	s_nop 0
	global_load_lds_dwordx4 v192, s[44:45] sc1
	v_mov_b32_e32 v241, v237
	v_cvt_pk_f16_f32 v220, v216, v217
	v_exp_f32_e32 v207, v119
	s_waitcnt lgkmcnt(4)
	v_mfma_f32_32x32x16_f16 v[0:15], a[96:99], v[160:163], v[0:15]
	ds_read_b128 v[160:163], v192 offset:57344
	s_nop 1
	v_permlane32_swap_b32_e32 v238, v239
	v_permlane32_swap_b32_e32 v240, v241
	v_add_f32_e32 v238, v238, v239
	v_add_f32_e32 v239, v240, v241
	ds_write_b64 v248, v[238:239] offset:1536
	v_exp_f32_e32 v208, v120
	v_mfma_f32_32x32x16_f16 v[16:31], a[96:99], v[164:167], v[16:31]
	ds_read_b128 v[164:167], v192 offset:58368
	v_cvt_pk_f16_f32 v221, v218, v219
	v_exp_f32_e32 v209, v121
	v_add_f32_e32 v200, 1.0, v200
	v_mfma_f32_32x32x16_f16 v[0:15], a[100:103], v[168:171], v[0:15]
	ds_read_b128 v[168:171], v192 offset:59392
	v_exp_f32_e32 v210, v122
	v_add_f32_e32 v201, 1.0, v201
	v_add_f32_e32 v202, 1.0, v202
	v_mfma_f32_32x32x16_f16 v[16:31], a[100:103], v[172:175], v[16:31]
	ds_read_b128 v[172:175], v192 offset:60416
	global_load_lds_dwordx4 v192, s[44:45] offset:1024 sc1
	v_exp_f32_e32 v211, v123
	v_add_f32_e32 v203, 1.0, v203
	v_add_f32_e32 v204, 1.0, v204
	s_waitcnt lgkmcnt(5)
	v_mfma_f32_32x32x16_f16 v[0:15], a[104:107], v[176:179], v[0:15]
	ds_read_b128 v[176:179], v192 offset:61440
	v_exp_f32_e32 v212, v124
	v_add_f32_e32 v205, 1.0, v205
	v_add_f32_e32 v206, 1.0, v206
	v_mfma_f32_32x32x16_f16 v[16:31], a[104:107], v[180:183], v[16:31]
	ds_read_b128 v[180:183], v192 offset:62464
	v_exp_f32_e32 v213, v125
	v_add_f32_e32 v207, 1.0, v207
	v_add_f32_e32 v208, 1.0, v208
	v_mfma_f32_32x32x16_f16 v[0:15], a[108:111], v[184:187], v[0:15]
	ds_read_b128 v[184:187], v192 offset:63488
	v_exp_f32_e32 v214, v126
	v_add_f32_e32 v209, 1.0, v209
	v_add_f32_e32 v210, 1.0, v210
	v_mfma_f32_32x32x16_f16 v[16:31], a[108:111], v[188:191], v[16:31]
	ds_read_b128 v[188:191], v192 offset:64512
	global_load_lds_dwordx4 v192, s[44:45] offset:2048 sc1
	v_exp_f32_e32 v215, v127
	v_add_f32_e32 v211, 1.0, v211
	v_add_f32_e32 v212, 1.0, v212
	s_waitcnt vmcnt(7)
	s_barrier
	s_waitcnt lgkmcnt(4)
	v_mfma_f32_32x32x16_f16 v[0:15], a[112:115], v[160:163], v[0:15]
	ds_read_b128 v[160:163], v193 offset:0
	v_add_f32_e32 v213, 1.0, v213
	v_add_f32_e32 v214, 1.0, v214
	v_rcp_f32_e32 v200, v200
	v_mfma_f32_32x32x16_f16 v[16:31], a[112:115], v[164:167], v[16:31]
	ds_read_b128 v[164:167], v193 offset:1024
	v_add_f32_e32 v215, 1.0, v215
	v_rcp_f32_e32 v201, v201
	v_mfma_f32_32x32x16_f16 v[0:15], a[116:119], v[168:171], v[0:15]
	ds_read_b128 v[168:171], v193 offset:2048
	v_rcp_f32_e32 v202, v202
	v_mfma_f32_32x32x16_f16 v[16:31], a[116:119], v[172:175], v[16:31]
	ds_read_b128 v[172:175], v193 offset:3072
	global_load_lds_dwordx4 v192, s[44:45] offset:3072 sc1
	v_rcp_f32_e32 v203, v203
	s_waitcnt lgkmcnt(4)
	v_mfma_f32_32x32x16_f16 v[0:15], a[120:123], v[176:179], v[0:15]
	ds_read_b128 v[176:179], v193 offset:4096
	v_rcp_f32_e32 v204, v204
	s_add_u32 s46, s42, 0x4000
	s_addc_u32 s47, s43, 0
	global_load_dwordx4 v[64:67], v192, s[46:47] offset:0
	v_mfma_f32_32x32x16_f16 v[16:31], a[120:123], v[180:183], v[16:31]
	ds_read_b128 v[180:183], v193 offset:5120
	v_rcp_f32_e32 v205, v205
	v_mul_f32_e32 v204, v204, v156
	global_load_dwordx4 v[68:71], v192, s[46:47] offset:1024
	global_load_dwordx4 v[72:75], v192, s[46:47] offset:2048
	v_mfma_f32_32x32x16_f16 v[0:15], a[124:127], v[184:187], v[0:15]
	ds_read_b128 v[184:187], v193 offset:6144
	v_rcp_f32_e32 v206, v206
	v_mul_f32_e32 v205, v205, v157
	global_load_dwordx4 v[76:79], v192, s[46:47] offset:3072
	s_add_u32 s46, s42, 0x5000
	s_addc_u32 s47, s43, 0
	v_mfma_f32_32x32x16_f16 v[16:31], a[124:127], v[188:191], v[16:31]
	ds_read_b128 v[188:191], v193 offset:7168
	v_cmp_gt_u32_e32 vcc, 2, v251
	s_cbranch_vccz .LD_tok20

.LD_join25:
	ds_read_b64 v[200:201], v249 offset:1536
	ds_read_b64 v[202:203], v249 offset:3584
	ds_read_b64 v[204:205], v249 offset:5632
	ds_read_b64 v[206:207], v249 offset:7680
	s_waitcnt lgkmcnt(8)
	v_mfma_f32_32x32x16_f16 v[0:15], a[208:211], v[160:163], v[0:15]
	ds_read_b128 v[160:163], v193 offset:49152
	v_mfma_f32_32x32x16_f16 v[16:31], a[208:211], v[164:167], v[16:31]
	ds_read_b128 v[164:167], v193 offset:50176
	v_mfma_f32_32x32x16_f16 v[0:15], a[212:215], v[168:171], v[0:15]
	ds_read_b128 v[168:171], v193 offset:51200
	v_mfma_f32_32x32x16_f16 v[16:31], a[212:215], v[172:175], v[16:31]
	ds_read_b128 v[172:175], v193 offset:52224
	global_load_lds_dwordx4 v192, s[44:45] offset:3072 sc1
	s_waitcnt lgkmcnt(8)
	v_mfma_f32_32x32x16_f16 v[0:15], a[216:219], v[176:179], v[0:15]
	ds_read_b128 v[176:179], v193 offset:53248
	v_mfma_f32_32x32x16_f16 v[16:31], a[216:219], v[180:183], v[16:31]
	ds_read_b128 v[180:183], v193 offset:54272
	v_mfma_f32_32x32x16_f16 v[0:15], a[220:223], v[184:187], v[0:15]
	ds_read_b128 v[184:187], v193 offset:55296
	v_mfma_f32_32x32x16_f16 v[16:31], a[220:223], v[188:191], v[16:31]
	ds_read_b128 v[188:191], v193 offset:56320
	s_add_u32 s44, s34, 0x9000
	s_addc_u32 s45, s35, 0
	s_mov_b32 m0, s55
	s_nop 0
	global_load_lds_dwordx4 v192, s[44:45] sc1
	s_waitcnt lgkmcnt(4)
	v_mfma_f32_32x32x16_f16 v[0:15], a[224:227], v[160:163], v[0:15]
	ds_read_b128 v[160:163], v193 offset:57344
	v_mfma_f32_32x32x16_f16 v[16:31], a[224:227], v[164:167], v[16:31]
	ds_read_b128 v[164:167], v193 offset:58368
	v_mfma_f32_32x32x16_f16 v[0:15], a[228:231], v[168:171], v[0:15]
	ds_read_b128 v[168:171], v193 offset:59392
	v_mfma_f32_32x32x16_f16 v[16:31], a[228:231], v[172:175], v[16:31]
	ds_read_b128 v[172:175], v193 offset:60416
	global_load_lds_dwordx4 v192, s[44:45] offset:1024 sc1
	v_add_f32_e32 v200, v200, v202
	v_add_f32_e32 v201, v201, v203
	v_add_f32_e32 v200, v200, v204
	v_add_f32_e32 v201, v201, v205
	v_add_f32_e32 v200, v200, v206
	v_add_f32_e32 v201, v201, v207
	global_store_dwordx2 v250, v[200:201], s[72:73]
	s_waitcnt lgkmcnt(4)
	v_mfma_f32_32x32x16_f16 v[0:15], a[232:235], v[176:179], v[0:15]
	ds_read_b128 v[176:179], v193 offset:61440
	v_mfma_f32_32x32x16_f16 v[16:31], a[232:235], v[180:183], v[16:31]
	ds_read_b128 v[180:183], v193 offset:62464
	v_mfma_f32_32x32x16_f16 v[0:15], a[236:239], v[184:187], v[0:15]
	ds_read_b128 v[184:187], v193 offset:63488
	v_mfma_f32_32x32x16_f16 v[16:31], a[236:239], v[188:191], v[16:31]
	ds_read_b128 v[188:191], v193 offset:64512
	global_load_lds_dwordx4 v192, s[44:45] offset:2048 sc1
	s_waitcnt vmcnt(9)
	s_barrier
	s_waitcnt lgkmcnt(4)
	v_mfma_f32_32x32x16_f16 v[0:15], a[240:243], v[160:163], v[0:15]
	ds_read_b128 v[160:163], v192 offset:0
	v_mfma_f32_32x32x16_f16 v[16:31], a[240:243], v[164:167], v[16:31]
	ds_read_b128 v[164:167], v192 offset:1024
	v_mfma_f32_32x32x16_f16 v[0:15], a[244:247], v[168:171], v[0:15]
	ds_read_b128 v[168:171], v192 offset:2048
	v_mfma_f32_32x32x16_f16 v[16:31], a[244:247], v[172:175], v[16:31]
	ds_read_b128 v[172:175], v192 offset:3072
	global_load_lds_dwordx4 v192, s[44:45] offset:3072 sc1
	s_waitcnt lgkmcnt(4)
	v_mfma_f32_32x32x16_f16 v[0:15], a[248:251], v[176:179], v[0:15]
	ds_read_b128 v[176:179], v192 offset:4096
	v_mfma_f32_32x32x16_f16 v[16:31], a[248:251], v[180:183], v[16:31]
	ds_read_b128 v[180:183], v192 offset:5120
	v_mfma_f32_32x32x16_f16 v[0:15], a[252:255], v[184:187], v[0:15]
	ds_read_b128 v[184:187], v192 offset:6144
	v_mfma_f32_32x32x16_f16 v[16:31], a[252:255], v[188:191], v[16:31]
	ds_read_b128 v[188:191], v192 offset:7168
	s_add_u32 s44, s34, 0x10000
	s_addc_u32 s45, s35, 0
	s_mov_b32 m0, s56
	s_nop 0
	global_load_lds_dwordx4 v192, s[44:45] sc1
	s_and_b32 s64, s33, 1
	s_lshl_b32 s64, s64, 22
	s_add_u32 s64, s64, s50
	s_add_u32 s36, s6, s64
	s_addc_u32 s37, s7, 0
	s_lshl_b32 s64, s33, 3
	s_add_u32 s64, s64, s29
	s_lshl_b32 s64, s64, 5
	s_add_u32 s64, s64, s30
	s_lshl_b32 s64, s64, 2
	s_add_u32 s40, s8, s64
	s_addc_u32 s41, s9, 0
	s_lshl_b32 s64, s33, 19
	s_add_u32 s72, s62, s64
	s_addc_u32 s73, s63, 0
	s_nop 3
	s_waitcnt lgkmcnt(4)
	v_mfma_f32_32x32x16_f16 v[32:47], a[0:3], v[160:163], v[32:47]
	ds_read_b128 v[160:163], v192 offset:8192
	v_exp_f32_e32 v200, v0
	v_mfma_f32_32x32x16_f16 v[48:63], a[0:3], v[164:167], v[48:63]
	ds_read_b128 v[164:167], v192 offset:9216
	s_lshl_b32 s64, s71, 3
	s_add_u32 s64, s64, s29
	s_lshl_b32 s64, s64, 7
	s_add_u32 s38, s8, s64
	s_addc_u32 s39, s9, 0
	global_load_dword v251, v196, s[38:39] sc1
	v_exp_f32_e32 v201, v1
	v_add_f32_e32 v200, 1.0, v200
	v_mfma_f32_32x32x16_f16 v[32:47], a[4:7], v[168:171], v[32:47]
	ds_read_b128 v[168:171], v192 offset:10240
	v_exp_f32_e32 v202, v2
	v_add_f32_e32 v201, 1.0, v201
	v_mfma_f32_32x32x16_f16 v[48:63], a[4:7], v[172:175], v[48:63]
	ds_read_b128 v[172:175], v192 offset:11264
	global_load_lds_dwordx4 v192, s[44:45] offset:1024 sc1
	v_exp_f32_e32 v203, v3
	v_add_f32_e32 v202, 1.0, v202
	s_waitcnt lgkmcnt(4)
	v_mfma_f32_32x32x16_f16 v[32:47], a[8:11], v[176:179], v[32:47]
	ds_read_b128 v[176:179], v192 offset:12288
	v_exp_f32_e32 v204, v4
	v_add_f32_e32 v203, 1.0, v203
	v_mfma_f32_32x32x16_f16 v[48:63], a[8:11], v[180:183], v[48:63]
	ds_read_b128 v[180:183], v192 offset:13312
	v_exp_f32_e32 v205, v5
	v_add_f32_e32 v204, 1.0, v204
	v_mfma_f32_32x32x16_f16 v[32:47], a[12:15], v[184:187], v[32:47]
	ds_read_b128 v[184:187], v192 offset:14336
	v_exp_f32_e32 v206, v6
	v_add_f32_e32 v205, 1.0, v205
	v_mfma_f32_32x32x16_f16 v[48:63], a[12:15], v[188:191], v[48:63]
	ds_read_b128 v[188:191], v192 offset:15360
	global_load_lds_dwordx4 v192, s[44:45] offset:2048 sc1
	v_exp_f32_e32 v207, v7
	v_add_f32_e32 v206, 1.0, v206
	s_waitcnt lgkmcnt(4)
	v_mfma_f32_32x32x16_f16 v[32:47], a[16:19], v[160:163], v[32:47]
	ds_read_b128 v[160:163], v192 offset:16384
	v_exp_f32_e32 v208, v8
	v_add_f32_e32 v207, 1.0, v207
	v_mfma_f32_32x32x16_f16 v[48:63], a[16:19], v[164:167], v[48:63]
	ds_read_b128 v[164:167], v192 offset:17408
	v_exp_f32_e32 v209, v9
	v_add_f32_e32 v208, 1.0, v208
	v_mfma_f32_32x32x16_f16 v[32:47], a[20:23], v[168:171], v[32:47]
	ds_read_b128 v[168:171], v192 offset:18432
	v_exp_f32_e32 v210, v10
	v_add_f32_e32 v209, 1.0, v209
	v_mfma_f32_32x32x16_f16 v[48:63], a[20:23], v[172:175], v[48:63]
	ds_read_b128 v[172:175], v192 offset:19456
	global_load_lds_dwordx4 v192, s[44:45] offset:3072 sc1
	v_exp_f32_e32 v211, v11
	v_add_f32_e32 v210, 1.0, v210
	s_waitcnt lgkmcnt(4)
	v_mfma_f32_32x32x16_f16 v[32:47], a[24:27], v[176:179], v[32:47]
	ds_read_b128 v[176:179], v192 offset:20480
	v_exp_f32_e32 v212, v12
	v_add_f32_e32 v211, 1.0, v211
	v_mfma_f32_32x32x16_f16 v[48:63], a[24:27], v[180:183], v[48:63]
	ds_read_b128 v[180:183], v192 offset:21504
	v_exp_f32_e32 v213, v13
	v_add_f32_e32 v212, 1.0, v212
	v_mfma_f32_32x32x16_f16 v[32:47], a[28:31], v[184:187], v[32:47]
	ds_read_b128 v[184:187], v192 offset:22528
	v_exp_f32_e32 v214, v14
	v_add_f32_e32 v213, 1.0, v213
	v_mfma_f32_32x32x16_f16 v[48:63], a[28:31], v[188:191], v[48:63]
	ds_read_b128 v[188:191], v192 offset:23552
	s_add_u32 s44, s34, 0x11000
	s_addc_u32 s45, s35, 0
	s_mov_b32 m0, s57
	s_nop 0
	global_load_lds_dwordx4 v192, s[44:45] sc1
	v_exp_f32_e32 v215, v15
	v_add_f32_e32 v214, 1.0, v214
	s_waitcnt lgkmcnt(4)
	v_mfma_f32_32x32x16_f16 v[32:47], a[32:35], v[160:163], v[32:47]
	ds_read_b128 v[160:163], v192 offset:24576
	v_add_f32_e32 v215, 1.0, v215
	v_rcp_f32_e32 v200, v200
	v_mfma_f32_32x32x16_f16 v[48:63], a[32:35], v[164:167], v[48:63]
	ds_read_b128 v[164:167], v192 offset:25600
	v_rcp_f32_e32 v201, v201
	v_mfma_f32_32x32x16_f16 v[32:47], a[36:39], v[168:171], v[32:47]
	ds_read_b128 v[168:171], v192 offset:26624
	v_rcp_f32_e32 v202, v202
	v_mfma_f32_32x32x16_f16 v[48:63], a[36:39], v[172:175], v[48:63]
	ds_read_b128 v[172:175], v192 offset:27648
	global_load_lds_dwordx4 v192, s[44:45] offset:1024 sc1
	v_rcp_f32_e32 v203, v203
	s_waitcnt lgkmcnt(4)
	v_mfma_f32_32x32x16_f16 v[32:47], a[40:43], v[176:179], v[32:47]
	ds_read_b128 v[176:179], v192 offset:28672
	v_rcp_f32_e32 v204, v204
	v_mfma_f32_32x32x16_f16 v[48:63], a[40:43], v[180:183], v[48:63]
	ds_read_b128 v[180:183], v192 offset:29696
	v_rcp_f32_e32 v205, v205
	v_mul_f32_e32 v204, v204, v128
	v_mfma_f32_32x32x16_f16 v[32:47], a[44:47], v[184:187], v[32:47]
	ds_read_b128 v[184:187], v192 offset:30720
	v_rcp_f32_e32 v206, v206
	v_mul_f32_e32 v205, v205, v129
	v_mfma_f32_32x32x16_f16 v[48:63], a[44:47], v[188:191], v[48:63]
	ds_read_b128 v[188:191], v192 offset:31744
	global_load_lds_dwordx4 v192, s[44:45] offset:2048 sc1
	v_rcp_f32_e32 v207, v207
	v_mul_f32_e32 v206, v206, v130
	s_waitcnt vmcnt(8)
	s_barrier
	s_waitcnt lgkmcnt(4)
	v_mfma_f32_32x32x16_f16 v[32:47], a[48:51], v[160:163], v[32:47]
	ds_read_b128 v[160:163], v192 offset:32768
	v_rcp_f32_e32 v208, v208
	v_mul_f32_e32 v207, v207, v131
	v_mfma_f32_32x32x16_f16 v[48:63], a[48:51], v[164:167], v[48:63]
	ds_read_b128 v[164:167], v192 offset:33792
	v_rcp_f32_e32 v209, v209
	v_fmamk_f32 v208, v208, 0xc0b8aa3b, v198
	v_mfma_f32_32x32x16_f16 v[32:47], a[52:55], v[168:171], v[32:47]
	ds_read_b128 v[168:171], v192 offset:34816
	v_rcp_f32_e32 v210, v210
	v_fmamk_f32 v209, v209, 0xc0b8aa3b, v198
	v_fma_f32 v128, v200, v208, v204
	v_mfma_f32_32x32x16_f16 v[48:63], a[52:55], v[172:175], v[48:63]
	ds_read_b128 v[172:175], v192 offset:35840
	global_load_lds_dwordx4 v192, s[44:45] offset:3072 sc1
	v_rcp_f32_e32 v211, v211
	v_fmamk_f32 v210, v210, 0xc0b8aa3b, v198
	v_fma_f32 v129, v201, v209, v205
	s_waitcnt lgkmcnt(4)
	v_mfma_f32_32x32x16_f16 v[32:47], a[56:59], v[176:179], v[32:47]
	ds_read_b128 v[176:179], v192 offset:36864
	v_rcp_f32_e32 v212, v212
	v_fmamk_f32 v211, v211, 0xc0b8aa3b, v198
	v_fma_f32 v130, v202, v210, v206
	v_mfma_f32_32x32x16_f16 v[48:63], a[56:59], v[180:183], v[48:63]
	ds_read_b128 v[180:183], v192 offset:37888
	v_rcp_f32_e32 v213, v213
	v_fma_f32 v131, v203, v211, v207
	v_mfma_f32_32x32x16_f16 v[32:47], a[60:63], v[184:187], v[32:47]
	ds_read_b128 v[184:187], v192 offset:38912
	v_rcp_f32_e32 v214, v214
	v_mfma_f32_32x32x16_f16 v[48:63], a[60:63], v[188:191], v[48:63]
	ds_read_b128 v[188:191], v192 offset:39936
	s_add_u32 s44, s34, 0x18000
	s_addc_u32 s45, s35, 0
	s_mov_b32 m0, s58
	s_nop 0
	global_load_lds_dwordx4 v192, s[44:45] sc1
	v_rcp_f32_e32 v215, v215
	s_waitcnt lgkmcnt(4)
	v_mfma_f32_32x32x16_f16 v[32:47], a[64:67], v[160:163], v[32:47]
	ds_read_b128 v[160:163], v192 offset:40960
	v_exp_f32_e32 v200, v128
	v_mfma_f32_32x32x16_f16 v[48:63], a[64:67], v[164:167], v[48:63]
	ds_read_b128 v[164:167], v192 offset:41984
	v_exp_f32_e32 v201, v129
	v_add_f32_e32 v200, 1.0, v200
	v_mfma_f32_32x32x16_f16 v[32:47], a[68:71], v[168:171], v[32:47]
	ds_read_b128 v[168:171], v192 offset:43008
	v_exp_f32_e32 v202, v130
	v_add_f32_e32 v201, 1.0, v201
	v_mfma_f32_32x32x16_f16 v[48:63], a[68:71], v[172:175], v[48:63]
	ds_read_b128 v[172:175], v192 offset:44032
	global_load_lds_dwordx4 v192, s[44:45] offset:1024 sc1
	v_exp_f32_e32 v203, v131
	v_add_f32_e32 v202, 1.0, v202
	s_waitcnt lgkmcnt(4)
	v_mfma_f32_32x32x16_f16 v[32:47], a[72:75], v[176:179], v[32:47]
	ds_read_b128 v[176:179], v192 offset:45056
	v_add_f32_e32 v203, 1.0, v203
	v_rcp_f32_e32 v200, v200
	v_mfma_f32_32x32x16_f16 v[48:63], a[72:75], v[180:183], v[48:63]
	ds_read_b128 v[180:183], v192 offset:46080
	v_rcp_f32_e32 v201, v201
	v_fma_f32 v200, v200, 2.0, -1.0
	v_mfma_f32_32x32x16_f16 v[32:47], a[76:79], v[184:187], v[32:47]
	ds_read_b128 v[184:187], v192 offset:47104
	v_rcp_f32_e32 v202, v202
	v_fma_f32 v201, v201, 2.0, -1.0
	v_mul_f32_e32 v216, v212, v200
	v_mfma_f32_32x32x16_f16 v[48:63], a[76:79], v[188:191], v[48:63]
	ds_read_b128 v[188:191], v192 offset:48128
	global_load_lds_dwordx4 v192, s[44:45] offset:2048 sc1
	v_rcp_f32_e32 v203, v203
	v_fma_f32 v202, v202, 2.0, -1.0
	v_mul_f32_e32 v217, v213, v201
	s_waitcnt lgkmcnt(4)
	v_mfma_f32_32x32x16_f16 v[32:47], a[80:83], v[160:163], v[32:47]
	ds_read_b128 v[160:163], v192 offset:49152
	v_fma_f32 v203, v203, 2.0, -1.0
	v_mul_f32_e32 v218, v214, v202
	v_exp_f32_e32 v200, v16
	v_mfma_f32_32x32x16_f16 v[48:63], a[80:83], v[164:167], v[48:63]
	ds_read_b128 v[164:167], v192 offset:50176
	v_mul_f32_e32 v219, v215, v203
	v_mul_f32_e32 v236, v216, v228
	v_exp_f32_e32 v201, v17
	v_mfma_f32_32x32x16_f16 v[32:47], a[84:87], v[168:171], v[32:47]
	ds_read_b128 v[168:171], v192 offset:51200
	v_mul_f32_e32 v237, v216, v232
	v_fmac_f32_e32 v236, v217, v229
	v_exp_f32_e32 v202, v18
	v_mfma_f32_32x32x16_f16 v[48:63], a[84:87], v[172:175], v[48:63]
	ds_read_b128 v[172:175], v192 offset:52224
	global_load_lds_dwordx4 v192, s[44:45] offset:3072 sc1
	v_fmac_f32_e32 v237, v217, v233
	v_fmac_f32_e32 v236, v218, v230
	v_exp_f32_e32 v203, v19
	s_waitcnt lgkmcnt(4)
	v_mfma_f32_32x32x16_f16 v[32:47], a[88:91], v[176:179], v[32:47]
	ds_read_b128 v[176:179], v192 offset:53248
	v_fmac_f32_e32 v237, v218, v234
	v_fmac_f32_e32 v236, v219, v231
	v_exp_f32_e32 v204, v20
	v_mfma_f32_32x32x16_f16 v[48:63], a[88:91], v[180:183], v[48:63]
	ds_read_b128 v[180:183], v192 offset:54272
	v_fmac_f32_e32 v237, v219, v235
	v_mov_b32_e32 v238, v236
	v_exp_f32_e32 v205, v21
	v_mfma_f32_32x32x16_f16 v[32:47], a[92:95], v[184:187], v[32:47]
	ds_read_b128 v[184:187], v192 offset:55296
	v_mov_b32_e32 v239, v236
	v_mov_b32_e32 v240, v237
	v_exp_f32_e32 v206, v22
	v_mfma_f32_32x32x16_f16 v[48:63], a[92:95], v[188:191], v[48:63]
	ds_read_b128 v[188:191], v192 offset:56320
	s_add_u32 s44, s34, 0x19000
	s_addc_u32 s45, s35, 0
	s_mov_b32 m0, s59
	s_nop 0
	global_load_lds_dwordx4 v192, s[44:45] sc1
	v_mov_b32_e32 v241, v237
	v_cvt_pk_f16_f32 v220, v216, v217
	v_exp_f32_e32 v207, v23
	s_waitcnt lgkmcnt(4)
	v_mfma_f32_32x32x16_f16 v[32:47], a[96:99], v[160:163], v[32:47]
	ds_read_b128 v[160:163], v192 offset:57344
	s_nop 1
	v_permlane32_swap_b32_e32 v238, v239
	v_permlane32_swap_b32_e32 v240, v241
	v_add_f32_e32 v238, v238, v239
	v_add_f32_e32 v239, v240, v241
	ds_write_b64 v248, v[238:239] offset:0
	v_exp_f32_e32 v208, v24
	v_mfma_f32_32x32x16_f16 v[48:63], a[96:99], v[164:167], v[48:63]
	ds_read_b128 v[164:167], v192 offset:58368
	v_cvt_pk_f16_f32 v221, v218, v219
	v_exp_f32_e32 v209, v25
	v_add_f32_e32 v200, 1.0, v200
	v_mfma_f32_32x32x16_f16 v[32:47], a[100:103], v[168:171], v[32:47]
	ds_read_b128 v[168:171], v192 offset:59392
	v_exp_f32_e32 v210, v26
	v_add_f32_e32 v201, 1.0, v201
	v_add_f32_e32 v202, 1.0, v202
	v_mfma_f32_32x32x16_f16 v[48:63], a[100:103], v[172:175], v[48:63]
	ds_read_b128 v[172:175], v192 offset:60416
	global_load_lds_dwordx4 v192, s[44:45] offset:1024 sc1
	v_exp_f32_e32 v211, v27
	v_add_f32_e32 v203, 1.0, v203
	v_add_f32_e32 v204, 1.0, v204
	s_waitcnt lgkmcnt(5)
	v_mfma_f32_32x32x16_f16 v[32:47], a[104:107], v[176:179], v[32:47]
	ds_read_b128 v[176:179], v192 offset:61440
	v_exp_f32_e32 v212, v28
	v_add_f32_e32 v205, 1.0, v205
	v_add_f32_e32 v206, 1.0, v206
	v_mfma_f32_32x32x16_f16 v[48:63], a[104:107], v[180:183], v[48:63]
	ds_read_b128 v[180:183], v192 offset:62464
	v_exp_f32_e32 v213, v29
	v_add_f32_e32 v207, 1.0, v207
	v_add_f32_e32 v208, 1.0, v208
	v_mfma_f32_32x32x16_f16 v[32:47], a[108:111], v[184:187], v[32:47]
	ds_read_b128 v[184:187], v192 offset:63488
	v_exp_f32_e32 v214, v30
	v_add_f32_e32 v209, 1.0, v209
	v_add_f32_e32 v210, 1.0, v210
	v_mfma_f32_32x32x16_f16 v[48:63], a[108:111], v[188:191], v[48:63]
	ds_read_b128 v[188:191], v192 offset:64512
	global_load_lds_dwordx4 v192, s[44:45] offset:2048 sc1
	v_exp_f32_e32 v215, v31
	v_add_f32_e32 v211, 1.0, v211
	v_add_f32_e32 v212, 1.0, v212
	s_waitcnt vmcnt(7)
	s_barrier
	s_waitcnt lgkmcnt(4)
	v_mfma_f32_32x32x16_f16 v[32:47], a[112:115], v[160:163], v[32:47]
	ds_read_b128 v[160:163], v193 offset:0
	v_add_f32_e32 v213, 1.0, v213
	v_add_f32_e32 v214, 1.0, v214
	v_rcp_f32_e32 v200, v200
	v_mfma_f32_32x32x16_f16 v[48:63], a[112:115], v[164:167], v[48:63]
	ds_read_b128 v[164:167], v193 offset:1024
	v_add_f32_e32 v215, 1.0, v215
	v_rcp_f32_e32 v201, v201
	v_mfma_f32_32x32x16_f16 v[32:47], a[116:119], v[168:171], v[32:47]
	ds_read_b128 v[168:171], v193 offset:2048
	v_rcp_f32_e32 v202, v202
	v_mfma_f32_32x32x16_f16 v[48:63], a[116:119], v[172:175], v[48:63]
	ds_read_b128 v[172:175], v193 offset:3072
	global_load_lds_dwordx4 v192, s[44:45] offset:3072 sc1
	v_rcp_f32_e32 v203, v203
	s_waitcnt lgkmcnt(4)
	v_mfma_f32_32x32x16_f16 v[32:47], a[120:123], v[176:179], v[32:47]
	ds_read_b128 v[176:179], v193 offset:4096
	v_rcp_f32_e32 v204, v204
	s_add_u32 s46, s42, 0x6000
	s_addc_u32 s47, s43, 0
	global_load_dwordx4 v[96:99], v192, s[46:47] offset:0
	v_mfma_f32_32x32x16_f16 v[48:63], a[120:123], v[180:183], v[48:63]
	ds_read_b128 v[180:183], v193 offset:5120
	v_rcp_f32_e32 v205, v205
	v_mul_f32_e32 v204, v204, v132
	global_load_dwordx4 v[100:103], v192, s[46:47] offset:1024
	global_load_dwordx4 v[104:107], v192, s[46:47] offset:2048
	v_mfma_f32_32x32x16_f16 v[32:47], a[124:127], v[184:187], v[32:47]
	ds_read_b128 v[184:187], v193 offset:6144
	v_rcp_f32_e32 v206, v206
	v_mul_f32_e32 v205, v205, v133
	global_load_dwordx4 v[108:111], v192, s[46:47] offset:3072
	s_add_u32 s46, s42, 0x7000
	s_addc_u32 s47, s43, 0
	v_mfma_f32_32x32x16_f16 v[48:63], a[124:127], v[188:191], v[48:63]
	ds_read_b128 v[188:191], v193 offset:7168
	v_cmp_gt_u32_e32 vcc, 3, v251
	s_cbranch_vccz .LD_tok26

.LD_join31:
	ds_read_b64 v[200:201], v249 offset:0
	ds_read_b64 v[202:203], v249 offset:2048
	ds_read_b64 v[204:205], v249 offset:4096
	ds_read_b64 v[206:207], v249 offset:6144
	s_waitcnt lgkmcnt(8)
	v_mfma_f32_32x32x16_f16 v[32:47], a[208:211], v[160:163], v[32:47]
	ds_read_b128 v[160:163], v193 offset:49152
	v_mfma_f32_32x32x16_f16 v[48:63], a[208:211], v[164:167], v[48:63]
	ds_read_b128 v[164:167], v193 offset:50176
	v_mfma_f32_32x32x16_f16 v[32:47], a[212:215], v[168:171], v[32:47]
	ds_read_b128 v[168:171], v193 offset:51200
	v_mfma_f32_32x32x16_f16 v[48:63], a[212:215], v[172:175], v[48:63]
	ds_read_b128 v[172:175], v193 offset:52224
	global_load_lds_dwordx4 v192, s[44:45] offset:3072 sc1
	s_waitcnt lgkmcnt(8)
	v_mfma_f32_32x32x16_f16 v[32:47], a[216:219], v[176:179], v[32:47]
	ds_read_b128 v[176:179], v193 offset:53248
	v_mfma_f32_32x32x16_f16 v[48:63], a[216:219], v[180:183], v[48:63]
	ds_read_b128 v[180:183], v193 offset:54272
	v_mfma_f32_32x32x16_f16 v[32:47], a[220:223], v[184:187], v[32:47]
	ds_read_b128 v[184:187], v193 offset:55296
	v_mfma_f32_32x32x16_f16 v[48:63], a[220:223], v[188:191], v[48:63]
	ds_read_b128 v[188:191], v193 offset:56320
	s_add_u32 s44, s34, 0x9000
	s_addc_u32 s45, s35, 0
	s_mov_b32 m0, s55
	s_nop 0
	global_load_lds_dwordx4 v192, s[44:45] sc1
	s_waitcnt lgkmcnt(4)
	v_mfma_f32_32x32x16_f16 v[32:47], a[224:227], v[160:163], v[32:47]
	ds_read_b128 v[160:163], v193 offset:57344
	v_mfma_f32_32x32x16_f16 v[48:63], a[224:227], v[164:167], v[48:63]
	ds_read_b128 v[164:167], v193 offset:58368
	v_mfma_f32_32x32x16_f16 v[32:47], a[228:231], v[168:171], v[32:47]
	ds_read_b128 v[168:171], v193 offset:59392
	v_mfma_f32_32x32x16_f16 v[48:63], a[228:231], v[172:175], v[48:63]
	ds_read_b128 v[172:175], v193 offset:60416
	global_load_lds_dwordx4 v192, s[44:45] offset:1024 sc1
	v_add_f32_e32 v200, v200, v202
	v_add_f32_e32 v201, v201, v203
	v_add_f32_e32 v200, v200, v204
	v_add_f32_e32 v201, v201, v205
	v_add_f32_e32 v200, v200, v206
	v_add_f32_e32 v201, v201, v207
	global_store_dwordx2 v250, v[200:201], s[72:73]
	s_waitcnt lgkmcnt(4)
	v_mfma_f32_32x32x16_f16 v[32:47], a[232:235], v[176:179], v[32:47]
	ds_read_b128 v[176:179], v193 offset:61440
	v_mfma_f32_32x32x16_f16 v[48:63], a[232:235], v[180:183], v[48:63]
	ds_read_b128 v[180:183], v193 offset:62464
	v_mfma_f32_32x32x16_f16 v[32:47], a[236:239], v[184:187], v[32:47]
	ds_read_b128 v[184:187], v193 offset:63488
	v_mfma_f32_32x32x16_f16 v[48:63], a[236:239], v[188:191], v[48:63]
	ds_read_b128 v[188:191], v193 offset:64512
	global_load_lds_dwordx4 v192, s[44:45] offset:2048 sc1
	s_waitcnt vmcnt(9)
	s_barrier
	s_waitcnt lgkmcnt(4)
	v_mfma_f32_32x32x16_f16 v[32:47], a[240:243], v[160:163], v[32:47]
	ds_read_b128 v[160:163], v192 offset:0
	v_mfma_f32_32x32x16_f16 v[48:63], a[240:243], v[164:167], v[48:63]
	ds_read_b128 v[164:167], v192 offset:1024
	v_mfma_f32_32x32x16_f16 v[32:47], a[244:247], v[168:171], v[32:47]
	ds_read_b128 v[168:171], v192 offset:2048
	v_mfma_f32_32x32x16_f16 v[48:63], a[244:247], v[172:175], v[48:63]
	ds_read_b128 v[172:175], v192 offset:3072
	global_load_lds_dwordx4 v192, s[44:45] offset:3072 sc1
	s_waitcnt lgkmcnt(4)
	v_mfma_f32_32x32x16_f16 v[32:47], a[248:251], v[176:179], v[32:47]
	ds_read_b128 v[176:179], v192 offset:4096
	v_mfma_f32_32x32x16_f16 v[48:63], a[248:251], v[180:183], v[48:63]
	ds_read_b128 v[180:183], v192 offset:5120
	v_mfma_f32_32x32x16_f16 v[32:47], a[252:255], v[184:187], v[32:47]
	ds_read_b128 v[184:187], v192 offset:6144
	v_mfma_f32_32x32x16_f16 v[48:63], a[252:255], v[188:191], v[48:63]
	ds_read_b128 v[188:191], v192 offset:7168
	s_add_u32 s44, s34, 0x10000
	s_addc_u32 s45, s35, 0
	s_mov_b32 m0, s56
	s_nop 0
	global_load_lds_dwordx4 v192, s[44:45] sc1
	s_and_b32 s64, s33, 1
	s_lshl_b32 s64, s64, 22
	s_add_u32 s64, s64, s50
	s_add_u32 s64, s64, 0x20000
	s_add_u32 s36, s6, s64
	s_addc_u32 s37, s7, 0
	s_lshl_b32 s64, s33, 3
	s_add_u32 s64, s64, s29
	s_lshl_b32 s64, s64, 5
	s_add_u32 s64, s64, s30
	s_lshl_b32 s64, s64, 2
	s_add_u32 s40, s8, s64
	s_addc_u32 s41, s9, 0
	s_lshl_b32 s64, s33, 19
	s_add_u32 s64, s64, 0x200
	s_add_u32 s72, s62, s64
	s_addc_u32 s73, s63, 0
	s_nop 3
	s_waitcnt lgkmcnt(4)
	v_mfma_f32_32x32x16_f16 v[64:79], a[0:3], v[160:163], v[64:79]
	ds_read_b128 v[160:163], v192 offset:8192
	v_exp_f32_e32 v200, v32
	v_mfma_f32_32x32x16_f16 v[80:95], a[0:3], v[164:167], v[80:95]
	ds_read_b128 v[164:167], v192 offset:9216
	s_lshl_b32 s64, s71, 3
	s_add_u32 s64, s64, s29
	s_lshl_b32 s64, s64, 7
	s_add_u32 s38, s8, s64
	s_addc_u32 s39, s9, 0
	global_load_dword v251, v196, s[38:39] sc1
	v_exp_f32_e32 v201, v33
	v_add_f32_e32 v200, 1.0, v200
	v_mfma_f32_32x32x16_f16 v[64:79], a[4:7], v[168:171], v[64:79]
	ds_read_b128 v[168:171], v192 offset:10240
	v_exp_f32_e32 v202, v34
	v_add_f32_e32 v201, 1.0, v201
	v_mfma_f32_32x32x16_f16 v[80:95], a[4:7], v[172:175], v[80:95]
	ds_read_b128 v[172:175], v192 offset:11264
	global_load_lds_dwordx4 v192, s[44:45] offset:1024 sc1
	v_exp_f32_e32 v203, v35
	v_add_f32_e32 v202, 1.0, v202
	s_waitcnt lgkmcnt(4)
	v_mfma_f32_32x32x16_f16 v[64:79], a[8:11], v[176:179], v[64:79]
	ds_read_b128 v[176:179], v192 offset:12288
	v_exp_f32_e32 v204, v36
	v_add_f32_e32 v203, 1.0, v203
	v_mfma_f32_32x32x16_f16 v[80:95], a[8:11], v[180:183], v[80:95]
	ds_read_b128 v[180:183], v192 offset:13312
	v_exp_f32_e32 v205, v37
	v_add_f32_e32 v204, 1.0, v204
	v_mfma_f32_32x32x16_f16 v[64:79], a[12:15], v[184:187], v[64:79]
	ds_read_b128 v[184:187], v192 offset:14336
	v_exp_f32_e32 v206, v38
	v_add_f32_e32 v205, 1.0, v205
	v_mfma_f32_32x32x16_f16 v[80:95], a[12:15], v[188:191], v[80:95]
	ds_read_b128 v[188:191], v192 offset:15360
	global_load_lds_dwordx4 v192, s[44:45] offset:2048 sc1
	v_exp_f32_e32 v207, v39
	v_add_f32_e32 v206, 1.0, v206
	s_waitcnt lgkmcnt(4)
	v_mfma_f32_32x32x16_f16 v[64:79], a[16:19], v[160:163], v[64:79]
	ds_read_b128 v[160:163], v192 offset:16384
	v_exp_f32_e32 v208, v40
	v_add_f32_e32 v207, 1.0, v207
	v_mfma_f32_32x32x16_f16 v[80:95], a[16:19], v[164:167], v[80:95]
	ds_read_b128 v[164:167], v192 offset:17408
	v_exp_f32_e32 v209, v41
	v_add_f32_e32 v208, 1.0, v208
	v_mfma_f32_32x32x16_f16 v[64:79], a[20:23], v[168:171], v[64:79]
	ds_read_b128 v[168:171], v192 offset:18432
	v_exp_f32_e32 v210, v42
	v_add_f32_e32 v209, 1.0, v209
	v_mfma_f32_32x32x16_f16 v[80:95], a[20:23], v[172:175], v[80:95]
	ds_read_b128 v[172:175], v192 offset:19456
	global_load_lds_dwordx4 v192, s[44:45] offset:3072 sc1
	v_exp_f32_e32 v211, v43
	v_add_f32_e32 v210, 1.0, v210
	s_waitcnt lgkmcnt(4)
	v_mfma_f32_32x32x16_f16 v[64:79], a[24:27], v[176:179], v[64:79]
	ds_read_b128 v[176:179], v192 offset:20480
	v_exp_f32_e32 v212, v44
	v_add_f32_e32 v211, 1.0, v211
	v_mfma_f32_32x32x16_f16 v[80:95], a[24:27], v[180:183], v[80:95]
	ds_read_b128 v[180:183], v192 offset:21504
	v_exp_f32_e32 v213, v45
	v_add_f32_e32 v212, 1.0, v212
	v_mfma_f32_32x32x16_f16 v[64:79], a[28:31], v[184:187], v[64:79]
	ds_read_b128 v[184:187], v192 offset:22528
	v_exp_f32_e32 v214, v46
	v_add_f32_e32 v213, 1.0, v213
	v_mfma_f32_32x32x16_f16 v[80:95], a[28:31], v[188:191], v[80:95]
	ds_read_b128 v[188:191], v192 offset:23552
	s_add_u32 s44, s34, 0x11000
	s_addc_u32 s45, s35, 0
	s_mov_b32 m0, s57
	s_nop 0
	global_load_lds_dwordx4 v192, s[44:45] sc1
	v_exp_f32_e32 v215, v47
	v_add_f32_e32 v214, 1.0, v214
	s_waitcnt lgkmcnt(4)
	v_mfma_f32_32x32x16_f16 v[64:79], a[32:35], v[160:163], v[64:79]
	ds_read_b128 v[160:163], v192 offset:24576
	v_add_f32_e32 v215, 1.0, v215
	v_rcp_f32_e32 v200, v200
	v_mfma_f32_32x32x16_f16 v[80:95], a[32:35], v[164:167], v[80:95]
	ds_read_b128 v[164:167], v192 offset:25600
	v_rcp_f32_e32 v201, v201
	v_mfma_f32_32x32x16_f16 v[64:79], a[36:39], v[168:171], v[64:79]
	ds_read_b128 v[168:171], v192 offset:26624
	v_rcp_f32_e32 v202, v202
	v_mfma_f32_32x32x16_f16 v[80:95], a[36:39], v[172:175], v[80:95]
	ds_read_b128 v[172:175], v192 offset:27648
	global_load_lds_dwordx4 v192, s[44:45] offset:1024 sc1
	v_rcp_f32_e32 v203, v203
	s_waitcnt lgkmcnt(4)
	v_mfma_f32_32x32x16_f16 v[64:79], a[40:43], v[176:179], v[64:79]
	ds_read_b128 v[176:179], v192 offset:28672
	v_rcp_f32_e32 v204, v204
	v_mfma_f32_32x32x16_f16 v[80:95], a[40:43], v[180:183], v[80:95]
	ds_read_b128 v[180:183], v192 offset:29696
	v_rcp_f32_e32 v205, v205
	v_mul_f32_e32 v204, v204, v136
	v_mfma_f32_32x32x16_f16 v[64:79], a[44:47], v[184:187], v[64:79]
	ds_read_b128 v[184:187], v192 offset:30720
	v_rcp_f32_e32 v206, v206
	v_mul_f32_e32 v205, v205, v137
	v_mfma_f32_32x32x16_f16 v[80:95], a[44:47], v[188:191], v[80:95]
	ds_read_b128 v[188:191], v192 offset:31744
	global_load_lds_dwordx4 v192, s[44:45] offset:2048 sc1
	v_rcp_f32_e32 v207, v207
	v_mul_f32_e32 v206, v206, v138
	s_waitcnt vmcnt(8)
	s_barrier
	s_waitcnt lgkmcnt(4)
	v_mfma_f32_32x32x16_f16 v[64:79], a[48:51], v[160:163], v[64:79]
	ds_read_b128 v[160:163], v192 offset:32768
	v_rcp_f32_e32 v208, v208
	v_mul_f32_e32 v207, v207, v139
	v_mfma_f32_32x32x16_f16 v[80:95], a[48:51], v[164:167], v[80:95]
	ds_read_b128 v[164:167], v192 offset:33792
	v_rcp_f32_e32 v209, v209
	v_fmamk_f32 v208, v208, 0xc0b8aa3b, v198
	v_mfma_f32_32x32x16_f16 v[64:79], a[52:55], v[168:171], v[64:79]
	ds_read_b128 v[168:171], v192 offset:34816
	v_rcp_f32_e32 v210, v210
	v_fmamk_f32 v209, v209, 0xc0b8aa3b, v198
	v_fma_f32 v136, v200, v208, v204
	v_mfma_f32_32x32x16_f16 v[80:95], a[52:55], v[172:175], v[80:95]
	ds_read_b128 v[172:175], v192 offset:35840
	global_load_lds_dwordx4 v192, s[44:45] offset:3072 sc1
	v_rcp_f32_e32 v211, v211
	v_fmamk_f32 v210, v210, 0xc0b8aa3b, v198
	v_fma_f32 v137, v201, v209, v205
	s_waitcnt lgkmcnt(4)
	v_mfma_f32_32x32x16_f16 v[64:79], a[56:59], v[176:179], v[64:79]
	ds_read_b128 v[176:179], v192 offset:36864
	v_rcp_f32_e32 v212, v212
	v_fmamk_f32 v211, v211, 0xc0b8aa3b, v198
	v_fma_f32 v138, v202, v210, v206
	v_mfma_f32_32x32x16_f16 v[80:95], a[56:59], v[180:183], v[80:95]
	ds_read_b128 v[180:183], v192 offset:37888
	v_rcp_f32_e32 v213, v213
	v_fma_f32 v139, v203, v211, v207
	v_mfma_f32_32x32x16_f16 v[64:79], a[60:63], v[184:187], v[64:79]
	ds_read_b128 v[184:187], v192 offset:38912
	v_rcp_f32_e32 v214, v214
	v_mfma_f32_32x32x16_f16 v[80:95], a[60:63], v[188:191], v[80:95]
	ds_read_b128 v[188:191], v192 offset:39936
	s_add_u32 s44, s34, 0x18000
	s_addc_u32 s45, s35, 0
	s_mov_b32 m0, s58
	s_nop 0
	global_load_lds_dwordx4 v192, s[44:45] sc1
	v_rcp_f32_e32 v215, v215
	s_waitcnt lgkmcnt(4)
	v_mfma_f32_32x32x16_f16 v[64:79], a[64:67], v[160:163], v[64:79]
	ds_read_b128 v[160:163], v192 offset:40960
	v_exp_f32_e32 v200, v136
	v_mfma_f32_32x32x16_f16 v[80:95], a[64:67], v[164:167], v[80:95]
	ds_read_b128 v[164:167], v192 offset:41984
	v_exp_f32_e32 v201, v137
	v_add_f32_e32 v200, 1.0, v200
	v_mfma_f32_32x32x16_f16 v[64:79], a[68:71], v[168:171], v[64:79]
	ds_read_b128 v[168:171], v192 offset:43008
	v_exp_f32_e32 v202, v138
	v_add_f32_e32 v201, 1.0, v201
	v_mfma_f32_32x32x16_f16 v[80:95], a[68:71], v[172:175], v[80:95]
	ds_read_b128 v[172:175], v192 offset:44032
	global_load_lds_dwordx4 v192, s[44:45] offset:1024 sc1
	v_exp_f32_e32 v203, v139
	v_add_f32_e32 v202, 1.0, v202
	s_waitcnt lgkmcnt(4)
	v_mfma_f32_32x32x16_f16 v[64:79], a[72:75], v[176:179], v[64:79]
	ds_read_b128 v[176:179], v192 offset:45056
	v_add_f32_e32 v203, 1.0, v203
	v_rcp_f32_e32 v200, v200
	v_mfma_f32_32x32x16_f16 v[80:95], a[72:75], v[180:183], v[80:95]
	ds_read_b128 v[180:183], v192 offset:46080
	v_rcp_f32_e32 v201, v201
	v_fma_f32 v200, v200, 2.0, -1.0
	v_mfma_f32_32x32x16_f16 v[64:79], a[76:79], v[184:187], v[64:79]
	ds_read_b128 v[184:187], v192 offset:47104
	v_rcp_f32_e32 v202, v202
	v_fma_f32 v201, v201, 2.0, -1.0
	v_mul_f32_e32 v216, v212, v200
	v_mfma_f32_32x32x16_f16 v[80:95], a[76:79], v[188:191], v[80:95]
	ds_read_b128 v[188:191], v192 offset:48128
	global_load_lds_dwordx4 v192, s[44:45] offset:2048 sc1
	v_rcp_f32_e32 v203, v203
	v_fma_f32 v202, v202, 2.0, -1.0
	v_mul_f32_e32 v217, v213, v201
	s_waitcnt lgkmcnt(4)
	v_mfma_f32_32x32x16_f16 v[64:79], a[80:83], v[160:163], v[64:79]
	ds_read_b128 v[160:163], v192 offset:49152
	v_fma_f32 v203, v203, 2.0, -1.0
	v_mul_f32_e32 v218, v214, v202
	v_exp_f32_e32 v200, v48
	v_mfma_f32_32x32x16_f16 v[80:95], a[80:83], v[164:167], v[80:95]
	ds_read_b128 v[164:167], v192 offset:50176
	v_mul_f32_e32 v219, v215, v203
	v_mul_f32_e32 v236, v216, v228
	v_exp_f32_e32 v201, v49
	v_mfma_f32_32x32x16_f16 v[64:79], a[84:87], v[168:171], v[64:79]
	ds_read_b128 v[168:171], v192 offset:51200
	v_mul_f32_e32 v237, v216, v232
	v_fmac_f32_e32 v236, v217, v229
	v_exp_f32_e32 v202, v50
	v_mfma_f32_32x32x16_f16 v[80:95], a[84:87], v[172:175], v[80:95]
	ds_read_b128 v[172:175], v192 offset:52224
	global_load_lds_dwordx4 v192, s[44:45] offset:3072 sc1
	v_fmac_f32_e32 v237, v217, v233
	v_fmac_f32_e32 v236, v218, v230
	v_exp_f32_e32 v203, v51
	s_waitcnt lgkmcnt(4)
	v_mfma_f32_32x32x16_f16 v[64:79], a[88:91], v[176:179], v[64:79]
	ds_read_b128 v[176:179], v192 offset:53248
	v_fmac_f32_e32 v237, v218, v234
	v_fmac_f32_e32 v236, v219, v231
	v_exp_f32_e32 v204, v52
	v_mfma_f32_32x32x16_f16 v[80:95], a[88:91], v[180:183], v[80:95]
	ds_read_b128 v[180:183], v192 offset:54272
	v_fmac_f32_e32 v237, v219, v235
	v_mov_b32_e32 v238, v236
	v_exp_f32_e32 v205, v53
	v_mfma_f32_32x32x16_f16 v[64:79], a[92:95], v[184:187], v[64:79]
	ds_read_b128 v[184:187], v192 offset:55296
	v_mov_b32_e32 v239, v236
	v_mov_b32_e32 v240, v237
	v_exp_f32_e32 v206, v54
	v_mfma_f32_32x32x16_f16 v[80:95], a[92:95], v[188:191], v[80:95]
	ds_read_b128 v[188:191], v192 offset:56320
	s_add_u32 s44, s34, 0x19000
	s_addc_u32 s45, s35, 0
	s_mov_b32 m0, s59
	s_nop 0
	global_load_lds_dwordx4 v192, s[44:45] sc1
	v_mov_b32_e32 v241, v237
	v_cvt_pk_f16_f32 v220, v216, v217
	v_exp_f32_e32 v207, v55
	s_waitcnt lgkmcnt(4)
	v_mfma_f32_32x32x16_f16 v[64:79], a[96:99], v[160:163], v[64:79]
	ds_read_b128 v[160:163], v192 offset:57344
	s_nop 1
	v_permlane32_swap_b32_e32 v238, v239
	v_permlane32_swap_b32_e32 v240, v241
	v_add_f32_e32 v238, v238, v239
	v_add_f32_e32 v239, v240, v241
	ds_write_b64 v248, v[238:239] offset:512
	v_exp_f32_e32 v208, v56
	v_mfma_f32_32x32x16_f16 v[80:95], a[96:99], v[164:167], v[80:95]
	ds_read_b128 v[164:167], v192 offset:58368
	v_cvt_pk_f16_f32 v221, v218, v219
	v_exp_f32_e32 v209, v57
	v_add_f32_e32 v200, 1.0, v200
	v_mfma_f32_32x32x16_f16 v[64:79], a[100:103], v[168:171], v[64:79]
	ds_read_b128 v[168:171], v192 offset:59392
	v_exp_f32_e32 v210, v58
	v_add_f32_e32 v201, 1.0, v201
	v_add_f32_e32 v202, 1.0, v202
	v_mfma_f32_32x32x16_f16 v[80:95], a[100:103], v[172:175], v[80:95]
	ds_read_b128 v[172:175], v192 offset:60416
	global_load_lds_dwordx4 v192, s[44:45] offset:1024 sc1
	v_exp_f32_e32 v211, v59
	v_add_f32_e32 v203, 1.0, v203
	v_add_f32_e32 v204, 1.0, v204
	s_waitcnt lgkmcnt(5)
	v_mfma_f32_32x32x16_f16 v[64:79], a[104:107], v[176:179], v[64:79]
	ds_read_b128 v[176:179], v192 offset:61440
	v_exp_f32_e32 v212, v60
	v_add_f32_e32 v205, 1.0, v205
	v_add_f32_e32 v206, 1.0, v206
	v_mfma_f32_32x32x16_f16 v[80:95], a[104:107], v[180:183], v[80:95]
	ds_read_b128 v[180:183], v192 offset:62464
	v_exp_f32_e32 v213, v61
	v_add_f32_e32 v207, 1.0, v207
	v_add_f32_e32 v208, 1.0, v208
	v_mfma_f32_32x32x16_f16 v[64:79], a[108:111], v[184:187], v[64:79]
	ds_read_b128 v[184:187], v192 offset:63488
	v_exp_f32_e32 v214, v62
	v_add_f32_e32 v209, 1.0, v209
	v_add_f32_e32 v210, 1.0, v210
	v_mfma_f32_32x32x16_f16 v[80:95], a[108:111], v[188:191], v[80:95]
	ds_read_b128 v[188:191], v192 offset:64512
	global_load_lds_dwordx4 v192, s[44:45] offset:2048 sc1
	v_exp_f32_e32 v215, v63
	v_add_f32_e32 v211, 1.0, v211
	v_add_f32_e32 v212, 1.0, v212
	s_waitcnt vmcnt(7)
	s_barrier
	s_waitcnt lgkmcnt(4)
	v_mfma_f32_32x32x16_f16 v[64:79], a[112:115], v[160:163], v[64:79]
	ds_read_b128 v[160:163], v193 offset:0
	v_add_f32_e32 v213, 1.0, v213
	v_add_f32_e32 v214, 1.0, v214
	v_rcp_f32_e32 v200, v200
	v_mfma_f32_32x32x16_f16 v[80:95], a[112:115], v[164:167], v[80:95]
	ds_read_b128 v[164:167], v193 offset:1024
	v_add_f32_e32 v215, 1.0, v215
	v_rcp_f32_e32 v201, v201
	v_mfma_f32_32x32x16_f16 v[64:79], a[116:119], v[168:171], v[64:79]
	ds_read_b128 v[168:171], v193 offset:2048
	v_rcp_f32_e32 v202, v202
	v_mfma_f32_32x32x16_f16 v[80:95], a[116:119], v[172:175], v[80:95]
	ds_read_b128 v[172:175], v193 offset:3072
	global_load_lds_dwordx4 v192, s[44:45] offset:3072 sc1
	v_rcp_f32_e32 v203, v203
	s_waitcnt lgkmcnt(4)
	v_mfma_f32_32x32x16_f16 v[64:79], a[120:123], v[176:179], v[64:79]
	ds_read_b128 v[176:179], v193 offset:4096
	v_rcp_f32_e32 v204, v204
	s_add_u32 s46, s42, 0x0
	s_addc_u32 s47, s43, 0
	global_load_dwordx4 v[0:3], v192, s[46:47] offset:0
	v_mfma_f32_32x32x16_f16 v[80:95], a[120:123], v[180:183], v[80:95]
	ds_read_b128 v[180:183], v193 offset:5120
	v_rcp_f32_e32 v205, v205
	v_mul_f32_e32 v204, v204, v140
	global_load_dwordx4 v[4:7], v192, s[46:47] offset:1024
	global_load_dwordx4 v[8:11], v192, s[46:47] offset:2048
	v_mfma_f32_32x32x16_f16 v[64:79], a[124:127], v[184:187], v[64:79]
	ds_read_b128 v[184:187], v193 offset:6144
	v_rcp_f32_e32 v206, v206
	v_mul_f32_e32 v205, v205, v141
	global_load_dwordx4 v[12:15], v192, s[46:47] offset:3072
	s_add_u32 s46, s42, 0x1000
	s_addc_u32 s47, s43, 0
	v_mfma_f32_32x32x16_f16 v[80:95], a[124:127], v[188:191], v[80:95]
	ds_read_b128 v[188:191], v193 offset:7168
	v_cmp_gt_u32_e32 vcc, 4, v251
	s_cbranch_vccz .LD_tok32

.LD_join37:
	ds_read_b64 v[200:201], v249 offset:512
	ds_read_b64 v[202:203], v249 offset:2560
	ds_read_b64 v[204:205], v249 offset:4608
	ds_read_b64 v[206:207], v249 offset:6656
	s_waitcnt lgkmcnt(8)
	v_mfma_f32_32x32x16_f16 v[64:79], a[208:211], v[160:163], v[64:79]
	ds_read_b128 v[160:163], v193 offset:49152
	v_mfma_f32_32x32x16_f16 v[80:95], a[208:211], v[164:167], v[80:95]
	ds_read_b128 v[164:167], v193 offset:50176
	v_mfma_f32_32x32x16_f16 v[64:79], a[212:215], v[168:171], v[64:79]
	ds_read_b128 v[168:171], v193 offset:51200
	v_mfma_f32_32x32x16_f16 v[80:95], a[212:215], v[172:175], v[80:95]
	ds_read_b128 v[172:175], v193 offset:52224
	global_load_lds_dwordx4 v192, s[44:45] offset:3072 sc1
	s_waitcnt lgkmcnt(8)
	v_mfma_f32_32x32x16_f16 v[64:79], a[216:219], v[176:179], v[64:79]
	ds_read_b128 v[176:179], v193 offset:53248
	v_mfma_f32_32x32x16_f16 v[80:95], a[216:219], v[180:183], v[80:95]
	ds_read_b128 v[180:183], v193 offset:54272
	v_mfma_f32_32x32x16_f16 v[64:79], a[220:223], v[184:187], v[64:79]
	ds_read_b128 v[184:187], v193 offset:55296
	v_mfma_f32_32x32x16_f16 v[80:95], a[220:223], v[188:191], v[80:95]
	ds_read_b128 v[188:191], v193 offset:56320
	s_add_u32 s44, s34, 0x9000
	s_addc_u32 s45, s35, 0
	s_mov_b32 m0, s55
	s_nop 0
	global_load_lds_dwordx4 v192, s[44:45] sc1
	s_waitcnt lgkmcnt(4)
	v_mfma_f32_32x32x16_f16 v[64:79], a[224:227], v[160:163], v[64:79]
	ds_read_b128 v[160:163], v193 offset:57344
	v_mfma_f32_32x32x16_f16 v[80:95], a[224:227], v[164:167], v[80:95]
	ds_read_b128 v[164:167], v193 offset:58368
	v_mfma_f32_32x32x16_f16 v[64:79], a[228:231], v[168:171], v[64:79]
	ds_read_b128 v[168:171], v193 offset:59392
	v_mfma_f32_32x32x16_f16 v[80:95], a[228:231], v[172:175], v[80:95]
	ds_read_b128 v[172:175], v193 offset:60416
	global_load_lds_dwordx4 v192, s[44:45] offset:1024 sc1
	v_add_f32_e32 v200, v200, v202
	v_add_f32_e32 v201, v201, v203
	v_add_f32_e32 v200, v200, v204
	v_add_f32_e32 v201, v201, v205
	v_add_f32_e32 v200, v200, v206
	v_add_f32_e32 v201, v201, v207
	global_store_dwordx2 v250, v[200:201], s[72:73]
	s_waitcnt lgkmcnt(4)
	v_mfma_f32_32x32x16_f16 v[64:79], a[232:235], v[176:179], v[64:79]
	ds_read_b128 v[176:179], v193 offset:61440
	v_mfma_f32_32x32x16_f16 v[80:95], a[232:235], v[180:183], v[80:95]
	ds_read_b128 v[180:183], v193 offset:62464
	v_mfma_f32_32x32x16_f16 v[64:79], a[236:239], v[184:187], v[64:79]
	ds_read_b128 v[184:187], v193 offset:63488
	v_mfma_f32_32x32x16_f16 v[80:95], a[236:239], v[188:191], v[80:95]
	ds_read_b128 v[188:191], v193 offset:64512
	global_load_lds_dwordx4 v192, s[44:45] offset:2048 sc1
	s_waitcnt vmcnt(9)
	s_barrier
	s_waitcnt lgkmcnt(4)
	v_mfma_f32_32x32x16_f16 v[64:79], a[240:243], v[160:163], v[64:79]
	ds_read_b128 v[160:163], v192 offset:0
	v_mfma_f32_32x32x16_f16 v[80:95], a[240:243], v[164:167], v[80:95]
	ds_read_b128 v[164:167], v192 offset:1024
	v_mfma_f32_32x32x16_f16 v[64:79], a[244:247], v[168:171], v[64:79]
	ds_read_b128 v[168:171], v192 offset:2048
	v_mfma_f32_32x32x16_f16 v[80:95], a[244:247], v[172:175], v[80:95]
	ds_read_b128 v[172:175], v192 offset:3072
	global_load_lds_dwordx4 v192, s[44:45] offset:3072 sc1
	s_waitcnt lgkmcnt(4)
	v_mfma_f32_32x32x16_f16 v[64:79], a[248:251], v[176:179], v[64:79]
	ds_read_b128 v[176:179], v192 offset:4096
	v_mfma_f32_32x32x16_f16 v[80:95], a[248:251], v[180:183], v[80:95]
	ds_read_b128 v[180:183], v192 offset:5120
	v_mfma_f32_32x32x16_f16 v[64:79], a[252:255], v[184:187], v[64:79]
	ds_read_b128 v[184:187], v192 offset:6144
	v_mfma_f32_32x32x16_f16 v[80:95], a[252:255], v[188:191], v[80:95]
	ds_read_b128 v[188:191], v192 offset:7168
	s_add_u32 s44, s34, 0x10000
	s_addc_u32 s45, s35, 0
	s_mov_b32 m0, s56
	s_nop 0
	global_load_lds_dwordx4 v192, s[44:45] sc1
	s_and_b32 s64, s33, 1
	s_lshl_b32 s64, s64, 22
	s_add_u32 s64, s64, s50
	s_add_u32 s64, s64, 0x40000
	s_add_u32 s36, s6, s64
	s_addc_u32 s37, s7, 0
	s_lshl_b32 s64, s33, 3
	s_add_u32 s64, s64, s29
	s_lshl_b32 s64, s64, 5
	s_add_u32 s64, s64, s30
	s_lshl_b32 s64, s64, 2
	s_add_u32 s40, s8, s64
	s_addc_u32 s41, s9, 0
	s_lshl_b32 s64, s33, 19
	s_add_u32 s64, s64, 0x400
	s_add_u32 s72, s62, s64
	s_addc_u32 s73, s63, 0
	s_nop 3
	s_waitcnt lgkmcnt(4)
	v_mfma_f32_32x32x16_f16 v[96:111], a[0:3], v[160:163], v[96:111]
	ds_read_b128 v[160:163], v192 offset:8192
	v_exp_f32_e32 v200, v64
	v_mfma_f32_32x32x16_f16 v[112:127], a[0:3], v[164:167], v[112:127]
	ds_read_b128 v[164:167], v192 offset:9216
	s_lshl_b32 s64, s33, 3
	s_add_u32 s64, s64, s29
	s_lshl_b32 s64, s64, 7
	s_add_u32 s38, s8, s64
	s_addc_u32 s39, s9, 0
	global_load_dword v251, v196, s[38:39] sc1
	v_exp_f32_e32 v201, v65
	v_add_f32_e32 v200, 1.0, v200
	v_mfma_f32_32x32x16_f16 v[96:111], a[4:7], v[168:171], v[96:111]
	ds_read_b128 v[168:171], v192 offset:10240
	v_exp_f32_e32 v202, v66
	v_add_f32_e32 v201, 1.0, v201
	v_mfma_f32_32x32x16_f16 v[112:127], a[4:7], v[172:175], v[112:127]
	ds_read_b128 v[172:175], v192 offset:11264
	global_load_lds_dwordx4 v192, s[44:45] offset:1024 sc1
	v_exp_f32_e32 v203, v67
	v_add_f32_e32 v202, 1.0, v202
	s_waitcnt lgkmcnt(4)
	v_mfma_f32_32x32x16_f16 v[96:111], a[8:11], v[176:179], v[96:111]
	ds_read_b128 v[176:179], v192 offset:12288
	v_exp_f32_e32 v204, v68
	v_add_f32_e32 v203, 1.0, v203
	v_mfma_f32_32x32x16_f16 v[112:127], a[8:11], v[180:183], v[112:127]
	ds_read_b128 v[180:183], v192 offset:13312
	v_exp_f32_e32 v205, v69
	v_add_f32_e32 v204, 1.0, v204
	v_mfma_f32_32x32x16_f16 v[96:111], a[12:15], v[184:187], v[96:111]
	ds_read_b128 v[184:187], v192 offset:14336
	v_exp_f32_e32 v206, v70
	v_add_f32_e32 v205, 1.0, v205
	v_mfma_f32_32x32x16_f16 v[112:127], a[12:15], v[188:191], v[112:127]
	ds_read_b128 v[188:191], v192 offset:15360
	global_load_lds_dwordx4 v192, s[44:45] offset:2048 sc1
	v_exp_f32_e32 v207, v71
	v_add_f32_e32 v206, 1.0, v206
	s_waitcnt lgkmcnt(4)
	v_mfma_f32_32x32x16_f16 v[96:111], a[16:19], v[160:163], v[96:111]
	ds_read_b128 v[160:163], v192 offset:16384
	v_exp_f32_e32 v208, v72
	v_add_f32_e32 v207, 1.0, v207
	v_mfma_f32_32x32x16_f16 v[112:127], a[16:19], v[164:167], v[112:127]
	ds_read_b128 v[164:167], v192 offset:17408
	v_exp_f32_e32 v209, v73
	v_add_f32_e32 v208, 1.0, v208
	v_mfma_f32_32x32x16_f16 v[96:111], a[20:23], v[168:171], v[96:111]
	ds_read_b128 v[168:171], v192 offset:18432
	v_exp_f32_e32 v210, v74
	v_add_f32_e32 v209, 1.0, v209
	v_mfma_f32_32x32x16_f16 v[112:127], a[20:23], v[172:175], v[112:127]
	ds_read_b128 v[172:175], v192 offset:19456
	global_load_lds_dwordx4 v192, s[44:45] offset:3072 sc1
	v_exp_f32_e32 v211, v75
	v_add_f32_e32 v210, 1.0, v210
	s_waitcnt lgkmcnt(4)
	v_mfma_f32_32x32x16_f16 v[96:111], a[24:27], v[176:179], v[96:111]
	ds_read_b128 v[176:179], v192 offset:20480
	v_exp_f32_e32 v212, v76
	v_add_f32_e32 v211, 1.0, v211
	v_mfma_f32_32x32x16_f16 v[112:127], a[24:27], v[180:183], v[112:127]
	ds_read_b128 v[180:183], v192 offset:21504
	v_exp_f32_e32 v213, v77
	v_add_f32_e32 v212, 1.0, v212
	v_mfma_f32_32x32x16_f16 v[96:111], a[28:31], v[184:187], v[96:111]
	ds_read_b128 v[184:187], v192 offset:22528
	v_exp_f32_e32 v214, v78
	v_add_f32_e32 v213, 1.0, v213
	v_mfma_f32_32x32x16_f16 v[112:127], a[28:31], v[188:191], v[112:127]
	ds_read_b128 v[188:191], v192 offset:23552
	s_add_u32 s44, s34, 0x11000
	s_addc_u32 s45, s35, 0
	s_mov_b32 m0, s57
	s_nop 0
	global_load_lds_dwordx4 v192, s[44:45] sc1
	v_exp_f32_e32 v215, v79
	v_add_f32_e32 v214, 1.0, v214
	s_waitcnt lgkmcnt(4)
	v_mfma_f32_32x32x16_f16 v[96:111], a[32:35], v[160:163], v[96:111]
	ds_read_b128 v[160:163], v192 offset:24576
	v_add_f32_e32 v215, 1.0, v215
	v_rcp_f32_e32 v200, v200
	v_mfma_f32_32x32x16_f16 v[112:127], a[32:35], v[164:167], v[112:127]
	ds_read_b128 v[164:167], v192 offset:25600
	v_rcp_f32_e32 v201, v201
	v_mfma_f32_32x32x16_f16 v[96:111], a[36:39], v[168:171], v[96:111]
	ds_read_b128 v[168:171], v192 offset:26624
	v_rcp_f32_e32 v202, v202
	v_mfma_f32_32x32x16_f16 v[112:127], a[36:39], v[172:175], v[112:127]
	ds_read_b128 v[172:175], v192 offset:27648
	global_load_lds_dwordx4 v192, s[44:45] offset:1024 sc1
	v_rcp_f32_e32 v203, v203
	s_waitcnt lgkmcnt(4)
	v_mfma_f32_32x32x16_f16 v[96:111], a[40:43], v[176:179], v[96:111]
	ds_read_b128 v[176:179], v192 offset:28672
	v_rcp_f32_e32 v204, v204
	v_mfma_f32_32x32x16_f16 v[112:127], a[40:43], v[180:183], v[112:127]
	ds_read_b128 v[180:183], v192 offset:29696
	v_rcp_f32_e32 v205, v205
	v_mul_f32_e32 v204, v204, v144
	v_mfma_f32_32x32x16_f16 v[96:111], a[44:47], v[184:187], v[96:111]
	ds_read_b128 v[184:187], v192 offset:30720
	v_rcp_f32_e32 v206, v206
	v_mul_f32_e32 v205, v205, v145
	v_mfma_f32_32x32x16_f16 v[112:127], a[44:47], v[188:191], v[112:127]
	ds_read_b128 v[188:191], v192 offset:31744
	global_load_lds_dwordx4 v192, s[44:45] offset:2048 sc1
	v_rcp_f32_e32 v207, v207
	v_mul_f32_e32 v206, v206, v146
	s_waitcnt vmcnt(8)
	s_barrier
	s_waitcnt lgkmcnt(4)
	v_mfma_f32_32x32x16_f16 v[96:111], a[48:51], v[160:163], v[96:111]
	ds_read_b128 v[160:163], v192 offset:32768
	v_rcp_f32_e32 v208, v208
	v_mul_f32_e32 v207, v207, v147
	v_mfma_f32_32x32x16_f16 v[112:127], a[48:51], v[164:167], v[112:127]
	ds_read_b128 v[164:167], v192 offset:33792
	v_rcp_f32_e32 v209, v209
	v_fmamk_f32 v208, v208, 0xc0b8aa3b, v198
	v_mfma_f32_32x32x16_f16 v[96:111], a[52:55], v[168:171], v[96:111]
	ds_read_b128 v[168:171], v192 offset:34816
	v_rcp_f32_e32 v210, v210
	v_fmamk_f32 v209, v209, 0xc0b8aa3b, v198
	v_fma_f32 v144, v200, v208, v204
	v_mfma_f32_32x32x16_f16 v[112:127], a[52:55], v[172:175], v[112:127]
	ds_read_b128 v[172:175], v192 offset:35840
	global_load_lds_dwordx4 v192, s[44:45] offset:3072 sc1
	v_rcp_f32_e32 v211, v211
	v_fmamk_f32 v210, v210, 0xc0b8aa3b, v198
	v_fma_f32 v145, v201, v209, v205
	s_waitcnt lgkmcnt(4)
	v_mfma_f32_32x32x16_f16 v[96:111], a[56:59], v[176:179], v[96:111]
	ds_read_b128 v[176:179], v192 offset:36864
	v_rcp_f32_e32 v212, v212
	v_fmamk_f32 v211, v211, 0xc0b8aa3b, v198
	v_fma_f32 v146, v202, v210, v206
	v_mfma_f32_32x32x16_f16 v[112:127], a[56:59], v[180:183], v[112:127]
	ds_read_b128 v[180:183], v192 offset:37888
	v_rcp_f32_e32 v213, v213
	v_fma_f32 v147, v203, v211, v207
	v_mfma_f32_32x32x16_f16 v[96:111], a[60:63], v[184:187], v[96:111]
	ds_read_b128 v[184:187], v192 offset:38912
	v_rcp_f32_e32 v214, v214
	v_mfma_f32_32x32x16_f16 v[112:127], a[60:63], v[188:191], v[112:127]
	ds_read_b128 v[188:191], v192 offset:39936
	s_add_u32 s44, s34, 0x18000
	s_addc_u32 s45, s35, 0
	s_mov_b32 m0, s58
	s_nop 0
	global_load_lds_dwordx4 v192, s[44:45] sc1
	v_rcp_f32_e32 v215, v215
	s_waitcnt lgkmcnt(4)
	v_mfma_f32_32x32x16_f16 v[96:111], a[64:67], v[160:163], v[96:111]
	ds_read_b128 v[160:163], v192 offset:40960
	v_exp_f32_e32 v200, v144
	v_mfma_f32_32x32x16_f16 v[112:127], a[64:67], v[164:167], v[112:127]
	ds_read_b128 v[164:167], v192 offset:41984
	v_exp_f32_e32 v201, v145
	v_add_f32_e32 v200, 1.0, v200
	v_mfma_f32_32x32x16_f16 v[96:111], a[68:71], v[168:171], v[96:111]
	ds_read_b128 v[168:171], v192 offset:43008
	v_exp_f32_e32 v202, v146
	v_add_f32_e32 v201, 1.0, v201
	v_mfma_f32_32x32x16_f16 v[112:127], a[68:71], v[172:175], v[112:127]
	ds_read_b128 v[172:175], v192 offset:44032
	global_load_lds_dwordx4 v192, s[44:45] offset:1024 sc1
	v_exp_f32_e32 v203, v147
	v_add_f32_e32 v202, 1.0, v202
	s_waitcnt lgkmcnt(4)
	v_mfma_f32_32x32x16_f16 v[96:111], a[72:75], v[176:179], v[96:111]
	ds_read_b128 v[176:179], v192 offset:45056
	v_add_f32_e32 v203, 1.0, v203
	v_rcp_f32_e32 v200, v200
	v_mfma_f32_32x32x16_f16 v[112:127], a[72:75], v[180:183], v[112:127]
	ds_read_b128 v[180:183], v192 offset:46080
	v_rcp_f32_e32 v201, v201
	v_fma_f32 v200, v200, 2.0, -1.0
	v_mfma_f32_32x32x16_f16 v[96:111], a[76:79], v[184:187], v[96:111]
	ds_read_b128 v[184:187], v192 offset:47104
	v_rcp_f32_e32 v202, v202
	v_fma_f32 v201, v201, 2.0, -1.0
	v_mul_f32_e32 v216, v212, v200
	v_mfma_f32_32x32x16_f16 v[112:127], a[76:79], v[188:191], v[112:127]
	ds_read_b128 v[188:191], v192 offset:48128
	global_load_lds_dwordx4 v192, s[44:45] offset:2048 sc1
	v_rcp_f32_e32 v203, v203
	v_fma_f32 v202, v202, 2.0, -1.0
	v_mul_f32_e32 v217, v213, v201
	s_waitcnt lgkmcnt(4)
	v_mfma_f32_32x32x16_f16 v[96:111], a[80:83], v[160:163], v[96:111]
	ds_read_b128 v[160:163], v192 offset:49152
	v_fma_f32 v203, v203, 2.0, -1.0
	v_mul_f32_e32 v218, v214, v202
	v_exp_f32_e32 v200, v80
	v_mfma_f32_32x32x16_f16 v[112:127], a[80:83], v[164:167], v[112:127]
	ds_read_b128 v[164:167], v192 offset:50176
	v_mul_f32_e32 v219, v215, v203
	v_mul_f32_e32 v236, v216, v228
	v_exp_f32_e32 v201, v81
	v_mfma_f32_32x32x16_f16 v[96:111], a[84:87], v[168:171], v[96:111]
	ds_read_b128 v[168:171], v192 offset:51200
	v_mul_f32_e32 v237, v216, v232
	v_fmac_f32_e32 v236, v217, v229
	v_exp_f32_e32 v202, v82
	v_mfma_f32_32x32x16_f16 v[112:127], a[84:87], v[172:175], v[112:127]
	ds_read_b128 v[172:175], v192 offset:52224
	global_load_lds_dwordx4 v192, s[44:45] offset:3072 sc1
	v_fmac_f32_e32 v237, v217, v233
	v_fmac_f32_e32 v236, v218, v230
	v_exp_f32_e32 v203, v83
	s_waitcnt lgkmcnt(4)
	v_mfma_f32_32x32x16_f16 v[96:111], a[88:91], v[176:179], v[96:111]
	ds_read_b128 v[176:179], v192 offset:53248
	v_fmac_f32_e32 v237, v218, v234
	v_fmac_f32_e32 v236, v219, v231
	v_exp_f32_e32 v204, v84
	v_mfma_f32_32x32x16_f16 v[112:127], a[88:91], v[180:183], v[112:127]
	ds_read_b128 v[180:183], v192 offset:54272
	v_fmac_f32_e32 v237, v219, v235
	v_mov_b32_e32 v238, v236
	v_exp_f32_e32 v205, v85
	v_mfma_f32_32x32x16_f16 v[96:111], a[92:95], v[184:187], v[96:111]
	ds_read_b128 v[184:187], v192 offset:55296
	v_mov_b32_e32 v239, v236
	v_mov_b32_e32 v240, v237
	v_exp_f32_e32 v206, v86
	v_mfma_f32_32x32x16_f16 v[112:127], a[92:95], v[188:191], v[112:127]
	ds_read_b128 v[188:191], v192 offset:56320
	s_add_u32 s44, s34, 0x19000
	s_addc_u32 s45, s35, 0
	s_mov_b32 m0, s59
	s_nop 0
	global_load_lds_dwordx4 v192, s[44:45] sc1
	v_mov_b32_e32 v241, v237
	v_cvt_pk_f16_f32 v220, v216, v217
	v_exp_f32_e32 v207, v87
	s_waitcnt lgkmcnt(4)
	v_mfma_f32_32x32x16_f16 v[96:111], a[96:99], v[160:163], v[96:111]
	ds_read_b128 v[160:163], v192 offset:57344
	s_nop 1
	v_permlane32_swap_b32_e32 v238, v239
	v_permlane32_swap_b32_e32 v240, v241
	v_add_f32_e32 v238, v238, v239
	v_add_f32_e32 v239, v240, v241
	ds_write_b64 v248, v[238:239] offset:1024
	v_exp_f32_e32 v208, v88
	v_mfma_f32_32x32x16_f16 v[112:127], a[96:99], v[164:167], v[112:127]
	ds_read_b128 v[164:167], v192 offset:58368
	v_cvt_pk_f16_f32 v221, v218, v219
	v_exp_f32_e32 v209, v89
	v_add_f32_e32 v200, 1.0, v200
	v_mfma_f32_32x32x16_f16 v[96:111], a[100:103], v[168:171], v[96:111]
	ds_read_b128 v[168:171], v192 offset:59392
	v_exp_f32_e32 v210, v90
	v_add_f32_e32 v201, 1.0, v201
	v_add_f32_e32 v202, 1.0, v202
	v_mfma_f32_32x32x16_f16 v[112:127], a[100:103], v[172:175], v[112:127]
	ds_read_b128 v[172:175], v192 offset:60416
	global_load_lds_dwordx4 v192, s[44:45] offset:1024 sc1
	v_exp_f32_e32 v211, v91
	v_add_f32_e32 v203, 1.0, v203
	v_add_f32_e32 v204, 1.0, v204
	s_waitcnt lgkmcnt(5)
	v_mfma_f32_32x32x16_f16 v[96:111], a[104:107], v[176:179], v[96:111]
	ds_read_b128 v[176:179], v192 offset:61440
	v_exp_f32_e32 v212, v92
	v_add_f32_e32 v205, 1.0, v205
	v_add_f32_e32 v206, 1.0, v206
	v_mfma_f32_32x32x16_f16 v[112:127], a[104:107], v[180:183], v[112:127]
	ds_read_b128 v[180:183], v192 offset:62464
	v_exp_f32_e32 v213, v93
	v_add_f32_e32 v207, 1.0, v207
	v_add_f32_e32 v208, 1.0, v208
	v_mfma_f32_32x32x16_f16 v[96:111], a[108:111], v[184:187], v[96:111]
	ds_read_b128 v[184:187], v192 offset:63488
	v_exp_f32_e32 v214, v94
	v_add_f32_e32 v209, 1.0, v209
	v_add_f32_e32 v210, 1.0, v210
	v_mfma_f32_32x32x16_f16 v[112:127], a[108:111], v[188:191], v[112:127]
	ds_read_b128 v[188:191], v192 offset:64512
	global_load_lds_dwordx4 v192, s[44:45] offset:2048 sc1
	v_exp_f32_e32 v215, v95
	v_add_f32_e32 v211, 1.0, v211
	v_add_f32_e32 v212, 1.0, v212
	s_waitcnt vmcnt(7)
	s_barrier
	s_waitcnt lgkmcnt(4)
	v_mfma_f32_32x32x16_f16 v[96:111], a[112:115], v[160:163], v[96:111]
	ds_read_b128 v[160:163], v193 offset:0
	v_add_f32_e32 v213, 1.0, v213
	v_add_f32_e32 v214, 1.0, v214
	v_rcp_f32_e32 v200, v200
	v_mfma_f32_32x32x16_f16 v[112:127], a[112:115], v[164:167], v[112:127]
	ds_read_b128 v[164:167], v193 offset:1024
	v_add_f32_e32 v215, 1.0, v215
	v_rcp_f32_e32 v201, v201
	v_mfma_f32_32x32x16_f16 v[96:111], a[116:119], v[168:171], v[96:111]
	ds_read_b128 v[168:171], v193 offset:2048
	v_rcp_f32_e32 v202, v202
	v_mfma_f32_32x32x16_f16 v[112:127], a[116:119], v[172:175], v[112:127]
	ds_read_b128 v[172:175], v193 offset:3072
	global_load_lds_dwordx4 v192, s[44:45] offset:3072 sc1
	v_rcp_f32_e32 v203, v203
	s_waitcnt lgkmcnt(4)
	v_mfma_f32_32x32x16_f16 v[96:111], a[120:123], v[176:179], v[96:111]
	ds_read_b128 v[176:179], v193 offset:4096
	v_rcp_f32_e32 v204, v204
	s_add_u32 s46, s42, 0x2000
	s_addc_u32 s47, s43, 0
	global_load_dwordx4 v[32:35], v192, s[46:47] offset:0
	v_mfma_f32_32x32x16_f16 v[112:127], a[120:123], v[180:183], v[112:127]
	ds_read_b128 v[180:183], v193 offset:5120
	v_rcp_f32_e32 v205, v205
	v_mul_f32_e32 v204, v204, v148
	global_load_dwordx4 v[36:39], v192, s[46:47] offset:1024
	global_load_dwordx4 v[40:43], v192, s[46:47] offset:2048
	v_mfma_f32_32x32x16_f16 v[96:111], a[124:127], v[184:187], v[96:111]
	ds_read_b128 v[184:187], v193 offset:6144
	v_rcp_f32_e32 v206, v206
	v_mul_f32_e32 v205, v205, v149
	global_load_dwordx4 v[44:47], v192, s[46:47] offset:3072
	s_add_u32 s46, s42, 0x3000
	s_addc_u32 s47, s43, 0
	v_mfma_f32_32x32x16_f16 v[112:127], a[124:127], v[188:191], v[112:127]
	ds_read_b128 v[188:191], v193 offset:7168
	v_cmp_gt_u32_e32 vcc, 1, v251
	s_cbranch_vccz .LD_tok38
